# GEMM K-loops: half of the per-stage 64-bit VALU address adds replaced by scalar-base LDS-DMA loads (112 sites incl. peeled copies); stacked
# speedup vs baseline: 1.0073x; 1.0026x over previous
.LBB0_84:
	s_ashr_i32 s15, s14, 31
	v_cmp_lt_i64_e32 vcc, s[16:17], v[142:143]
	s_lshl_b64 s[16:17], s[14:15], 20
	s_add_u32 s16, s36, s16
	s_addc_u32 s17, s37, s17
	s_and_b64 s[22:23], vcc, exec
	s_cselect_b32 s15, s17, s25
	s_cselect_b32 s55, s16, s24
	s_ashr_i32 s13, s12, 31
	s_lshl_b64 s[22:23], s[12:13], 20
	s_add_u32 s22, s6, s22
	s_addc_u32 s23, s7, s23
	s_and_b64 s[56:57], vcc, exec
	s_cselect_b32 s13, s23, s85
	s_cselect_b32 s56, s22, s84
	s_add_u32 s24, s24, 0x80080
	s_addc_u32 s25, s25, 0
	s_add_u32 s57, s84, 0x100
	v_mov_b32_e32 v2, 0
	s_addc_u32 s58, s85, 0
	s_mov_b32 s59, -2
	ds_read_b128 v[154:157], v150
	ds_read_b128 v[158:161], v150 offset:1024
	ds_read_b128 v[162:165], v150 offset:2048
	ds_read_b128 v[166:169], v150 offset:3072
	s_add_u32 s60, s24, 0xfff80080
	s_addc_u32 s61, s25, -1
	s_cmp_eq_u32 s59, 28
	s_cselect_b32 s87, s15, s61
	s_cselect_b32 s86, s55, s60
	s_cselect_b32 s85, s13, s58
	s_cselect_b32 s84, s56, s57
	s_add_i32 m0, s11, 0xc000
	ds_read_b128 v[170:173], v151
	ds_read_b128 v[174:177], v151 offset:1024
	ds_read_b128 v[178:181], v151 offset:2048
	ds_read_b128 v[182:185], v151 offset:3072
	ds_read_b128 v[186:189], v151 offset:4096
	ds_read_b128 v[190:193], v151 offset:5120
	ds_read_b128 v[194:197], v151 offset:6144
	ds_read_b128 v[198:201], v151 offset:7168
	global_load_lds_dwordx4 v138, s[24:25]
	s_add_i32 m0, s11, 0xe000
	s_nop 0
	global_load_lds_dwordx4 v140, s[24:25]
	s_waitcnt lgkmcnt(8)
	s_barrier
	s_waitcnt lgkmcnt(0)
	s_setprio 1
	s_waitcnt lgkmcnt(0)
	v_mfma_f32_16x16x32_bf16 v[126:129], v[154:157], v[170:173], 0
	v_mfma_f32_16x16x32_bf16 v[122:125], v[162:165], v[170:173], 0
	v_mfma_f32_16x16x32_bf16 v[118:121], v[154:157], v[178:181], 0
	v_mfma_f32_16x16x32_bf16 v[114:117], v[162:165], v[178:181], 0
	v_mfma_f32_16x16x32_bf16 v[102:105], v[154:157], v[186:189], 0
	v_mfma_f32_16x16x32_bf16 v[98:101], v[162:165], v[186:189], 0
	v_mfma_f32_16x16x32_bf16 v[86:89], v[154:157], v[194:197], 0
	v_mfma_f32_16x16x32_bf16 v[82:85], v[162:165], v[194:197], 0
	v_mfma_f32_16x16x32_bf16 v[126:129], v[158:161], v[174:177], v[126:129]
	v_mfma_f32_16x16x32_bf16 v[122:125], v[166:169], v[174:177], v[122:125]
	v_mfma_f32_16x16x32_bf16 v[118:121], v[158:161], v[182:185], v[118:121]
	v_mfma_f32_16x16x32_bf16 v[114:117], v[166:169], v[182:185], v[114:117]
	v_mfma_f32_16x16x32_bf16 v[102:105], v[158:161], v[190:193], v[102:105]
	v_mfma_f32_16x16x32_bf16 v[98:101], v[166:169], v[190:193], v[98:101]
	v_mfma_f32_16x16x32_bf16 v[86:89], v[158:161], v[198:201], v[86:89]
	v_mfma_f32_16x16x32_bf16 v[82:85], v[166:169], v[198:201], v[82:85]
	s_setprio 0
	s_barrier
	s_add_i32 s60, s41, s18
	v_lshl_add_u64 v[218:219], s[84:85], 0, v[134:135]
	s_mov_b32 m0, s60
	ds_read_b128 v[202:205], v152
	ds_read_b128 v[206:209], v152 offset:1024
	ds_read_b128 v[210:213], v152 offset:2048
	ds_read_b128 v[214:217], v152 offset:3072
	global_load_lds_dwordx4 v[218:219], off
	v_lshl_add_u64 v[220:221], s[84:85], 0, v[130:131]
	s_add_i32 m0, s60, 0x2000
	s_nop 0
	global_load_lds_dwordx4 v[220:221], off
	s_barrier
	s_waitcnt lgkmcnt(0)
	s_setprio 1
	s_waitcnt lgkmcnt(0)
	v_mfma_f32_16x16x32_bf16 v[110:113], v[202:205], v[170:173], 0
	v_mfma_f32_16x16x32_bf16 v[106:109], v[210:213], v[170:173], 0
	v_mfma_f32_16x16x32_bf16 v[94:97], v[202:205], v[178:181], 0
	v_mfma_f32_16x16x32_bf16 v[90:93], v[210:213], v[178:181], 0
	v_mfma_f32_16x16x32_bf16 v[78:81], v[202:205], v[186:189], 0
	v_mfma_f32_16x16x32_bf16 v[74:77], v[210:213], v[186:189], 0
	v_mfma_f32_16x16x32_bf16 v[70:73], v[202:205], v[194:197], 0
	v_mfma_f32_16x16x32_bf16 v[66:69], v[210:213], v[194:197], 0
	v_mfma_f32_16x16x32_bf16 v[110:113], v[206:209], v[174:177], v[110:113]
	v_mfma_f32_16x16x32_bf16 v[106:109], v[214:217], v[174:177], v[106:109]
	v_mfma_f32_16x16x32_bf16 v[94:97], v[206:209], v[182:185], v[94:97]
	v_mfma_f32_16x16x32_bf16 v[90:93], v[214:217], v[182:185], v[90:93]
	v_mfma_f32_16x16x32_bf16 v[78:81], v[206:209], v[190:193], v[78:81]
	v_mfma_f32_16x16x32_bf16 v[74:77], v[214:217], v[190:193], v[74:77]
	v_mfma_f32_16x16x32_bf16 v[70:73], v[206:209], v[198:201], v[70:73]
	v_mfma_f32_16x16x32_bf16 v[66:69], v[214:217], v[198:201], v[66:69]
	s_setprio 0
	s_mov_b32 m0, s11
	v_lshl_add_u64 v[222:223], s[86:87], 0, v[136:137]
	s_barrier
	ds_read_b128 v[170:173], v151 offset:16384
	ds_read_b128 v[174:177], v151 offset:17408
	ds_read_b128 v[178:181], v151 offset:18432
	ds_read_b128 v[182:185], v151 offset:19456
	ds_read_b128 v[186:189], v151 offset:20480
	ds_read_b128 v[190:193], v151 offset:21504
	ds_read_b128 v[194:197], v151 offset:22528
	ds_read_b128 v[198:201], v151 offset:23552
	global_load_lds_dwordx4 v[222:223], off
	v_lshl_add_u64 v[224:225], s[86:87], 0, v[132:133]
	s_mov_b32 m0, s21
	s_nop 0
	global_load_lds_dwordx4 v[224:225], off
	s_barrier
	s_waitcnt lgkmcnt(0)
	s_setprio 1
	s_waitcnt lgkmcnt(0)
	v_mfma_f32_16x16x32_bf16 v[62:65], v[154:157], v[170:173], 0
	v_mfma_f32_16x16x32_bf16 v[58:61], v[162:165], v[170:173], 0
	v_mfma_f32_16x16x32_bf16 v[54:57], v[154:157], v[178:181], 0
	v_mfma_f32_16x16x32_bf16 v[50:53], v[162:165], v[178:181], 0
	v_mfma_f32_16x16x32_bf16 v[38:41], v[154:157], v[186:189], 0
	v_mfma_f32_16x16x32_bf16 v[34:37], v[162:165], v[186:189], 0
	v_mfma_f32_16x16x32_bf16 v[22:25], v[154:157], v[194:197], 0
	v_mfma_f32_16x16x32_bf16 v[18:21], v[162:165], v[194:197], 0
	v_mfma_f32_16x16x32_bf16 v[62:65], v[158:161], v[174:177], v[62:65]
	v_mfma_f32_16x16x32_bf16 v[58:61], v[166:169], v[174:177], v[58:61]
	v_mfma_f32_16x16x32_bf16 v[54:57], v[158:161], v[182:185], v[54:57]
	v_mfma_f32_16x16x32_bf16 v[50:53], v[166:169], v[182:185], v[50:53]
	v_mfma_f32_16x16x32_bf16 v[38:41], v[158:161], v[190:193], v[38:41]
	v_mfma_f32_16x16x32_bf16 v[34:37], v[166:169], v[190:193], v[34:37]
	v_mfma_f32_16x16x32_bf16 v[22:25], v[158:161], v[198:201], v[22:25]
	v_mfma_f32_16x16x32_bf16 v[18:21], v[166:169], v[198:201], v[18:21]
	s_setprio 0
	s_barrier
	s_add_u32 s60, s84, 0x80000
	s_addc_u32 s61, s85, 0
	s_add_i32 s62, s52, s18
	s_mov_b32 m0, s62
	s_nop 0
	global_load_lds_dwordx4 v134, s[60:61]
	s_add_i32 m0, s62, 0x2000
	s_nop 0
	global_load_lds_dwordx4 v130, s[60:61]
	s_waitcnt vmcnt(6)
	s_barrier
	s_setprio 1
	v_mfma_f32_16x16x32_bf16 v[46:49], v[202:205], v[170:173], 0
	v_mfma_f32_16x16x32_bf16 v[42:45], v[210:213], v[170:173], 0
	v_mfma_f32_16x16x32_bf16 v[30:33], v[202:205], v[178:181], 0
	v_mfma_f32_16x16x32_bf16 v[26:29], v[210:213], v[178:181], 0
	v_mfma_f32_16x16x32_bf16 v[14:17], v[202:205], v[186:189], 0
	v_mfma_f32_16x16x32_bf16 v[10:13], v[210:213], v[186:189], 0
	v_mfma_f32_16x16x32_bf16 v[6:9], v[202:205], v[194:197], 0
	v_mfma_f32_16x16x32_bf16 v[2:5], v[210:213], v[194:197], 0
	v_mfma_f32_16x16x32_bf16 v[46:49], v[206:209], v[174:177], v[46:49]
	v_mfma_f32_16x16x32_bf16 v[42:45], v[214:217], v[174:177], v[42:45]
	v_mfma_f32_16x16x32_bf16 v[30:33], v[206:209], v[182:185], v[30:33]
	v_mfma_f32_16x16x32_bf16 v[26:29], v[214:217], v[182:185], v[26:29]
	v_mfma_f32_16x16x32_bf16 v[14:17], v[206:209], v[190:193], v[14:17]
	v_mfma_f32_16x16x32_bf16 v[10:13], v[214:217], v[190:193], v[10:13]
	v_mfma_f32_16x16x32_bf16 v[6:9], v[206:209], v[198:201], v[6:9]
	v_mfma_f32_16x16x32_bf16 v[2:5], v[214:217], v[198:201], v[2:5]
	s_setprio 0
	s_add_i32 s62, 0, 0x18000
	v_add_u32_e32 v1, s62, v148
	s_barrier
	ds_read_b128 v[154:157], v1
	ds_read_b128 v[158:161], v1 offset:1024
	ds_read_b128 v[162:165], v1 offset:2048
	ds_read_b128 v[166:169], v1 offset:3072
	s_add_u32 s60, s86, 0x80000
	s_addc_u32 s61, s87, 0
	s_mov_b32 m0, s26
	ds_read_b128 v[170:173], v151 offset:32768
	ds_read_b128 v[174:177], v151 offset:33792
	ds_read_b128 v[178:181], v151 offset:34816
	ds_read_b128 v[182:185], v151 offset:35840
	ds_read_b128 v[186:189], v151 offset:36864
	ds_read_b128 v[190:193], v151 offset:37888
	ds_read_b128 v[194:197], v151 offset:38912
	ds_read_b128 v[198:201], v151 offset:39936
	global_load_lds_dwordx4 v136, s[60:61]
	s_mov_b32 m0, s27
	s_nop 0
	global_load_lds_dwordx4 v132, s[60:61]
	s_waitcnt lgkmcnt(8)
	s_barrier
	s_waitcnt lgkmcnt(0)
	s_setprio 1
	s_waitcnt lgkmcnt(0)
	v_mfma_f32_16x16x32_bf16 v[126:129], v[154:157], v[170:173], v[126:129]
	v_mfma_f32_16x16x32_bf16 v[122:125], v[162:165], v[170:173], v[122:125]
	v_mfma_f32_16x16x32_bf16 v[118:121], v[154:157], v[178:181], v[118:121]
	v_mfma_f32_16x16x32_bf16 v[114:117], v[162:165], v[178:181], v[114:117]
	v_mfma_f32_16x16x32_bf16 v[102:105], v[154:157], v[186:189], v[102:105]
	v_mfma_f32_16x16x32_bf16 v[98:101], v[162:165], v[186:189], v[98:101]
	v_mfma_f32_16x16x32_bf16 v[86:89], v[154:157], v[194:197], v[86:89]
	v_mfma_f32_16x16x32_bf16 v[82:85], v[162:165], v[194:197], v[82:85]
	v_mfma_f32_16x16x32_bf16 v[126:129], v[158:161], v[174:177], v[126:129]
	v_mfma_f32_16x16x32_bf16 v[122:125], v[166:169], v[174:177], v[122:125]
	v_mfma_f32_16x16x32_bf16 v[118:121], v[158:161], v[182:185], v[118:121]
	v_mfma_f32_16x16x32_bf16 v[114:117], v[166:169], v[182:185], v[114:117]
	v_mfma_f32_16x16x32_bf16 v[102:105], v[158:161], v[190:193], v[102:105]
	v_mfma_f32_16x16x32_bf16 v[98:101], v[166:169], v[190:193], v[98:101]
	v_mfma_f32_16x16x32_bf16 v[86:89], v[158:161], v[198:201], v[86:89]
	v_mfma_f32_16x16x32_bf16 v[82:85], v[166:169], v[198:201], v[82:85]
	s_setprio 0
	s_barrier
	s_add_i32 s63, 0, 0x1c000
	s_add_i32 s60, s62, s18
	v_add_u32_e32 v1, s63, v148
	v_lshl_add_u64 v[218:219], v[218:219], 0, s[8:9]
	s_mov_b32 m0, s60
	ds_read_b128 v[202:205], v1
	ds_read_b128 v[206:209], v1 offset:1024
	ds_read_b128 v[210:213], v1 offset:2048
	ds_read_b128 v[214:217], v1 offset:3072
	global_load_lds_dwordx4 v[218:219], off
	v_lshl_add_u64 v[218:219], v[220:221], 0, s[8:9]
	s_add_i32 m0, s60, 0x2000
	s_nop 0
	global_load_lds_dwordx4 v[218:219], off
	s_barrier
	s_waitcnt lgkmcnt(0)
	s_setprio 1
	s_waitcnt lgkmcnt(0)
	v_mfma_f32_16x16x32_bf16 v[110:113], v[202:205], v[170:173], v[110:113]
	v_mfma_f32_16x16x32_bf16 v[106:109], v[210:213], v[170:173], v[106:109]
	v_mfma_f32_16x16x32_bf16 v[94:97], v[202:205], v[178:181], v[94:97]
	v_mfma_f32_16x16x32_bf16 v[90:93], v[210:213], v[178:181], v[90:93]
	v_mfma_f32_16x16x32_bf16 v[78:81], v[202:205], v[186:189], v[78:81]
	v_mfma_f32_16x16x32_bf16 v[74:77], v[210:213], v[186:189], v[74:77]
	v_mfma_f32_16x16x32_bf16 v[70:73], v[202:205], v[194:197], v[70:73]
	v_mfma_f32_16x16x32_bf16 v[66:69], v[210:213], v[194:197], v[66:69]
	v_mfma_f32_16x16x32_bf16 v[110:113], v[206:209], v[174:177], v[110:113]
	v_mfma_f32_16x16x32_bf16 v[106:109], v[214:217], v[174:177], v[106:109]
	v_mfma_f32_16x16x32_bf16 v[94:97], v[206:209], v[182:185], v[94:97]
	v_mfma_f32_16x16x32_bf16 v[90:93], v[214:217], v[182:185], v[90:93]
	v_mfma_f32_16x16x32_bf16 v[78:81], v[206:209], v[190:193], v[78:81]
	v_mfma_f32_16x16x32_bf16 v[74:77], v[214:217], v[190:193], v[74:77]
	v_mfma_f32_16x16x32_bf16 v[70:73], v[206:209], v[198:201], v[70:73]
	v_mfma_f32_16x16x32_bf16 v[66:69], v[214:217], v[198:201], v[66:69]
	s_setprio 0
	s_mov_b32 m0, s34
	v_lshl_add_u64 v[218:219], v[222:223], 0, s[8:9]
	s_barrier
	ds_read_b128 v[170:173], v151 offset:49152
	ds_read_b128 v[174:177], v151 offset:50176
	ds_read_b128 v[178:181], v151 offset:51200
	ds_read_b128 v[182:185], v151 offset:52224
	ds_read_b128 v[186:189], v151 offset:53248
	ds_read_b128 v[190:193], v151 offset:54272
	ds_read_b128 v[194:197], v151 offset:55296
	ds_read_b128 v[198:201], v151 offset:56320
	global_load_lds_dwordx4 v[218:219], off
	v_lshl_add_u64 v[218:219], v[224:225], 0, s[8:9]
	s_mov_b32 m0, s35
	s_nop 0
	global_load_lds_dwordx4 v[218:219], off
	s_barrier
	s_waitcnt lgkmcnt(0)
	s_setprio 1
	s_waitcnt lgkmcnt(0)
	v_mfma_f32_16x16x32_bf16 v[62:65], v[154:157], v[170:173], v[62:65]
	v_mfma_f32_16x16x32_bf16 v[58:61], v[162:165], v[170:173], v[58:61]
	v_mfma_f32_16x16x32_bf16 v[54:57], v[154:157], v[178:181], v[54:57]
	v_mfma_f32_16x16x32_bf16 v[50:53], v[162:165], v[178:181], v[50:53]
	v_mfma_f32_16x16x32_bf16 v[38:41], v[154:157], v[186:189], v[38:41]
	v_mfma_f32_16x16x32_bf16 v[34:37], v[162:165], v[186:189], v[34:37]
	v_mfma_f32_16x16x32_bf16 v[22:25], v[154:157], v[194:197], v[22:25]
	v_mfma_f32_16x16x32_bf16 v[18:21], v[162:165], v[194:197], v[18:21]
	v_mfma_f32_16x16x32_bf16 v[62:65], v[158:161], v[174:177], v[62:65]
	v_mfma_f32_16x16x32_bf16 v[58:61], v[166:169], v[174:177], v[58:61]
	v_mfma_f32_16x16x32_bf16 v[54:57], v[158:161], v[182:185], v[54:57]
	v_mfma_f32_16x16x32_bf16 v[50:53], v[166:169], v[182:185], v[50:53]
	v_mfma_f32_16x16x32_bf16 v[38:41], v[158:161], v[190:193], v[38:41]
	v_mfma_f32_16x16x32_bf16 v[34:37], v[166:169], v[190:193], v[34:37]
	v_mfma_f32_16x16x32_bf16 v[22:25], v[158:161], v[198:201], v[22:25]
	v_mfma_f32_16x16x32_bf16 v[18:21], v[166:169], v[198:201], v[18:21]
	s_setprio 0
	s_barrier
	s_add_u32 s60, s84, 0x80080
	s_addc_u32 s61, s85, 0
	s_add_i32 s62, s63, s18
	s_mov_b32 m0, s62
	s_nop 0
	global_load_lds_dwordx4 v134, s[60:61]
	s_add_i32 m0, s62, 0x2000
	s_nop 0
	global_load_lds_dwordx4 v130, s[60:61]
	s_waitcnt vmcnt(6)
	s_barrier
	s_setprio 1
	v_mfma_f32_16x16x32_bf16 v[46:49], v[202:205], v[170:173], v[46:49]
	v_mfma_f32_16x16x32_bf16 v[42:45], v[210:213], v[170:173], v[42:45]
	v_mfma_f32_16x16x32_bf16 v[30:33], v[202:205], v[178:181], v[30:33]
	v_mfma_f32_16x16x32_bf16 v[26:29], v[210:213], v[178:181], v[26:29]
	v_mfma_f32_16x16x32_bf16 v[14:17], v[202:205], v[186:189], v[14:17]
	v_mfma_f32_16x16x32_bf16 v[10:13], v[210:213], v[186:189], v[10:13]
	v_mfma_f32_16x16x32_bf16 v[6:9], v[202:205], v[194:197], v[6:9]
	v_mfma_f32_16x16x32_bf16 v[2:5], v[210:213], v[194:197], v[2:5]
	v_mfma_f32_16x16x32_bf16 v[46:49], v[206:209], v[174:177], v[46:49]
	v_mfma_f32_16x16x32_bf16 v[42:45], v[214:217], v[174:177], v[42:45]
	v_mfma_f32_16x16x32_bf16 v[30:33], v[206:209], v[182:185], v[30:33]
	v_mfma_f32_16x16x32_bf16 v[26:29], v[214:217], v[182:185], v[26:29]
	v_mfma_f32_16x16x32_bf16 v[14:17], v[206:209], v[190:193], v[14:17]
	v_mfma_f32_16x16x32_bf16 v[10:13], v[214:217], v[190:193], v[10:13]
	v_mfma_f32_16x16x32_bf16 v[6:9], v[206:209], v[198:201], v[6:9]
	v_mfma_f32_16x16x32_bf16 v[2:5], v[214:217], v[198:201], v[2:5]
	s_setprio 0
	s_add_i32 s59, s59, 2
	s_add_u32 s24, s24, 0x100
	s_addc_u32 s25, s25, 0
	s_add_u32 s57, s57, 0x100
	s_addc_u32 s58, s58, 0
	s_cmp_gt_u32 s59, 29
	s_barrier
	s_cbranch_scc1 .Lpeel_85_after
.LBB0_85:
	ds_read_b128 v[154:157], v150
	ds_read_b128 v[158:161], v150 offset:1024
	ds_read_b128 v[162:165], v150 offset:2048
	ds_read_b128 v[166:169], v150 offset:3072
	s_add_u32 s60, s24, 0xfff80080
	s_addc_u32 s61, s25, -1
	s_cmp_eq_u32 s59, 28
	s_cselect_b32 s87, s15, s61
	s_cselect_b32 s86, s55, s60
	s_cselect_b32 s85, s13, s58
	s_cselect_b32 s84, s56, s57
	s_add_i32 m0, s11, 0xc000
	ds_read_b128 v[170:173], v151
	ds_read_b128 v[174:177], v151 offset:1024
	ds_read_b128 v[178:181], v151 offset:2048
	ds_read_b128 v[182:185], v151 offset:3072
	ds_read_b128 v[186:189], v151 offset:4096
	ds_read_b128 v[190:193], v151 offset:5120
	ds_read_b128 v[194:197], v151 offset:6144
	ds_read_b128 v[198:201], v151 offset:7168
	global_load_lds_dwordx4 v138, s[24:25]
	s_add_i32 m0, s11, 0xe000
	s_nop 0
	global_load_lds_dwordx4 v140, s[24:25]
	s_waitcnt lgkmcnt(8)
	s_barrier
	s_waitcnt lgkmcnt(0)
	s_setprio 1
	s_waitcnt lgkmcnt(0)
	v_mfma_f32_16x16x32_bf16 v[126:129], v[154:157], v[170:173], v[126:129]
	v_mfma_f32_16x16x32_bf16 v[122:125], v[162:165], v[170:173], v[122:125]
	v_mfma_f32_16x16x32_bf16 v[118:121], v[154:157], v[178:181], v[118:121]
	v_mfma_f32_16x16x32_bf16 v[114:117], v[162:165], v[178:181], v[114:117]
	v_mfma_f32_16x16x32_bf16 v[102:105], v[154:157], v[186:189], v[102:105]
	v_mfma_f32_16x16x32_bf16 v[98:101], v[162:165], v[186:189], v[98:101]
	v_mfma_f32_16x16x32_bf16 v[86:89], v[154:157], v[194:197], v[86:89]
	v_mfma_f32_16x16x32_bf16 v[82:85], v[162:165], v[194:197], v[82:85]
	v_mfma_f32_16x16x32_bf16 v[126:129], v[158:161], v[174:177], v[126:129]
	v_mfma_f32_16x16x32_bf16 v[122:125], v[166:169], v[174:177], v[122:125]
	v_mfma_f32_16x16x32_bf16 v[118:121], v[158:161], v[182:185], v[118:121]
	v_mfma_f32_16x16x32_bf16 v[114:117], v[166:169], v[182:185], v[114:117]
	v_mfma_f32_16x16x32_bf16 v[102:105], v[158:161], v[190:193], v[102:105]
	v_mfma_f32_16x16x32_bf16 v[98:101], v[166:169], v[190:193], v[98:101]
	v_mfma_f32_16x16x32_bf16 v[86:89], v[158:161], v[198:201], v[86:89]
	v_mfma_f32_16x16x32_bf16 v[82:85], v[166:169], v[198:201], v[82:85]
	s_setprio 0
	s_barrier
	s_add_i32 s60, s41, s18
	v_lshl_add_u64 v[218:219], s[84:85], 0, v[134:135]
	s_mov_b32 m0, s60
	ds_read_b128 v[202:205], v152
	ds_read_b128 v[206:209], v152 offset:1024
	ds_read_b128 v[210:213], v152 offset:2048
	ds_read_b128 v[214:217], v152 offset:3072
	global_load_lds_dwordx4 v[218:219], off
	v_lshl_add_u64 v[220:221], s[84:85], 0, v[130:131]
	s_add_i32 m0, s60, 0x2000
	s_nop 0
	global_load_lds_dwordx4 v[220:221], off
	s_barrier
	s_waitcnt lgkmcnt(0)
	s_setprio 1
	s_waitcnt lgkmcnt(0)
	v_mfma_f32_16x16x32_bf16 v[110:113], v[202:205], v[170:173], v[110:113]
	v_mfma_f32_16x16x32_bf16 v[106:109], v[210:213], v[170:173], v[106:109]
	v_mfma_f32_16x16x32_bf16 v[94:97], v[202:205], v[178:181], v[94:97]
	v_mfma_f32_16x16x32_bf16 v[90:93], v[210:213], v[178:181], v[90:93]
	v_mfma_f32_16x16x32_bf16 v[78:81], v[202:205], v[186:189], v[78:81]
	v_mfma_f32_16x16x32_bf16 v[74:77], v[210:213], v[186:189], v[74:77]
	v_mfma_f32_16x16x32_bf16 v[70:73], v[202:205], v[194:197], v[70:73]
	v_mfma_f32_16x16x32_bf16 v[66:69], v[210:213], v[194:197], v[66:69]
	v_mfma_f32_16x16x32_bf16 v[110:113], v[206:209], v[174:177], v[110:113]
	v_mfma_f32_16x16x32_bf16 v[106:109], v[214:217], v[174:177], v[106:109]
	v_mfma_f32_16x16x32_bf16 v[94:97], v[206:209], v[182:185], v[94:97]
	v_mfma_f32_16x16x32_bf16 v[90:93], v[214:217], v[182:185], v[90:93]
	v_mfma_f32_16x16x32_bf16 v[78:81], v[206:209], v[190:193], v[78:81]
	v_mfma_f32_16x16x32_bf16 v[74:77], v[214:217], v[190:193], v[74:77]
	v_mfma_f32_16x16x32_bf16 v[70:73], v[206:209], v[198:201], v[70:73]
	v_mfma_f32_16x16x32_bf16 v[66:69], v[214:217], v[198:201], v[66:69]
	s_setprio 0
	s_mov_b32 m0, s11
	v_lshl_add_u64 v[222:223], s[86:87], 0, v[136:137]
	s_barrier
	ds_read_b128 v[170:173], v151 offset:16384
	ds_read_b128 v[174:177], v151 offset:17408
	ds_read_b128 v[178:181], v151 offset:18432
	ds_read_b128 v[182:185], v151 offset:19456
	ds_read_b128 v[186:189], v151 offset:20480
	ds_read_b128 v[190:193], v151 offset:21504
	ds_read_b128 v[194:197], v151 offset:22528
	ds_read_b128 v[198:201], v151 offset:23552
	global_load_lds_dwordx4 v[222:223], off
	v_lshl_add_u64 v[224:225], s[86:87], 0, v[132:133]
	s_mov_b32 m0, s21
	s_nop 0
	global_load_lds_dwordx4 v[224:225], off
	s_barrier
	s_waitcnt lgkmcnt(0)
	s_setprio 1
	s_waitcnt lgkmcnt(0)
	v_mfma_f32_16x16x32_bf16 v[62:65], v[154:157], v[170:173], v[62:65]
	v_mfma_f32_16x16x32_bf16 v[58:61], v[162:165], v[170:173], v[58:61]
	v_mfma_f32_16x16x32_bf16 v[54:57], v[154:157], v[178:181], v[54:57]
	v_mfma_f32_16x16x32_bf16 v[50:53], v[162:165], v[178:181], v[50:53]
	v_mfma_f32_16x16x32_bf16 v[38:41], v[154:157], v[186:189], v[38:41]
	v_mfma_f32_16x16x32_bf16 v[34:37], v[162:165], v[186:189], v[34:37]
	v_mfma_f32_16x16x32_bf16 v[22:25], v[154:157], v[194:197], v[22:25]
	v_mfma_f32_16x16x32_bf16 v[18:21], v[162:165], v[194:197], v[18:21]
	v_mfma_f32_16x16x32_bf16 v[62:65], v[158:161], v[174:177], v[62:65]
	v_mfma_f32_16x16x32_bf16 v[58:61], v[166:169], v[174:177], v[58:61]
	v_mfma_f32_16x16x32_bf16 v[54:57], v[158:161], v[182:185], v[54:57]
	v_mfma_f32_16x16x32_bf16 v[50:53], v[166:169], v[182:185], v[50:53]
	v_mfma_f32_16x16x32_bf16 v[38:41], v[158:161], v[190:193], v[38:41]
	v_mfma_f32_16x16x32_bf16 v[34:37], v[166:169], v[190:193], v[34:37]
	v_mfma_f32_16x16x32_bf16 v[22:25], v[158:161], v[198:201], v[22:25]
	v_mfma_f32_16x16x32_bf16 v[18:21], v[166:169], v[198:201], v[18:21]
	s_setprio 0
	s_barrier
	s_add_u32 s60, s84, 0x80000
	s_addc_u32 s61, s85, 0
	s_add_i32 s62, s52, s18
	s_mov_b32 m0, s62
	s_nop 0
	global_load_lds_dwordx4 v134, s[60:61]
	s_add_i32 m0, s62, 0x2000
	s_nop 0
	global_load_lds_dwordx4 v130, s[60:61]
	s_waitcnt vmcnt(6)
	s_barrier
	s_setprio 1
	v_mfma_f32_16x16x32_bf16 v[46:49], v[202:205], v[170:173], v[46:49]
	v_mfma_f32_16x16x32_bf16 v[42:45], v[210:213], v[170:173], v[42:45]
	v_mfma_f32_16x16x32_bf16 v[30:33], v[202:205], v[178:181], v[30:33]
	v_mfma_f32_16x16x32_bf16 v[26:29], v[210:213], v[178:181], v[26:29]
	v_mfma_f32_16x16x32_bf16 v[14:17], v[202:205], v[186:189], v[14:17]
	v_mfma_f32_16x16x32_bf16 v[10:13], v[210:213], v[186:189], v[10:13]
	v_mfma_f32_16x16x32_bf16 v[6:9], v[202:205], v[194:197], v[6:9]
	v_mfma_f32_16x16x32_bf16 v[2:5], v[210:213], v[194:197], v[2:5]
	v_mfma_f32_16x16x32_bf16 v[46:49], v[206:209], v[174:177], v[46:49]
	v_mfma_f32_16x16x32_bf16 v[42:45], v[214:217], v[174:177], v[42:45]
	v_mfma_f32_16x16x32_bf16 v[30:33], v[206:209], v[182:185], v[30:33]
	v_mfma_f32_16x16x32_bf16 v[26:29], v[214:217], v[182:185], v[26:29]
	v_mfma_f32_16x16x32_bf16 v[14:17], v[206:209], v[190:193], v[14:17]
	v_mfma_f32_16x16x32_bf16 v[10:13], v[214:217], v[190:193], v[10:13]
	v_mfma_f32_16x16x32_bf16 v[6:9], v[206:209], v[198:201], v[6:9]
	v_mfma_f32_16x16x32_bf16 v[2:5], v[214:217], v[198:201], v[2:5]
	s_setprio 0
	s_add_i32 s62, 0, 0x18000
	v_add_u32_e32 v1, s62, v148
	s_barrier
	ds_read_b128 v[154:157], v1
	ds_read_b128 v[158:161], v1 offset:1024
	ds_read_b128 v[162:165], v1 offset:2048
	ds_read_b128 v[166:169], v1 offset:3072
	s_add_u32 s60, s86, 0x80000
	s_addc_u32 s61, s87, 0
	s_mov_b32 m0, s26
	ds_read_b128 v[170:173], v151 offset:32768
	ds_read_b128 v[174:177], v151 offset:33792
	ds_read_b128 v[178:181], v151 offset:34816
	ds_read_b128 v[182:185], v151 offset:35840
	ds_read_b128 v[186:189], v151 offset:36864
	ds_read_b128 v[190:193], v151 offset:37888
	ds_read_b128 v[194:197], v151 offset:38912
	ds_read_b128 v[198:201], v151 offset:39936
	global_load_lds_dwordx4 v136, s[60:61]
	s_mov_b32 m0, s27
	s_nop 0
	global_load_lds_dwordx4 v132, s[60:61]
	s_waitcnt lgkmcnt(8)
	s_barrier
	s_waitcnt lgkmcnt(0)
	s_setprio 1
	s_waitcnt lgkmcnt(0)
	v_mfma_f32_16x16x32_bf16 v[126:129], v[154:157], v[170:173], v[126:129]
	v_mfma_f32_16x16x32_bf16 v[122:125], v[162:165], v[170:173], v[122:125]
	v_mfma_f32_16x16x32_bf16 v[118:121], v[154:157], v[178:181], v[118:121]
	v_mfma_f32_16x16x32_bf16 v[114:117], v[162:165], v[178:181], v[114:117]
	v_mfma_f32_16x16x32_bf16 v[102:105], v[154:157], v[186:189], v[102:105]
	v_mfma_f32_16x16x32_bf16 v[98:101], v[162:165], v[186:189], v[98:101]
	v_mfma_f32_16x16x32_bf16 v[86:89], v[154:157], v[194:197], v[86:89]
	v_mfma_f32_16x16x32_bf16 v[82:85], v[162:165], v[194:197], v[82:85]
	v_mfma_f32_16x16x32_bf16 v[126:129], v[158:161], v[174:177], v[126:129]
	v_mfma_f32_16x16x32_bf16 v[122:125], v[166:169], v[174:177], v[122:125]
	v_mfma_f32_16x16x32_bf16 v[118:121], v[158:161], v[182:185], v[118:121]
	v_mfma_f32_16x16x32_bf16 v[114:117], v[166:169], v[182:185], v[114:117]
	v_mfma_f32_16x16x32_bf16 v[102:105], v[158:161], v[190:193], v[102:105]
	v_mfma_f32_16x16x32_bf16 v[98:101], v[166:169], v[190:193], v[98:101]
	v_mfma_f32_16x16x32_bf16 v[86:89], v[158:161], v[198:201], v[86:89]
	v_mfma_f32_16x16x32_bf16 v[82:85], v[166:169], v[198:201], v[82:85]
	s_setprio 0
	s_barrier
	s_add_i32 s63, 0, 0x1c000
	s_add_i32 s60, s62, s18
	v_add_u32_e32 v1, s63, v148
	v_lshl_add_u64 v[218:219], v[218:219], 0, s[8:9]
	s_mov_b32 m0, s60
	ds_read_b128 v[202:205], v1
	ds_read_b128 v[206:209], v1 offset:1024
	ds_read_b128 v[210:213], v1 offset:2048
	ds_read_b128 v[214:217], v1 offset:3072
	global_load_lds_dwordx4 v[218:219], off
	v_lshl_add_u64 v[218:219], v[220:221], 0, s[8:9]
	s_add_i32 m0, s60, 0x2000
	s_nop 0
	global_load_lds_dwordx4 v[218:219], off
	s_barrier
	s_waitcnt lgkmcnt(0)
	s_setprio 1
	s_waitcnt lgkmcnt(0)
	v_mfma_f32_16x16x32_bf16 v[110:113], v[202:205], v[170:173], v[110:113]
	v_mfma_f32_16x16x32_bf16 v[106:109], v[210:213], v[170:173], v[106:109]
	v_mfma_f32_16x16x32_bf16 v[94:97], v[202:205], v[178:181], v[94:97]
	v_mfma_f32_16x16x32_bf16 v[90:93], v[210:213], v[178:181], v[90:93]
	v_mfma_f32_16x16x32_bf16 v[78:81], v[202:205], v[186:189], v[78:81]
	v_mfma_f32_16x16x32_bf16 v[74:77], v[210:213], v[186:189], v[74:77]
	v_mfma_f32_16x16x32_bf16 v[70:73], v[202:205], v[194:197], v[70:73]
	v_mfma_f32_16x16x32_bf16 v[66:69], v[210:213], v[194:197], v[66:69]
	v_mfma_f32_16x16x32_bf16 v[110:113], v[206:209], v[174:177], v[110:113]
	v_mfma_f32_16x16x32_bf16 v[106:109], v[214:217], v[174:177], v[106:109]
	v_mfma_f32_16x16x32_bf16 v[94:97], v[206:209], v[182:185], v[94:97]
	v_mfma_f32_16x16x32_bf16 v[90:93], v[214:217], v[182:185], v[90:93]
	v_mfma_f32_16x16x32_bf16 v[78:81], v[206:209], v[190:193], v[78:81]
	v_mfma_f32_16x16x32_bf16 v[74:77], v[214:217], v[190:193], v[74:77]
	v_mfma_f32_16x16x32_bf16 v[70:73], v[206:209], v[198:201], v[70:73]
	v_mfma_f32_16x16x32_bf16 v[66:69], v[214:217], v[198:201], v[66:69]
	s_setprio 0
	s_mov_b32 m0, s34
	v_lshl_add_u64 v[218:219], v[222:223], 0, s[8:9]
	s_barrier
	ds_read_b128 v[170:173], v151 offset:49152
	ds_read_b128 v[174:177], v151 offset:50176
	ds_read_b128 v[178:181], v151 offset:51200
	ds_read_b128 v[182:185], v151 offset:52224
	ds_read_b128 v[186:189], v151 offset:53248
	ds_read_b128 v[190:193], v151 offset:54272
	ds_read_b128 v[194:197], v151 offset:55296
	ds_read_b128 v[198:201], v151 offset:56320
	global_load_lds_dwordx4 v[218:219], off
	v_lshl_add_u64 v[218:219], v[224:225], 0, s[8:9]
	s_mov_b32 m0, s35
	s_nop 0
	global_load_lds_dwordx4 v[218:219], off
	s_barrier
	s_waitcnt lgkmcnt(0)
	s_setprio 1
	s_waitcnt lgkmcnt(0)
	v_mfma_f32_16x16x32_bf16 v[62:65], v[154:157], v[170:173], v[62:65]
	v_mfma_f32_16x16x32_bf16 v[58:61], v[162:165], v[170:173], v[58:61]
	v_mfma_f32_16x16x32_bf16 v[54:57], v[154:157], v[178:181], v[54:57]
	v_mfma_f32_16x16x32_bf16 v[50:53], v[162:165], v[178:181], v[50:53]
	v_mfma_f32_16x16x32_bf16 v[38:41], v[154:157], v[186:189], v[38:41]
	v_mfma_f32_16x16x32_bf16 v[34:37], v[162:165], v[186:189], v[34:37]
	v_mfma_f32_16x16x32_bf16 v[22:25], v[154:157], v[194:197], v[22:25]
	v_mfma_f32_16x16x32_bf16 v[18:21], v[162:165], v[194:197], v[18:21]
	v_mfma_f32_16x16x32_bf16 v[62:65], v[158:161], v[174:177], v[62:65]
	v_mfma_f32_16x16x32_bf16 v[58:61], v[166:169], v[174:177], v[58:61]
	v_mfma_f32_16x16x32_bf16 v[54:57], v[158:161], v[182:185], v[54:57]
	v_mfma_f32_16x16x32_bf16 v[50:53], v[166:169], v[182:185], v[50:53]
	v_mfma_f32_16x16x32_bf16 v[38:41], v[158:161], v[190:193], v[38:41]
	v_mfma_f32_16x16x32_bf16 v[34:37], v[166:169], v[190:193], v[34:37]
	v_mfma_f32_16x16x32_bf16 v[22:25], v[158:161], v[198:201], v[22:25]
	v_mfma_f32_16x16x32_bf16 v[18:21], v[166:169], v[198:201], v[18:21]
	s_setprio 0
	s_barrier
	s_add_u32 s60, s84, 0x80080
	s_addc_u32 s61, s85, 0
	s_add_i32 s62, s63, s18
	s_mov_b32 m0, s62
	s_nop 0
	global_load_lds_dwordx4 v134, s[60:61]
	s_add_i32 m0, s62, 0x2000
	s_nop 0
	global_load_lds_dwordx4 v130, s[60:61]
	s_waitcnt vmcnt(6)
	s_barrier
	s_setprio 1
	v_mfma_f32_16x16x32_bf16 v[46:49], v[202:205], v[170:173], v[46:49]
	v_mfma_f32_16x16x32_bf16 v[42:45], v[210:213], v[170:173], v[42:45]
	v_mfma_f32_16x16x32_bf16 v[30:33], v[202:205], v[178:181], v[30:33]
	v_mfma_f32_16x16x32_bf16 v[26:29], v[210:213], v[178:181], v[26:29]
	v_mfma_f32_16x16x32_bf16 v[14:17], v[202:205], v[186:189], v[14:17]
	v_mfma_f32_16x16x32_bf16 v[10:13], v[210:213], v[186:189], v[10:13]
	v_mfma_f32_16x16x32_bf16 v[6:9], v[202:205], v[194:197], v[6:9]
	v_mfma_f32_16x16x32_bf16 v[2:5], v[210:213], v[194:197], v[2:5]
	v_mfma_f32_16x16x32_bf16 v[46:49], v[206:209], v[174:177], v[46:49]
	v_mfma_f32_16x16x32_bf16 v[42:45], v[214:217], v[174:177], v[42:45]
	v_mfma_f32_16x16x32_bf16 v[30:33], v[206:209], v[182:185], v[30:33]
	v_mfma_f32_16x16x32_bf16 v[26:29], v[214:217], v[182:185], v[26:29]
	v_mfma_f32_16x16x32_bf16 v[14:17], v[206:209], v[190:193], v[14:17]
	v_mfma_f32_16x16x32_bf16 v[10:13], v[214:217], v[190:193], v[10:13]
	v_mfma_f32_16x16x32_bf16 v[6:9], v[206:209], v[198:201], v[6:9]
	v_mfma_f32_16x16x32_bf16 v[2:5], v[214:217], v[198:201], v[2:5]
	s_setprio 0
	s_add_i32 s59, s59, 2
	s_add_u32 s24, s24, 0x100
	s_addc_u32 s25, s25, 0
	s_add_u32 s57, s57, 0x100
	s_addc_u32 s58, s58, 0
	s_cmp_gt_u32 s59, 29
	s_barrier
	s_cbranch_scc0 .LBB0_85

.LBB0_527:
	s_ashr_i32 s23, s22, 31
	v_cmp_lt_i64_e32 vcc, s[24:25], v[138:139]
	s_lshl_b64 s[24:25], s[22:23], 21
	v_readlane_b32 s17, v254, 38
	s_add_u32 s24, s17, s24
	s_addc_u32 s25, s66, s25
	s_and_b64 s[44:45], vcc, exec
	s_cselect_b32 s23, s25, s49
	s_cselect_b32 s56, s24, s48
	s_ashr_i32 s17, s16, 31
	s_lshl_b64 s[44:45], s[16:17], 21
	v_readlane_b32 s54, v254, 28
	v_readlane_b32 s55, v254, 29
	s_add_u32 s44, s54, s44
	s_addc_u32 s45, s55, s45
	s_and_b64 s[54:55], vcc, exec
	s_cselect_b32 s17, s45, s53
	s_cselect_b32 s57, s44, s52
	s_add_u32 s48, s48, 0x100080
	s_addc_u32 s49, s49, 0
	s_add_u32 s58, s52, 0x100
	v_mov_b32_e32 v2, 0
	s_addc_u32 s59, s53, 0
	s_mov_b32 s60, -2
	s_waitcnt vmcnt(0)
	ds_read_b128 v[142:145], v151
	ds_read_b128 v[154:157], v151 offset:1024
	ds_read_b128 v[158:161], v151 offset:2048
	ds_read_b128 v[162:165], v151 offset:3072
	s_add_u32 s52, s48, 0xfff00080
	s_addc_u32 s53, s49, -1
	s_cmp_eq_u32 s60, 60
	s_cselect_b32 s55, s23, s53
	s_cselect_b32 s54, s56, s52
	s_cselect_b32 s53, s17, s59
	s_cselect_b32 s52, s57, s58
	s_add_i32 m0, s19, 0xc000
	ds_read_b128 v[166:169], v152
	ds_read_b128 v[170:173], v152 offset:1024
	ds_read_b128 v[174:177], v152 offset:2048
	ds_read_b128 v[178:181], v152 offset:3072
	ds_read_b128 v[182:185], v152 offset:4096
	ds_read_b128 v[186:189], v152 offset:5120
	ds_read_b128 v[190:193], v152 offset:6144
	ds_read_b128 v[194:197], v152 offset:7168
	global_load_lds_dwordx4 v134, s[48:49]
	s_add_i32 m0, s19, 0xe000
	s_nop 0
	global_load_lds_dwordx4 v136, s[48:49]
	s_waitcnt lgkmcnt(8)
	s_barrier
	s_waitcnt lgkmcnt(0)
	s_setprio 1
	s_waitcnt lgkmcnt(0)
	v_mfma_f32_16x16x32_bf16 v[126:129], v[142:145], v[166:169], 0
	v_mfma_f32_16x16x32_bf16 v[122:125], v[158:161], v[166:169], 0
	v_mfma_f32_16x16x32_bf16 v[118:121], v[142:145], v[174:177], 0
	v_mfma_f32_16x16x32_bf16 v[114:117], v[158:161], v[174:177], 0
	v_mfma_f32_16x16x32_bf16 v[94:97], v[142:145], v[182:185], 0
	v_mfma_f32_16x16x32_bf16 v[90:93], v[158:161], v[182:185], 0
	v_mfma_f32_16x16x32_bf16 v[86:89], v[142:145], v[190:193], 0
	v_mfma_f32_16x16x32_bf16 v[82:85], v[158:161], v[190:193], 0
	v_mfma_f32_16x16x32_bf16 v[126:129], v[154:157], v[170:173], v[126:129]
	v_mfma_f32_16x16x32_bf16 v[122:125], v[162:165], v[170:173], v[122:125]
	v_mfma_f32_16x16x32_bf16 v[118:121], v[154:157], v[178:181], v[118:121]
	v_mfma_f32_16x16x32_bf16 v[114:117], v[162:165], v[178:181], v[114:117]
	v_mfma_f32_16x16x32_bf16 v[94:97], v[154:157], v[186:189], v[94:97]
	v_mfma_f32_16x16x32_bf16 v[90:93], v[162:165], v[186:189], v[90:93]
	v_mfma_f32_16x16x32_bf16 v[86:89], v[154:157], v[194:197], v[86:89]
	v_mfma_f32_16x16x32_bf16 v[82:85], v[162:165], v[194:197], v[82:85]
	s_setprio 0
	s_barrier
	s_add_i32 s61, s40, s18
	v_lshl_add_u64 v[146:147], s[52:53], 0, v[130:131]
	s_mov_b32 m0, s61
	ds_read_b128 v[198:201], v153
	ds_read_b128 v[202:205], v153 offset:1024
	ds_read_b128 v[206:209], v153 offset:2048
	ds_read_b128 v[210:213], v153 offset:3072
	global_load_lds_dwordx4 v[146:147], off
	v_lshl_add_u64 v[214:215], s[52:53], 0, v[132:133]
	s_add_i32 m0, s61, 0x2000
	s_nop 0
	global_load_lds_dwordx4 v[214:215], off
	s_barrier
	s_waitcnt lgkmcnt(0)
	s_setprio 1
	s_waitcnt lgkmcnt(0)
	v_mfma_f32_16x16x32_bf16 v[110:113], v[198:201], v[166:169], 0
	v_mfma_f32_16x16x32_bf16 v[106:109], v[206:209], v[166:169], 0
	v_mfma_f32_16x16x32_bf16 v[102:105], v[198:201], v[174:177], 0
	v_mfma_f32_16x16x32_bf16 v[98:101], v[206:209], v[174:177], 0
	v_mfma_f32_16x16x32_bf16 v[78:81], v[198:201], v[182:185], 0
	v_mfma_f32_16x16x32_bf16 v[74:77], v[206:209], v[182:185], 0
	v_mfma_f32_16x16x32_bf16 v[70:73], v[198:201], v[190:193], 0
	v_mfma_f32_16x16x32_bf16 v[66:69], v[206:209], v[190:193], 0
	v_mfma_f32_16x16x32_bf16 v[110:113], v[202:205], v[170:173], v[110:113]
	v_mfma_f32_16x16x32_bf16 v[106:109], v[210:213], v[170:173], v[106:109]
	v_mfma_f32_16x16x32_bf16 v[102:105], v[202:205], v[178:181], v[102:105]
	v_mfma_f32_16x16x32_bf16 v[98:101], v[210:213], v[178:181], v[98:101]
	v_mfma_f32_16x16x32_bf16 v[78:81], v[202:205], v[186:189], v[78:81]
	v_mfma_f32_16x16x32_bf16 v[74:77], v[210:213], v[186:189], v[74:77]
	v_mfma_f32_16x16x32_bf16 v[70:73], v[202:205], v[194:197], v[70:73]
	v_mfma_f32_16x16x32_bf16 v[66:69], v[210:213], v[194:197], v[66:69]
	s_setprio 0
	s_mov_b32 m0, s19
	v_lshl_add_u64 v[216:217], s[54:55], 0, v[130:131]
	s_barrier
	ds_read_b128 v[166:169], v152 offset:16384
	ds_read_b128 v[170:173], v152 offset:17408
	ds_read_b128 v[174:177], v152 offset:18432
	ds_read_b128 v[178:181], v152 offset:19456
	ds_read_b128 v[182:185], v152 offset:20480
	ds_read_b128 v[186:189], v152 offset:21504
	ds_read_b128 v[190:193], v152 offset:22528
	ds_read_b128 v[194:197], v152 offset:23552
	global_load_lds_dwordx4 v[216:217], off
	v_lshl_add_u64 v[218:219], s[54:55], 0, v[132:133]
	s_mov_b32 m0, s20
	s_nop 0
	global_load_lds_dwordx4 v[218:219], off
	s_barrier
	s_waitcnt lgkmcnt(0)
	s_setprio 1
	s_waitcnt lgkmcnt(0)
	v_mfma_f32_16x16x32_bf16 v[62:65], v[142:145], v[166:169], 0
	v_mfma_f32_16x16x32_bf16 v[58:61], v[158:161], v[166:169], 0
	v_mfma_f32_16x16x32_bf16 v[54:57], v[142:145], v[174:177], 0
	v_mfma_f32_16x16x32_bf16 v[50:53], v[158:161], v[174:177], 0
	v_mfma_f32_16x16x32_bf16 v[30:33], v[142:145], v[182:185], 0
	v_mfma_f32_16x16x32_bf16 v[26:29], v[158:161], v[182:185], 0
	v_mfma_f32_16x16x32_bf16 v[22:25], v[142:145], v[190:193], 0
	v_mfma_f32_16x16x32_bf16 v[18:21], v[158:161], v[190:193], 0
	v_mfma_f32_16x16x32_bf16 v[62:65], v[154:157], v[170:173], v[62:65]
	v_mfma_f32_16x16x32_bf16 v[58:61], v[162:165], v[170:173], v[58:61]
	v_mfma_f32_16x16x32_bf16 v[54:57], v[154:157], v[178:181], v[54:57]
	v_mfma_f32_16x16x32_bf16 v[50:53], v[162:165], v[178:181], v[50:53]
	v_mfma_f32_16x16x32_bf16 v[30:33], v[154:157], v[186:189], v[30:33]
	v_mfma_f32_16x16x32_bf16 v[26:29], v[162:165], v[186:189], v[26:29]
	v_mfma_f32_16x16x32_bf16 v[22:25], v[154:157], v[194:197], v[22:25]
	v_mfma_f32_16x16x32_bf16 v[18:21], v[162:165], v[194:197], v[18:21]
	s_setprio 0
	s_barrier
	s_add_u32 s62, s52, 0x100000
	s_addc_u32 s63, s53, 0
	s_add_i32 s61, s41, s18
	s_mov_b32 m0, s61
	s_nop 0
	global_load_lds_dwordx4 v130, s[62:63]
	s_add_i32 m0, s61, 0x2000
	s_nop 0
	global_load_lds_dwordx4 v132, s[62:63]
	s_waitcnt vmcnt(6)
	s_barrier
	s_setprio 1
	v_mfma_f32_16x16x32_bf16 v[46:49], v[198:201], v[166:169], 0
	v_mfma_f32_16x16x32_bf16 v[42:45], v[206:209], v[166:169], 0
	v_mfma_f32_16x16x32_bf16 v[38:41], v[198:201], v[174:177], 0
	v_mfma_f32_16x16x32_bf16 v[34:37], v[206:209], v[174:177], 0
	v_mfma_f32_16x16x32_bf16 v[14:17], v[198:201], v[182:185], 0
	v_mfma_f32_16x16x32_bf16 v[10:13], v[206:209], v[182:185], 0
	v_mfma_f32_16x16x32_bf16 v[6:9], v[198:201], v[190:193], 0
	v_mfma_f32_16x16x32_bf16 v[2:5], v[206:209], v[190:193], 0
	v_mfma_f32_16x16x32_bf16 v[46:49], v[202:205], v[170:173], v[46:49]
	v_mfma_f32_16x16x32_bf16 v[42:45], v[210:213], v[170:173], v[42:45]
	v_mfma_f32_16x16x32_bf16 v[38:41], v[202:205], v[178:181], v[38:41]
	v_mfma_f32_16x16x32_bf16 v[34:37], v[210:213], v[178:181], v[34:37]
	v_mfma_f32_16x16x32_bf16 v[14:17], v[202:205], v[186:189], v[14:17]
	v_mfma_f32_16x16x32_bf16 v[10:13], v[210:213], v[186:189], v[10:13]
	v_mfma_f32_16x16x32_bf16 v[6:9], v[202:205], v[194:197], v[6:9]
	v_mfma_f32_16x16x32_bf16 v[2:5], v[210:213], v[194:197], v[2:5]
	s_setprio 0
	s_add_i32 s61, 0, 0x18000
	v_add_u32_e32 v1, s61, v149
	s_barrier
	ds_read_b128 v[142:145], v1
	ds_read_b128 v[154:157], v1 offset:1024
	ds_read_b128 v[158:161], v1 offset:2048
	ds_read_b128 v[162:165], v1 offset:3072
	s_add_u32 s54, s54, 0x100000
	s_addc_u32 s55, s55, 0
	s_mov_b32 m0, s21
	ds_read_b128 v[166:169], v152 offset:32768
	ds_read_b128 v[170:173], v152 offset:33792
	ds_read_b128 v[174:177], v152 offset:34816
	ds_read_b128 v[178:181], v152 offset:35840
	ds_read_b128 v[182:185], v152 offset:36864
	ds_read_b128 v[186:189], v152 offset:37888
	ds_read_b128 v[190:193], v152 offset:38912
	ds_read_b128 v[194:197], v152 offset:39936
	global_load_lds_dwordx4 v130, s[54:55]
	s_mov_b32 m0, s26
	s_nop 0
	global_load_lds_dwordx4 v132, s[54:55]
	s_waitcnt lgkmcnt(8)
	s_barrier
	s_waitcnt lgkmcnt(0)
	s_setprio 1
	s_waitcnt lgkmcnt(0)
	v_mfma_f32_16x16x32_bf16 v[126:129], v[142:145], v[166:169], v[126:129]
	v_mfma_f32_16x16x32_bf16 v[122:125], v[158:161], v[166:169], v[122:125]
	v_mfma_f32_16x16x32_bf16 v[118:121], v[142:145], v[174:177], v[118:121]
	v_mfma_f32_16x16x32_bf16 v[114:117], v[158:161], v[174:177], v[114:117]
	v_mfma_f32_16x16x32_bf16 v[94:97], v[142:145], v[182:185], v[94:97]
	v_mfma_f32_16x16x32_bf16 v[90:93], v[158:161], v[182:185], v[90:93]
	v_mfma_f32_16x16x32_bf16 v[86:89], v[142:145], v[190:193], v[86:89]
	v_mfma_f32_16x16x32_bf16 v[82:85], v[158:161], v[190:193], v[82:85]
	v_mfma_f32_16x16x32_bf16 v[126:129], v[154:157], v[170:173], v[126:129]
	v_mfma_f32_16x16x32_bf16 v[122:125], v[162:165], v[170:173], v[122:125]
	v_mfma_f32_16x16x32_bf16 v[118:121], v[154:157], v[178:181], v[118:121]
	v_mfma_f32_16x16x32_bf16 v[114:117], v[162:165], v[178:181], v[114:117]
	v_mfma_f32_16x16x32_bf16 v[94:97], v[154:157], v[186:189], v[94:97]
	v_mfma_f32_16x16x32_bf16 v[90:93], v[162:165], v[186:189], v[90:93]
	v_mfma_f32_16x16x32_bf16 v[86:89], v[154:157], v[194:197], v[86:89]
	v_mfma_f32_16x16x32_bf16 v[82:85], v[162:165], v[194:197], v[82:85]
	s_setprio 0
	s_barrier
	s_add_i32 s54, 0, 0x1c000
	s_add_i32 s55, s61, s18
	v_add_u32_e32 v1, s54, v149
	v_lshl_add_u64 v[146:147], v[146:147], 0, s[8:9]
	s_mov_b32 m0, s55
	ds_read_b128 v[198:201], v1
	ds_read_b128 v[202:205], v1 offset:1024
	ds_read_b128 v[206:209], v1 offset:2048
	ds_read_b128 v[210:213], v1 offset:3072
	global_load_lds_dwordx4 v[146:147], off
	v_lshl_add_u64 v[146:147], v[214:215], 0, s[8:9]
	s_add_i32 m0, s55, 0x2000
	s_nop 0
	global_load_lds_dwordx4 v[146:147], off
	s_barrier
	s_waitcnt lgkmcnt(0)
	s_setprio 1
	s_waitcnt lgkmcnt(0)
	v_mfma_f32_16x16x32_bf16 v[110:113], v[198:201], v[166:169], v[110:113]
	v_mfma_f32_16x16x32_bf16 v[106:109], v[206:209], v[166:169], v[106:109]
	v_mfma_f32_16x16x32_bf16 v[102:105], v[198:201], v[174:177], v[102:105]
	v_mfma_f32_16x16x32_bf16 v[98:101], v[206:209], v[174:177], v[98:101]
	v_mfma_f32_16x16x32_bf16 v[78:81], v[198:201], v[182:185], v[78:81]
	v_mfma_f32_16x16x32_bf16 v[74:77], v[206:209], v[182:185], v[74:77]
	v_mfma_f32_16x16x32_bf16 v[70:73], v[198:201], v[190:193], v[70:73]
	v_mfma_f32_16x16x32_bf16 v[66:69], v[206:209], v[190:193], v[66:69]
	v_mfma_f32_16x16x32_bf16 v[110:113], v[202:205], v[170:173], v[110:113]
	v_mfma_f32_16x16x32_bf16 v[106:109], v[210:213], v[170:173], v[106:109]
	v_mfma_f32_16x16x32_bf16 v[102:105], v[202:205], v[178:181], v[102:105]
	v_mfma_f32_16x16x32_bf16 v[98:101], v[210:213], v[178:181], v[98:101]
	v_mfma_f32_16x16x32_bf16 v[78:81], v[202:205], v[186:189], v[78:81]
	v_mfma_f32_16x16x32_bf16 v[74:77], v[210:213], v[186:189], v[74:77]
	v_mfma_f32_16x16x32_bf16 v[70:73], v[202:205], v[194:197], v[70:73]
	v_mfma_f32_16x16x32_bf16 v[66:69], v[210:213], v[194:197], v[66:69]
	s_setprio 0
	s_mov_b32 m0, s33
	v_lshl_add_u64 v[146:147], v[216:217], 0, s[8:9]
	s_barrier
	ds_read_b128 v[166:169], v152 offset:49152
	ds_read_b128 v[170:173], v152 offset:50176
	ds_read_b128 v[174:177], v152 offset:51200
	ds_read_b128 v[178:181], v152 offset:52224
	ds_read_b128 v[182:185], v152 offset:53248
	ds_read_b128 v[186:189], v152 offset:54272
	ds_read_b128 v[190:193], v152 offset:55296
	ds_read_b128 v[194:197], v152 offset:56320
	global_load_lds_dwordx4 v[146:147], off
	v_lshl_add_u64 v[146:147], v[218:219], 0, s[8:9]
	s_mov_b32 m0, s34
	s_nop 0
	global_load_lds_dwordx4 v[146:147], off
	s_barrier
	s_waitcnt lgkmcnt(0)
	s_setprio 1
	s_waitcnt lgkmcnt(0)
	v_mfma_f32_16x16x32_bf16 v[62:65], v[142:145], v[166:169], v[62:65]
	v_mfma_f32_16x16x32_bf16 v[58:61], v[158:161], v[166:169], v[58:61]
	v_mfma_f32_16x16x32_bf16 v[54:57], v[142:145], v[174:177], v[54:57]
	v_mfma_f32_16x16x32_bf16 v[50:53], v[158:161], v[174:177], v[50:53]
	v_mfma_f32_16x16x32_bf16 v[30:33], v[142:145], v[182:185], v[30:33]
	v_mfma_f32_16x16x32_bf16 v[26:29], v[158:161], v[182:185], v[26:29]
	v_mfma_f32_16x16x32_bf16 v[22:25], v[142:145], v[190:193], v[22:25]
	v_mfma_f32_16x16x32_bf16 v[18:21], v[158:161], v[190:193], v[18:21]
	v_mfma_f32_16x16x32_bf16 v[62:65], v[154:157], v[170:173], v[62:65]
	v_mfma_f32_16x16x32_bf16 v[58:61], v[162:165], v[170:173], v[58:61]
	v_mfma_f32_16x16x32_bf16 v[54:57], v[154:157], v[178:181], v[54:57]
	v_mfma_f32_16x16x32_bf16 v[50:53], v[162:165], v[178:181], v[50:53]
	v_mfma_f32_16x16x32_bf16 v[30:33], v[154:157], v[186:189], v[30:33]
	v_mfma_f32_16x16x32_bf16 v[26:29], v[162:165], v[186:189], v[26:29]
	v_mfma_f32_16x16x32_bf16 v[22:25], v[154:157], v[194:197], v[22:25]
	v_mfma_f32_16x16x32_bf16 v[18:21], v[162:165], v[194:197], v[18:21]
	s_setprio 0
	s_barrier
	s_add_u32 s52, s52, 0x100080
	s_addc_u32 s53, s53, 0
	s_add_i32 s54, s54, s18
	s_mov_b32 m0, s54
	s_nop 0
	global_load_lds_dwordx4 v130, s[52:53]
	s_add_i32 m0, s54, 0x2000
	s_nop 0
	global_load_lds_dwordx4 v132, s[52:53]
	s_waitcnt vmcnt(6)
	s_barrier
	s_setprio 1
	v_mfma_f32_16x16x32_bf16 v[46:49], v[198:201], v[166:169], v[46:49]
	v_mfma_f32_16x16x32_bf16 v[42:45], v[206:209], v[166:169], v[42:45]
	v_mfma_f32_16x16x32_bf16 v[38:41], v[198:201], v[174:177], v[38:41]
	v_mfma_f32_16x16x32_bf16 v[34:37], v[206:209], v[174:177], v[34:37]
	v_mfma_f32_16x16x32_bf16 v[14:17], v[198:201], v[182:185], v[14:17]
	v_mfma_f32_16x16x32_bf16 v[10:13], v[206:209], v[182:185], v[10:13]
	v_mfma_f32_16x16x32_bf16 v[6:9], v[198:201], v[190:193], v[6:9]
	v_mfma_f32_16x16x32_bf16 v[2:5], v[206:209], v[190:193], v[2:5]
	v_mfma_f32_16x16x32_bf16 v[46:49], v[202:205], v[170:173], v[46:49]
	v_mfma_f32_16x16x32_bf16 v[42:45], v[210:213], v[170:173], v[42:45]
	v_mfma_f32_16x16x32_bf16 v[38:41], v[202:205], v[178:181], v[38:41]
	v_mfma_f32_16x16x32_bf16 v[34:37], v[210:213], v[178:181], v[34:37]
	v_mfma_f32_16x16x32_bf16 v[14:17], v[202:205], v[186:189], v[14:17]
	v_mfma_f32_16x16x32_bf16 v[10:13], v[210:213], v[186:189], v[10:13]
	v_mfma_f32_16x16x32_bf16 v[6:9], v[202:205], v[194:197], v[6:9]
	v_mfma_f32_16x16x32_bf16 v[2:5], v[210:213], v[194:197], v[2:5]
	s_setprio 0
	s_add_i32 s60, s60, 2
	s_add_u32 s48, s48, 0x100
	s_addc_u32 s49, s49, 0
	s_add_u32 s58, s58, 0x100
	s_addc_u32 s59, s59, 0
	s_cmp_gt_u32 s60, 61
	s_barrier
	s_cbranch_scc1 .Lpeel_528_after
.LBB0_528:
	ds_read_b128 v[142:145], v151
	ds_read_b128 v[154:157], v151 offset:1024
	ds_read_b128 v[158:161], v151 offset:2048
	ds_read_b128 v[162:165], v151 offset:3072
	s_add_u32 s52, s48, 0xfff00080
	s_addc_u32 s53, s49, -1
	s_cmp_eq_u32 s60, 60
	s_cselect_b32 s55, s23, s53
	s_cselect_b32 s54, s56, s52
	s_cselect_b32 s53, s17, s59
	s_cselect_b32 s52, s57, s58
	s_add_i32 m0, s19, 0xc000
	ds_read_b128 v[166:169], v152
	ds_read_b128 v[170:173], v152 offset:1024
	ds_read_b128 v[174:177], v152 offset:2048
	ds_read_b128 v[178:181], v152 offset:3072
	ds_read_b128 v[182:185], v152 offset:4096
	ds_read_b128 v[186:189], v152 offset:5120
	ds_read_b128 v[190:193], v152 offset:6144
	ds_read_b128 v[194:197], v152 offset:7168
	global_load_lds_dwordx4 v134, s[48:49]
	s_add_i32 m0, s19, 0xe000
	s_nop 0
	global_load_lds_dwordx4 v136, s[48:49]
	s_waitcnt lgkmcnt(8)
	s_barrier
	s_waitcnt lgkmcnt(0)
	s_setprio 1
	s_waitcnt lgkmcnt(0)
	v_mfma_f32_16x16x32_bf16 v[126:129], v[142:145], v[166:169], v[126:129]
	v_mfma_f32_16x16x32_bf16 v[122:125], v[158:161], v[166:169], v[122:125]
	v_mfma_f32_16x16x32_bf16 v[118:121], v[142:145], v[174:177], v[118:121]
	v_mfma_f32_16x16x32_bf16 v[114:117], v[158:161], v[174:177], v[114:117]
	v_mfma_f32_16x16x32_bf16 v[94:97], v[142:145], v[182:185], v[94:97]
	v_mfma_f32_16x16x32_bf16 v[90:93], v[158:161], v[182:185], v[90:93]
	v_mfma_f32_16x16x32_bf16 v[86:89], v[142:145], v[190:193], v[86:89]
	v_mfma_f32_16x16x32_bf16 v[82:85], v[158:161], v[190:193], v[82:85]
	v_mfma_f32_16x16x32_bf16 v[126:129], v[154:157], v[170:173], v[126:129]
	v_mfma_f32_16x16x32_bf16 v[122:125], v[162:165], v[170:173], v[122:125]
	v_mfma_f32_16x16x32_bf16 v[118:121], v[154:157], v[178:181], v[118:121]
	v_mfma_f32_16x16x32_bf16 v[114:117], v[162:165], v[178:181], v[114:117]
	v_mfma_f32_16x16x32_bf16 v[94:97], v[154:157], v[186:189], v[94:97]
	v_mfma_f32_16x16x32_bf16 v[90:93], v[162:165], v[186:189], v[90:93]
	v_mfma_f32_16x16x32_bf16 v[86:89], v[154:157], v[194:197], v[86:89]
	v_mfma_f32_16x16x32_bf16 v[82:85], v[162:165], v[194:197], v[82:85]
	s_setprio 0
	s_barrier
	s_add_i32 s61, s40, s18
	v_lshl_add_u64 v[146:147], s[52:53], 0, v[130:131]
	s_mov_b32 m0, s61
	ds_read_b128 v[198:201], v153
	ds_read_b128 v[202:205], v153 offset:1024
	ds_read_b128 v[206:209], v153 offset:2048
	ds_read_b128 v[210:213], v153 offset:3072
	global_load_lds_dwordx4 v[146:147], off
	v_lshl_add_u64 v[214:215], s[52:53], 0, v[132:133]
	s_add_i32 m0, s61, 0x2000
	s_nop 0
	global_load_lds_dwordx4 v[214:215], off
	s_barrier
	s_waitcnt lgkmcnt(0)
	s_setprio 1
	s_waitcnt lgkmcnt(0)
	v_mfma_f32_16x16x32_bf16 v[110:113], v[198:201], v[166:169], v[110:113]
	v_mfma_f32_16x16x32_bf16 v[106:109], v[206:209], v[166:169], v[106:109]
	v_mfma_f32_16x16x32_bf16 v[102:105], v[198:201], v[174:177], v[102:105]
	v_mfma_f32_16x16x32_bf16 v[98:101], v[206:209], v[174:177], v[98:101]
	v_mfma_f32_16x16x32_bf16 v[78:81], v[198:201], v[182:185], v[78:81]
	v_mfma_f32_16x16x32_bf16 v[74:77], v[206:209], v[182:185], v[74:77]
	v_mfma_f32_16x16x32_bf16 v[70:73], v[198:201], v[190:193], v[70:73]
	v_mfma_f32_16x16x32_bf16 v[66:69], v[206:209], v[190:193], v[66:69]
	v_mfma_f32_16x16x32_bf16 v[110:113], v[202:205], v[170:173], v[110:113]
	v_mfma_f32_16x16x32_bf16 v[106:109], v[210:213], v[170:173], v[106:109]
	v_mfma_f32_16x16x32_bf16 v[102:105], v[202:205], v[178:181], v[102:105]
	v_mfma_f32_16x16x32_bf16 v[98:101], v[210:213], v[178:181], v[98:101]
	v_mfma_f32_16x16x32_bf16 v[78:81], v[202:205], v[186:189], v[78:81]
	v_mfma_f32_16x16x32_bf16 v[74:77], v[210:213], v[186:189], v[74:77]
	v_mfma_f32_16x16x32_bf16 v[70:73], v[202:205], v[194:197], v[70:73]
	v_mfma_f32_16x16x32_bf16 v[66:69], v[210:213], v[194:197], v[66:69]
	s_setprio 0
	s_mov_b32 m0, s19
	v_lshl_add_u64 v[216:217], s[54:55], 0, v[130:131]
	s_barrier
	ds_read_b128 v[166:169], v152 offset:16384
	ds_read_b128 v[170:173], v152 offset:17408
	ds_read_b128 v[174:177], v152 offset:18432
	ds_read_b128 v[178:181], v152 offset:19456
	ds_read_b128 v[182:185], v152 offset:20480
	ds_read_b128 v[186:189], v152 offset:21504
	ds_read_b128 v[190:193], v152 offset:22528
	ds_read_b128 v[194:197], v152 offset:23552
	global_load_lds_dwordx4 v[216:217], off
	v_lshl_add_u64 v[218:219], s[54:55], 0, v[132:133]
	s_mov_b32 m0, s20
	s_nop 0
	global_load_lds_dwordx4 v[218:219], off
	s_barrier
	s_waitcnt lgkmcnt(0)
	s_setprio 1
	s_waitcnt lgkmcnt(0)
	v_mfma_f32_16x16x32_bf16 v[62:65], v[142:145], v[166:169], v[62:65]
	v_mfma_f32_16x16x32_bf16 v[58:61], v[158:161], v[166:169], v[58:61]
	v_mfma_f32_16x16x32_bf16 v[54:57], v[142:145], v[174:177], v[54:57]
	v_mfma_f32_16x16x32_bf16 v[50:53], v[158:161], v[174:177], v[50:53]
	v_mfma_f32_16x16x32_bf16 v[30:33], v[142:145], v[182:185], v[30:33]
	v_mfma_f32_16x16x32_bf16 v[26:29], v[158:161], v[182:185], v[26:29]
	v_mfma_f32_16x16x32_bf16 v[22:25], v[142:145], v[190:193], v[22:25]
	v_mfma_f32_16x16x32_bf16 v[18:21], v[158:161], v[190:193], v[18:21]
	v_mfma_f32_16x16x32_bf16 v[62:65], v[154:157], v[170:173], v[62:65]
	v_mfma_f32_16x16x32_bf16 v[58:61], v[162:165], v[170:173], v[58:61]
	v_mfma_f32_16x16x32_bf16 v[54:57], v[154:157], v[178:181], v[54:57]
	v_mfma_f32_16x16x32_bf16 v[50:53], v[162:165], v[178:181], v[50:53]
	v_mfma_f32_16x16x32_bf16 v[30:33], v[154:157], v[186:189], v[30:33]
	v_mfma_f32_16x16x32_bf16 v[26:29], v[162:165], v[186:189], v[26:29]
	v_mfma_f32_16x16x32_bf16 v[22:25], v[154:157], v[194:197], v[22:25]
	v_mfma_f32_16x16x32_bf16 v[18:21], v[162:165], v[194:197], v[18:21]
	s_setprio 0
	s_barrier
	s_add_u32 s62, s52, 0x100000
	s_addc_u32 s63, s53, 0
	s_add_i32 s61, s41, s18
	s_mov_b32 m0, s61
	s_nop 0
	global_load_lds_dwordx4 v130, s[62:63]
	s_add_i32 m0, s61, 0x2000
	s_nop 0
	global_load_lds_dwordx4 v132, s[62:63]
	s_waitcnt vmcnt(6)
	s_barrier
	s_setprio 1
	v_mfma_f32_16x16x32_bf16 v[46:49], v[198:201], v[166:169], v[46:49]
	v_mfma_f32_16x16x32_bf16 v[42:45], v[206:209], v[166:169], v[42:45]
	v_mfma_f32_16x16x32_bf16 v[38:41], v[198:201], v[174:177], v[38:41]
	v_mfma_f32_16x16x32_bf16 v[34:37], v[206:209], v[174:177], v[34:37]
	v_mfma_f32_16x16x32_bf16 v[14:17], v[198:201], v[182:185], v[14:17]
	v_mfma_f32_16x16x32_bf16 v[10:13], v[206:209], v[182:185], v[10:13]
	v_mfma_f32_16x16x32_bf16 v[6:9], v[198:201], v[190:193], v[6:9]
	v_mfma_f32_16x16x32_bf16 v[2:5], v[206:209], v[190:193], v[2:5]
	v_mfma_f32_16x16x32_bf16 v[46:49], v[202:205], v[170:173], v[46:49]
	v_mfma_f32_16x16x32_bf16 v[42:45], v[210:213], v[170:173], v[42:45]
	v_mfma_f32_16x16x32_bf16 v[38:41], v[202:205], v[178:181], v[38:41]
	v_mfma_f32_16x16x32_bf16 v[34:37], v[210:213], v[178:181], v[34:37]
	v_mfma_f32_16x16x32_bf16 v[14:17], v[202:205], v[186:189], v[14:17]
	v_mfma_f32_16x16x32_bf16 v[10:13], v[210:213], v[186:189], v[10:13]
	v_mfma_f32_16x16x32_bf16 v[6:9], v[202:205], v[194:197], v[6:9]
	v_mfma_f32_16x16x32_bf16 v[2:5], v[210:213], v[194:197], v[2:5]
	s_setprio 0
	s_add_i32 s61, 0, 0x18000
	v_add_u32_e32 v1, s61, v149
	s_barrier
	ds_read_b128 v[142:145], v1
	ds_read_b128 v[154:157], v1 offset:1024
	ds_read_b128 v[158:161], v1 offset:2048
	ds_read_b128 v[162:165], v1 offset:3072
	s_add_u32 s54, s54, 0x100000
	s_addc_u32 s55, s55, 0
	s_mov_b32 m0, s21
	ds_read_b128 v[166:169], v152 offset:32768
	ds_read_b128 v[170:173], v152 offset:33792
	ds_read_b128 v[174:177], v152 offset:34816
	ds_read_b128 v[178:181], v152 offset:35840
	ds_read_b128 v[182:185], v152 offset:36864
	ds_read_b128 v[186:189], v152 offset:37888
	ds_read_b128 v[190:193], v152 offset:38912
	ds_read_b128 v[194:197], v152 offset:39936
	global_load_lds_dwordx4 v130, s[54:55]
	s_mov_b32 m0, s26
	s_nop 0
	global_load_lds_dwordx4 v132, s[54:55]
	s_waitcnt lgkmcnt(8)
	s_barrier
	s_waitcnt lgkmcnt(0)
	s_setprio 1
	s_waitcnt lgkmcnt(0)
	v_mfma_f32_16x16x32_bf16 v[126:129], v[142:145], v[166:169], v[126:129]
	v_mfma_f32_16x16x32_bf16 v[122:125], v[158:161], v[166:169], v[122:125]
	v_mfma_f32_16x16x32_bf16 v[118:121], v[142:145], v[174:177], v[118:121]
	v_mfma_f32_16x16x32_bf16 v[114:117], v[158:161], v[174:177], v[114:117]
	v_mfma_f32_16x16x32_bf16 v[94:97], v[142:145], v[182:185], v[94:97]
	v_mfma_f32_16x16x32_bf16 v[90:93], v[158:161], v[182:185], v[90:93]
	v_mfma_f32_16x16x32_bf16 v[86:89], v[142:145], v[190:193], v[86:89]
	v_mfma_f32_16x16x32_bf16 v[82:85], v[158:161], v[190:193], v[82:85]
	v_mfma_f32_16x16x32_bf16 v[126:129], v[154:157], v[170:173], v[126:129]
	v_mfma_f32_16x16x32_bf16 v[122:125], v[162:165], v[170:173], v[122:125]
	v_mfma_f32_16x16x32_bf16 v[118:121], v[154:157], v[178:181], v[118:121]
	v_mfma_f32_16x16x32_bf16 v[114:117], v[162:165], v[178:181], v[114:117]
	v_mfma_f32_16x16x32_bf16 v[94:97], v[154:157], v[186:189], v[94:97]
	v_mfma_f32_16x16x32_bf16 v[90:93], v[162:165], v[186:189], v[90:93]
	v_mfma_f32_16x16x32_bf16 v[86:89], v[154:157], v[194:197], v[86:89]
	v_mfma_f32_16x16x32_bf16 v[82:85], v[162:165], v[194:197], v[82:85]
	s_setprio 0
	s_barrier
	s_add_i32 s54, 0, 0x1c000
	s_add_i32 s55, s61, s18
	v_add_u32_e32 v1, s54, v149
	v_lshl_add_u64 v[146:147], v[146:147], 0, s[8:9]
	s_mov_b32 m0, s55
	ds_read_b128 v[198:201], v1
	ds_read_b128 v[202:205], v1 offset:1024
	ds_read_b128 v[206:209], v1 offset:2048
	ds_read_b128 v[210:213], v1 offset:3072
	global_load_lds_dwordx4 v[146:147], off
	v_lshl_add_u64 v[146:147], v[214:215], 0, s[8:9]
	s_add_i32 m0, s55, 0x2000
	s_nop 0
	global_load_lds_dwordx4 v[146:147], off
	s_barrier
	s_waitcnt lgkmcnt(0)
	s_setprio 1
	s_waitcnt lgkmcnt(0)
	v_mfma_f32_16x16x32_bf16 v[110:113], v[198:201], v[166:169], v[110:113]
	v_mfma_f32_16x16x32_bf16 v[106:109], v[206:209], v[166:169], v[106:109]
	v_mfma_f32_16x16x32_bf16 v[102:105], v[198:201], v[174:177], v[102:105]
	v_mfma_f32_16x16x32_bf16 v[98:101], v[206:209], v[174:177], v[98:101]
	v_mfma_f32_16x16x32_bf16 v[78:81], v[198:201], v[182:185], v[78:81]
	v_mfma_f32_16x16x32_bf16 v[74:77], v[206:209], v[182:185], v[74:77]
	v_mfma_f32_16x16x32_bf16 v[70:73], v[198:201], v[190:193], v[70:73]
	v_mfma_f32_16x16x32_bf16 v[66:69], v[206:209], v[190:193], v[66:69]
	v_mfma_f32_16x16x32_bf16 v[110:113], v[202:205], v[170:173], v[110:113]
	v_mfma_f32_16x16x32_bf16 v[106:109], v[210:213], v[170:173], v[106:109]
	v_mfma_f32_16x16x32_bf16 v[102:105], v[202:205], v[178:181], v[102:105]
	v_mfma_f32_16x16x32_bf16 v[98:101], v[210:213], v[178:181], v[98:101]
	v_mfma_f32_16x16x32_bf16 v[78:81], v[202:205], v[186:189], v[78:81]
	v_mfma_f32_16x16x32_bf16 v[74:77], v[210:213], v[186:189], v[74:77]
	v_mfma_f32_16x16x32_bf16 v[70:73], v[202:205], v[194:197], v[70:73]
	v_mfma_f32_16x16x32_bf16 v[66:69], v[210:213], v[194:197], v[66:69]
	s_setprio 0
	s_mov_b32 m0, s33
	v_lshl_add_u64 v[146:147], v[216:217], 0, s[8:9]
	s_barrier
	ds_read_b128 v[166:169], v152 offset:49152
	ds_read_b128 v[170:173], v152 offset:50176
	ds_read_b128 v[174:177], v152 offset:51200
	ds_read_b128 v[178:181], v152 offset:52224
	ds_read_b128 v[182:185], v152 offset:53248
	ds_read_b128 v[186:189], v152 offset:54272
	ds_read_b128 v[190:193], v152 offset:55296
	ds_read_b128 v[194:197], v152 offset:56320
	global_load_lds_dwordx4 v[146:147], off
	v_lshl_add_u64 v[146:147], v[218:219], 0, s[8:9]
	s_mov_b32 m0, s34
	s_nop 0
	global_load_lds_dwordx4 v[146:147], off
	s_barrier
	s_waitcnt lgkmcnt(0)
	s_setprio 1
	s_waitcnt lgkmcnt(0)
	v_mfma_f32_16x16x32_bf16 v[62:65], v[142:145], v[166:169], v[62:65]
	v_mfma_f32_16x16x32_bf16 v[58:61], v[158:161], v[166:169], v[58:61]
	v_mfma_f32_16x16x32_bf16 v[54:57], v[142:145], v[174:177], v[54:57]
	v_mfma_f32_16x16x32_bf16 v[50:53], v[158:161], v[174:177], v[50:53]
	v_mfma_f32_16x16x32_bf16 v[30:33], v[142:145], v[182:185], v[30:33]
	v_mfma_f32_16x16x32_bf16 v[26:29], v[158:161], v[182:185], v[26:29]
	v_mfma_f32_16x16x32_bf16 v[22:25], v[142:145], v[190:193], v[22:25]
	v_mfma_f32_16x16x32_bf16 v[18:21], v[158:161], v[190:193], v[18:21]
	v_mfma_f32_16x16x32_bf16 v[62:65], v[154:157], v[170:173], v[62:65]
	v_mfma_f32_16x16x32_bf16 v[58:61], v[162:165], v[170:173], v[58:61]
	v_mfma_f32_16x16x32_bf16 v[54:57], v[154:157], v[178:181], v[54:57]
	v_mfma_f32_16x16x32_bf16 v[50:53], v[162:165], v[178:181], v[50:53]
	v_mfma_f32_16x16x32_bf16 v[30:33], v[154:157], v[186:189], v[30:33]
	v_mfma_f32_16x16x32_bf16 v[26:29], v[162:165], v[186:189], v[26:29]
	v_mfma_f32_16x16x32_bf16 v[22:25], v[154:157], v[194:197], v[22:25]
	v_mfma_f32_16x16x32_bf16 v[18:21], v[162:165], v[194:197], v[18:21]
	s_setprio 0
	s_barrier
	s_add_u32 s52, s52, 0x100080
	s_addc_u32 s53, s53, 0
	s_add_i32 s54, s54, s18
	s_mov_b32 m0, s54
	s_nop 0
	global_load_lds_dwordx4 v130, s[52:53]
	s_add_i32 m0, s54, 0x2000
	s_nop 0
	global_load_lds_dwordx4 v132, s[52:53]
	s_waitcnt vmcnt(6)
	s_barrier
	s_setprio 1
	v_mfma_f32_16x16x32_bf16 v[46:49], v[198:201], v[166:169], v[46:49]
	v_mfma_f32_16x16x32_bf16 v[42:45], v[206:209], v[166:169], v[42:45]
	v_mfma_f32_16x16x32_bf16 v[38:41], v[198:201], v[174:177], v[38:41]
	v_mfma_f32_16x16x32_bf16 v[34:37], v[206:209], v[174:177], v[34:37]
	v_mfma_f32_16x16x32_bf16 v[14:17], v[198:201], v[182:185], v[14:17]
	v_mfma_f32_16x16x32_bf16 v[10:13], v[206:209], v[182:185], v[10:13]
	v_mfma_f32_16x16x32_bf16 v[6:9], v[198:201], v[190:193], v[6:9]
	v_mfma_f32_16x16x32_bf16 v[2:5], v[206:209], v[190:193], v[2:5]
	v_mfma_f32_16x16x32_bf16 v[46:49], v[202:205], v[170:173], v[46:49]
	v_mfma_f32_16x16x32_bf16 v[42:45], v[210:213], v[170:173], v[42:45]
	v_mfma_f32_16x16x32_bf16 v[38:41], v[202:205], v[178:181], v[38:41]
	v_mfma_f32_16x16x32_bf16 v[34:37], v[210:213], v[178:181], v[34:37]
	v_mfma_f32_16x16x32_bf16 v[14:17], v[202:205], v[186:189], v[14:17]
	v_mfma_f32_16x16x32_bf16 v[10:13], v[210:213], v[186:189], v[10:13]
	v_mfma_f32_16x16x32_bf16 v[6:9], v[202:205], v[194:197], v[6:9]
	v_mfma_f32_16x16x32_bf16 v[2:5], v[210:213], v[194:197], v[2:5]
	s_setprio 0
	s_add_i32 s60, s60, 2
	s_add_u32 s48, s48, 0x100
	s_addc_u32 s49, s49, 0
	s_add_u32 s58, s58, 0x100
	s_addc_u32 s59, s59, 0
	s_cmp_gt_u32 s60, 61
	s_barrier
	s_cbranch_scc0 .LBB0_528

.LBB0_810:
	s_ashr_i32 s9, s8, 31
	s_lshl_b64 s[10:11], s[8:9], 20
	v_readlane_b32 s9, v254, 34
	s_add_u32 s10, s9, s10
	v_readlane_b32 s9, v254, 35
	s_addc_u32 s11, s9, s11
	s_and_b64 s[14:15], s[14:15], exec
	s_cselect_b32 s9, s11, s13
	s_cselect_b32 s59, s10, s12
	v_mov_b32_e32 v139, v135
	v_mov_b32_e32 v141, v135
	s_add_u32 s60, s12, 0x100
	v_mov_b32_e32 v2, 0
	v_lshl_add_u64 v[142:143], s[6:7], 0, v[140:141]
	v_lshl_add_u64 v[144:145], s[6:7], 0, v[138:139]
	s_addc_u32 s61, s13, 0
	s_mov_b32 s62, -2
	s_mov_b64 s[12:13], 0
	s_add_u32 s14, s28, s12
	s_addc_u32 s15, s29, s13
	s_add_u32 s16, s14, 0x2a300100
	ds_read_b128 v[160:163], v152
	ds_read_b128 v[164:167], v152 offset:1024
	ds_read_b128 v[168:171], v152 offset:2048
	ds_read_b128 v[172:175], v152 offset:3072
	s_addc_u32 s17, s15, 0
	s_add_u32 s63, s60, s12
	s_addc_u32 s64, s61, s13
	s_cmpk_eq_i32 s12, 0xf00
	s_cselect_b64 vcc, -1, 0
	s_and_b64 s[14:15], vcc, exec
	v_cndmask_b32_e32 v134, v137, v155, vcc
	v_cndmask_b32_e32 v216, v136, v156, vcc
	v_cndmask_b32_e32 v1, v138, v157, vcc
	v_cndmask_b32_e32 v139, v140, v158, vcc
	s_cselect_b32 s17, s37, s17
	s_cselect_b32 s16, s36, s16
	s_cselect_b32 s15, s9, s64
	s_cselect_b32 s14, s59, s63
	v_lshl_add_u64 v[208:209], v[144:145], 0, s[12:13]
	s_add_i32 m0, s26, 0xc000
	ds_read_b128 v[176:179], v153
	ds_read_b128 v[180:183], v153 offset:1024
	ds_read_b128 v[184:187], v153 offset:2048
	ds_read_b128 v[188:191], v153 offset:3072
	ds_read_b128 v[192:195], v153 offset:4096
	ds_read_b128 v[196:199], v153 offset:5120
	ds_read_b128 v[200:203], v153 offset:6144
	ds_read_b128 v[204:207], v153 offset:7168
	global_load_lds_dwordx4 v[208:209], off
	v_lshl_add_u64 v[208:209], v[142:143], 0, s[12:13]
	s_add_i32 m0, s26, 0xe000
	s_nop 0
	global_load_lds_dwordx4 v[208:209], off
	s_waitcnt lgkmcnt(8)
	s_barrier
	s_waitcnt lgkmcnt(0)
	s_setprio 1
	s_waitcnt lgkmcnt(0)
	v_mfma_f32_16x16x32_bf16 v[126:129], v[160:163], v[176:179], 0
	v_mfma_f32_16x16x32_bf16 v[122:125], v[168:171], v[176:179], 0
	v_mfma_f32_16x16x32_bf16 v[110:113], v[160:163], v[184:187], 0
	v_mfma_f32_16x16x32_bf16 v[106:109], v[168:171], v[184:187], 0
	v_mfma_f32_16x16x32_bf16 v[94:97], v[160:163], v[192:195], 0
	v_mfma_f32_16x16x32_bf16 v[90:93], v[168:171], v[192:195], 0
	v_mfma_f32_16x16x32_bf16 v[78:81], v[160:163], v[200:203], 0
	v_mfma_f32_16x16x32_bf16 v[74:77], v[168:171], v[200:203], 0
	v_mfma_f32_16x16x32_bf16 v[126:129], v[164:167], v[180:183], v[126:129]
	v_mfma_f32_16x16x32_bf16 v[122:125], v[172:175], v[180:183], v[122:125]
	v_mfma_f32_16x16x32_bf16 v[110:113], v[164:167], v[188:191], v[110:113]
	v_mfma_f32_16x16x32_bf16 v[106:109], v[172:175], v[188:191], v[106:109]
	v_mfma_f32_16x16x32_bf16 v[94:97], v[164:167], v[196:199], v[94:97]
	v_mfma_f32_16x16x32_bf16 v[90:93], v[172:175], v[196:199], v[90:93]
	v_mfma_f32_16x16x32_bf16 v[78:81], v[164:167], v[204:207], v[78:81]
	v_mfma_f32_16x16x32_bf16 v[74:77], v[172:175], v[204:207], v[74:77]
	s_setprio 0
	s_barrier
	s_add_i32 s63, s41, s25
	v_lshl_add_u64 v[228:229], s[14:15], 0, v[132:133]
	s_mov_b32 m0, s63
	ds_read_b128 v[208:211], v154
	ds_read_b128 v[212:215], v154 offset:1024
	ds_read_b128 v[220:223], v154 offset:2048
	ds_read_b128 v[224:227], v154 offset:3072
	global_load_lds_dwordx4 v[228:229], off
	v_lshl_add_u64 v[230:231], s[14:15], 0, v[130:131]
	s_add_i32 m0, s63, 0x2000
	s_nop 0
	global_load_lds_dwordx4 v[230:231], off
	s_barrier
	s_waitcnt lgkmcnt(0)
	s_setprio 1
	s_waitcnt lgkmcnt(0)
	v_mfma_f32_16x16x32_bf16 v[118:121], v[208:211], v[176:179], 0
	v_mfma_f32_16x16x32_bf16 v[114:117], v[220:223], v[176:179], 0
	v_mfma_f32_16x16x32_bf16 v[102:105], v[208:211], v[184:187], 0
	v_mfma_f32_16x16x32_bf16 v[98:101], v[220:223], v[184:187], 0
	v_mfma_f32_16x16x32_bf16 v[86:89], v[208:211], v[192:195], 0
	v_mfma_f32_16x16x32_bf16 v[82:85], v[220:223], v[192:195], 0
	v_mfma_f32_16x16x32_bf16 v[70:73], v[208:211], v[200:203], 0
	v_mfma_f32_16x16x32_bf16 v[66:69], v[220:223], v[200:203], 0
	v_mfma_f32_16x16x32_bf16 v[118:121], v[212:215], v[180:183], v[118:121]
	v_mfma_f32_16x16x32_bf16 v[114:117], v[224:227], v[180:183], v[114:117]
	v_mfma_f32_16x16x32_bf16 v[102:105], v[212:215], v[188:191], v[102:105]
	v_mfma_f32_16x16x32_bf16 v[98:101], v[224:227], v[188:191], v[98:101]
	v_mfma_f32_16x16x32_bf16 v[86:89], v[212:215], v[196:199], v[86:89]
	v_mfma_f32_16x16x32_bf16 v[82:85], v[224:227], v[196:199], v[82:85]
	v_mfma_f32_16x16x32_bf16 v[70:73], v[212:215], v[204:207], v[70:73]
	v_mfma_f32_16x16x32_bf16 v[66:69], v[224:227], v[204:207], v[66:69]
	s_setprio 0
	s_mov_b32 m0, s26
	s_barrier
	ds_read_b128 v[176:179], v153 offset:16384
	ds_read_b128 v[180:183], v153 offset:17408
	ds_read_b128 v[184:187], v153 offset:18432
	ds_read_b128 v[188:191], v153 offset:19456
	ds_read_b128 v[192:195], v153 offset:20480
	ds_read_b128 v[196:199], v153 offset:21504
	ds_read_b128 v[200:203], v153 offset:22528
	ds_read_b128 v[204:207], v153 offset:23552
	global_load_lds_dwordx4 v134, s[16:17]
	s_mov_b32 m0, s27
	v_mov_b32_e32 v217, v135
	global_load_lds_dwordx4 v216, s[16:17]
	s_barrier
	s_waitcnt lgkmcnt(0)
	v_lshl_add_u64 v[232:233], s[16:17], 0, v[134:135]
	v_lshl_add_u64 v[216:217], s[16:17], 0, v[216:217]
	s_setprio 1
	s_waitcnt lgkmcnt(0)
	v_mfma_f32_16x16x32_bf16 v[62:65], v[160:163], v[176:179], 0
	v_mfma_f32_16x16x32_bf16 v[58:61], v[168:171], v[176:179], 0
	v_mfma_f32_16x16x32_bf16 v[46:49], v[160:163], v[184:187], 0
	v_mfma_f32_16x16x32_bf16 v[42:45], v[168:171], v[184:187], 0
	v_mfma_f32_16x16x32_bf16 v[30:33], v[160:163], v[192:195], 0
	v_mfma_f32_16x16x32_bf16 v[26:29], v[168:171], v[192:195], 0
	v_mfma_f32_16x16x32_bf16 v[14:17], v[160:163], v[200:203], 0
	v_mfma_f32_16x16x32_bf16 v[10:13], v[168:171], v[200:203], 0
	v_mfma_f32_16x16x32_bf16 v[62:65], v[164:167], v[180:183], v[62:65]
	v_mfma_f32_16x16x32_bf16 v[58:61], v[172:175], v[180:183], v[58:61]
	v_mfma_f32_16x16x32_bf16 v[46:49], v[164:167], v[188:191], v[46:49]
	v_mfma_f32_16x16x32_bf16 v[42:45], v[172:175], v[188:191], v[42:45]
	v_mfma_f32_16x16x32_bf16 v[30:33], v[164:167], v[196:199], v[30:33]
	v_mfma_f32_16x16x32_bf16 v[26:29], v[172:175], v[196:199], v[26:29]
	v_mfma_f32_16x16x32_bf16 v[14:17], v[164:167], v[204:207], v[14:17]
	v_mfma_f32_16x16x32_bf16 v[10:13], v[172:175], v[204:207], v[10:13]
	s_setprio 0
	s_barrier
	s_add_u32 s64, s14, 0x80000
	s_addc_u32 s65, s15, 0
	s_add_i32 s63, s48, s25
	s_mov_b32 m0, s63
	s_nop 0
	global_load_lds_dwordx4 v132, s[64:65]
	s_add_i32 m0, s63, 0x2000
	s_nop 0
	global_load_lds_dwordx4 v130, s[64:65]
	s_waitcnt vmcnt(6)
	s_barrier
	s_setprio 1
	v_mfma_f32_16x16x32_bf16 v[54:57], v[208:211], v[176:179], 0
	v_mfma_f32_16x16x32_bf16 v[50:53], v[220:223], v[176:179], 0
	v_mfma_f32_16x16x32_bf16 v[38:41], v[208:211], v[184:187], 0
	v_mfma_f32_16x16x32_bf16 v[34:37], v[220:223], v[184:187], 0
	v_mfma_f32_16x16x32_bf16 v[22:25], v[208:211], v[192:195], 0
	v_mfma_f32_16x16x32_bf16 v[18:21], v[220:223], v[192:195], 0
	v_mfma_f32_16x16x32_bf16 v[6:9], v[208:211], v[200:203], 0
	v_mfma_f32_16x16x32_bf16 v[2:5], v[220:223], v[200:203], 0
	v_mfma_f32_16x16x32_bf16 v[54:57], v[212:215], v[180:183], v[54:57]
	v_mfma_f32_16x16x32_bf16 v[50:53], v[224:227], v[180:183], v[50:53]
	v_mfma_f32_16x16x32_bf16 v[38:41], v[212:215], v[188:191], v[38:41]
	v_mfma_f32_16x16x32_bf16 v[34:37], v[224:227], v[188:191], v[34:37]
	v_mfma_f32_16x16x32_bf16 v[22:25], v[212:215], v[196:199], v[22:25]
	v_mfma_f32_16x16x32_bf16 v[18:21], v[224:227], v[196:199], v[18:21]
	v_mfma_f32_16x16x32_bf16 v[6:9], v[212:215], v[204:207], v[6:9]
	v_mfma_f32_16x16x32_bf16 v[2:5], v[224:227], v[204:207], v[2:5]
	s_setprio 0
	s_add_i32 s63, 0, 0x18000
	v_add_u32_e32 v134, s63, v150
	s_barrier
	ds_read_b128 v[160:163], v134
	ds_read_b128 v[164:167], v134 offset:1024
	ds_read_b128 v[168:171], v134 offset:2048
	ds_read_b128 v[172:175], v134 offset:3072
	s_mov_b32 m0, s33
	ds_read_b128 v[176:179], v153 offset:32768
	ds_read_b128 v[180:183], v153 offset:33792
	ds_read_b128 v[184:187], v153 offset:34816
	ds_read_b128 v[188:191], v153 offset:35840
	ds_read_b128 v[192:195], v153 offset:36864
	ds_read_b128 v[196:199], v153 offset:37888
	ds_read_b128 v[200:203], v153 offset:38912
	ds_read_b128 v[204:207], v153 offset:39936
	global_load_lds_dwordx4 v1, s[16:17]
	s_mov_b32 m0, s34
	s_nop 0
	global_load_lds_dwordx4 v139, s[16:17]
	s_waitcnt lgkmcnt(8)
	s_barrier
	s_waitcnt lgkmcnt(0)
	s_setprio 1
	s_waitcnt lgkmcnt(0)
	v_mfma_f32_16x16x32_bf16 v[126:129], v[160:163], v[176:179], v[126:129]
	v_mfma_f32_16x16x32_bf16 v[122:125], v[168:171], v[176:179], v[122:125]
	v_mfma_f32_16x16x32_bf16 v[110:113], v[160:163], v[184:187], v[110:113]
	v_mfma_f32_16x16x32_bf16 v[106:109], v[168:171], v[184:187], v[106:109]
	v_mfma_f32_16x16x32_bf16 v[94:97], v[160:163], v[192:195], v[94:97]
	v_mfma_f32_16x16x32_bf16 v[90:93], v[168:171], v[192:195], v[90:93]
	v_mfma_f32_16x16x32_bf16 v[78:81], v[160:163], v[200:203], v[78:81]
	v_mfma_f32_16x16x32_bf16 v[74:77], v[168:171], v[200:203], v[74:77]
	v_mfma_f32_16x16x32_bf16 v[126:129], v[164:167], v[180:183], v[126:129]
	v_mfma_f32_16x16x32_bf16 v[122:125], v[172:175], v[180:183], v[122:125]
	v_mfma_f32_16x16x32_bf16 v[110:113], v[164:167], v[188:191], v[110:113]
	v_mfma_f32_16x16x32_bf16 v[106:109], v[172:175], v[188:191], v[106:109]
	v_mfma_f32_16x16x32_bf16 v[94:97], v[164:167], v[196:199], v[94:97]
	v_mfma_f32_16x16x32_bf16 v[90:93], v[172:175], v[196:199], v[90:93]
	v_mfma_f32_16x16x32_bf16 v[78:81], v[164:167], v[204:207], v[78:81]
	v_mfma_f32_16x16x32_bf16 v[74:77], v[172:175], v[204:207], v[74:77]
	s_setprio 0
	s_barrier
	s_add_i32 s16, 0, 0x1c000
	s_add_i32 s17, s63, s25
	v_add_u32_e32 v1, s16, v150
	v_lshl_add_u64 v[228:229], v[228:229], 0, s[0:1]
	s_mov_b32 m0, s17
	ds_read_b128 v[208:211], v1
	ds_read_b128 v[212:215], v1 offset:1024
	ds_read_b128 v[220:223], v1 offset:2048
	ds_read_b128 v[224:227], v1 offset:3072
	global_load_lds_dwordx4 v[228:229], off
	v_lshl_add_u64 v[228:229], v[230:231], 0, s[0:1]
	s_add_i32 m0, s17, 0x2000
	s_nop 0
	global_load_lds_dwordx4 v[228:229], off
	s_barrier
	s_waitcnt lgkmcnt(0)
	s_setprio 1
	s_waitcnt lgkmcnt(0)
	v_mfma_f32_16x16x32_bf16 v[118:121], v[208:211], v[176:179], v[118:121]
	v_mfma_f32_16x16x32_bf16 v[114:117], v[220:223], v[176:179], v[114:117]
	v_mfma_f32_16x16x32_bf16 v[102:105], v[208:211], v[184:187], v[102:105]
	v_mfma_f32_16x16x32_bf16 v[98:101], v[220:223], v[184:187], v[98:101]
	v_mfma_f32_16x16x32_bf16 v[86:89], v[208:211], v[192:195], v[86:89]
	v_mfma_f32_16x16x32_bf16 v[82:85], v[220:223], v[192:195], v[82:85]
	v_mfma_f32_16x16x32_bf16 v[70:73], v[208:211], v[200:203], v[70:73]
	v_mfma_f32_16x16x32_bf16 v[66:69], v[220:223], v[200:203], v[66:69]
	v_mfma_f32_16x16x32_bf16 v[118:121], v[212:215], v[180:183], v[118:121]
	v_mfma_f32_16x16x32_bf16 v[114:117], v[224:227], v[180:183], v[114:117]
	v_mfma_f32_16x16x32_bf16 v[102:105], v[212:215], v[188:191], v[102:105]
	v_mfma_f32_16x16x32_bf16 v[98:101], v[224:227], v[188:191], v[98:101]
	v_mfma_f32_16x16x32_bf16 v[86:89], v[212:215], v[196:199], v[86:89]
	v_mfma_f32_16x16x32_bf16 v[82:85], v[224:227], v[196:199], v[82:85]
	v_mfma_f32_16x16x32_bf16 v[70:73], v[212:215], v[204:207], v[70:73]
	v_mfma_f32_16x16x32_bf16 v[66:69], v[224:227], v[204:207], v[66:69]
	s_setprio 0
	s_mov_b32 m0, s35
	v_lshl_add_u64 v[228:229], v[232:233], 0, s[0:1]
	s_barrier
	ds_read_b128 v[176:179], v153 offset:49152
	ds_read_b128 v[180:183], v153 offset:50176
	ds_read_b128 v[184:187], v153 offset:51200
	ds_read_b128 v[188:191], v153 offset:52224
	ds_read_b128 v[192:195], v153 offset:53248
	ds_read_b128 v[196:199], v153 offset:54272
	ds_read_b128 v[200:203], v153 offset:55296
	ds_read_b128 v[204:207], v153 offset:56320
	global_load_lds_dwordx4 v[228:229], off
	v_lshl_add_u64 v[216:217], v[216:217], 0, s[0:1]
	s_mov_b32 m0, s40
	s_nop 0
	global_load_lds_dwordx4 v[216:217], off
	s_barrier
	s_waitcnt lgkmcnt(0)
	s_setprio 1
	s_waitcnt lgkmcnt(0)
	v_mfma_f32_16x16x32_bf16 v[62:65], v[160:163], v[176:179], v[62:65]
	v_mfma_f32_16x16x32_bf16 v[58:61], v[168:171], v[176:179], v[58:61]
	v_mfma_f32_16x16x32_bf16 v[46:49], v[160:163], v[184:187], v[46:49]
	v_mfma_f32_16x16x32_bf16 v[42:45], v[168:171], v[184:187], v[42:45]
	v_mfma_f32_16x16x32_bf16 v[30:33], v[160:163], v[192:195], v[30:33]
	v_mfma_f32_16x16x32_bf16 v[26:29], v[168:171], v[192:195], v[26:29]
	v_mfma_f32_16x16x32_bf16 v[14:17], v[160:163], v[200:203], v[14:17]
	v_mfma_f32_16x16x32_bf16 v[10:13], v[168:171], v[200:203], v[10:13]
	v_mfma_f32_16x16x32_bf16 v[62:65], v[164:167], v[180:183], v[62:65]
	v_mfma_f32_16x16x32_bf16 v[58:61], v[172:175], v[180:183], v[58:61]
	v_mfma_f32_16x16x32_bf16 v[46:49], v[164:167], v[188:191], v[46:49]
	v_mfma_f32_16x16x32_bf16 v[42:45], v[172:175], v[188:191], v[42:45]
	v_mfma_f32_16x16x32_bf16 v[30:33], v[164:167], v[196:199], v[30:33]
	v_mfma_f32_16x16x32_bf16 v[26:29], v[172:175], v[196:199], v[26:29]
	v_mfma_f32_16x16x32_bf16 v[14:17], v[164:167], v[204:207], v[14:17]
	v_mfma_f32_16x16x32_bf16 v[10:13], v[172:175], v[204:207], v[10:13]
	s_setprio 0
	s_barrier
	s_add_u32 s14, s14, 0x80080
	s_addc_u32 s15, s15, 0
	s_add_i32 s16, s16, s25
	s_mov_b32 m0, s16
	s_nop 0
	global_load_lds_dwordx4 v132, s[14:15]
	s_add_i32 m0, s16, 0x2000
	s_nop 0
	global_load_lds_dwordx4 v130, s[14:15]
	s_waitcnt vmcnt(6)
	s_barrier
	s_setprio 1
	v_mfma_f32_16x16x32_bf16 v[54:57], v[208:211], v[176:179], v[54:57]
	v_mfma_f32_16x16x32_bf16 v[50:53], v[220:223], v[176:179], v[50:53]
	v_mfma_f32_16x16x32_bf16 v[38:41], v[208:211], v[184:187], v[38:41]
	v_mfma_f32_16x16x32_bf16 v[34:37], v[220:223], v[184:187], v[34:37]
	v_mfma_f32_16x16x32_bf16 v[22:25], v[208:211], v[192:195], v[22:25]
	v_mfma_f32_16x16x32_bf16 v[18:21], v[220:223], v[192:195], v[18:21]
	v_mfma_f32_16x16x32_bf16 v[6:9], v[208:211], v[200:203], v[6:9]
	v_mfma_f32_16x16x32_bf16 v[2:5], v[220:223], v[200:203], v[2:5]
	v_mfma_f32_16x16x32_bf16 v[54:57], v[212:215], v[180:183], v[54:57]
	v_mfma_f32_16x16x32_bf16 v[50:53], v[224:227], v[180:183], v[50:53]
	v_mfma_f32_16x16x32_bf16 v[38:41], v[212:215], v[188:191], v[38:41]
	v_mfma_f32_16x16x32_bf16 v[34:37], v[224:227], v[188:191], v[34:37]
	v_mfma_f32_16x16x32_bf16 v[22:25], v[212:215], v[196:199], v[22:25]
	v_mfma_f32_16x16x32_bf16 v[18:21], v[224:227], v[196:199], v[18:21]
	v_mfma_f32_16x16x32_bf16 v[6:9], v[212:215], v[204:207], v[6:9]
	v_mfma_f32_16x16x32_bf16 v[2:5], v[224:227], v[204:207], v[2:5]
	s_setprio 0
	s_add_i32 s62, s62, 2
	s_add_u32 s12, s12, 0x100
	s_addc_u32 s13, s13, 0
	s_cmp_gt_u32 s62, 29
	s_barrier
	s_cbranch_scc1 .Lpeel_811_after
.LBB0_811:
	s_add_u32 s14, s28, s12
	s_addc_u32 s15, s29, s13
	s_add_u32 s16, s14, 0x2a300100
	ds_read_b128 v[160:163], v152
	ds_read_b128 v[164:167], v152 offset:1024
	ds_read_b128 v[168:171], v152 offset:2048
	ds_read_b128 v[172:175], v152 offset:3072
	s_addc_u32 s17, s15, 0
	s_add_u32 s63, s60, s12
	s_addc_u32 s64, s61, s13
	s_cmpk_eq_i32 s12, 0xf00
	s_cselect_b64 vcc, -1, 0
	s_and_b64 s[14:15], vcc, exec
	v_cndmask_b32_e32 v134, v137, v155, vcc
	v_cndmask_b32_e32 v216, v136, v156, vcc
	v_cndmask_b32_e32 v1, v138, v157, vcc
	v_cndmask_b32_e32 v139, v140, v158, vcc
	s_cselect_b32 s17, s37, s17
	s_cselect_b32 s16, s36, s16
	s_cselect_b32 s15, s9, s64
	s_cselect_b32 s14, s59, s63
	v_lshl_add_u64 v[208:209], v[144:145], 0, s[12:13]
	s_add_i32 m0, s26, 0xc000
	ds_read_b128 v[176:179], v153
	ds_read_b128 v[180:183], v153 offset:1024
	ds_read_b128 v[184:187], v153 offset:2048
	ds_read_b128 v[188:191], v153 offset:3072
	ds_read_b128 v[192:195], v153 offset:4096
	ds_read_b128 v[196:199], v153 offset:5120
	ds_read_b128 v[200:203], v153 offset:6144
	ds_read_b128 v[204:207], v153 offset:7168
	global_load_lds_dwordx4 v[208:209], off
	v_lshl_add_u64 v[208:209], v[142:143], 0, s[12:13]
	s_add_i32 m0, s26, 0xe000
	s_nop 0
	global_load_lds_dwordx4 v[208:209], off
	s_waitcnt lgkmcnt(8)
	s_barrier
	s_waitcnt lgkmcnt(0)
	s_setprio 1
	s_waitcnt lgkmcnt(0)
	v_mfma_f32_16x16x32_bf16 v[126:129], v[160:163], v[176:179], v[126:129]
	v_mfma_f32_16x16x32_bf16 v[122:125], v[168:171], v[176:179], v[122:125]
	v_mfma_f32_16x16x32_bf16 v[110:113], v[160:163], v[184:187], v[110:113]
	v_mfma_f32_16x16x32_bf16 v[106:109], v[168:171], v[184:187], v[106:109]
	v_mfma_f32_16x16x32_bf16 v[94:97], v[160:163], v[192:195], v[94:97]
	v_mfma_f32_16x16x32_bf16 v[90:93], v[168:171], v[192:195], v[90:93]
	v_mfma_f32_16x16x32_bf16 v[78:81], v[160:163], v[200:203], v[78:81]
	v_mfma_f32_16x16x32_bf16 v[74:77], v[168:171], v[200:203], v[74:77]
	v_mfma_f32_16x16x32_bf16 v[126:129], v[164:167], v[180:183], v[126:129]
	v_mfma_f32_16x16x32_bf16 v[122:125], v[172:175], v[180:183], v[122:125]
	v_mfma_f32_16x16x32_bf16 v[110:113], v[164:167], v[188:191], v[110:113]
	v_mfma_f32_16x16x32_bf16 v[106:109], v[172:175], v[188:191], v[106:109]
	v_mfma_f32_16x16x32_bf16 v[94:97], v[164:167], v[196:199], v[94:97]
	v_mfma_f32_16x16x32_bf16 v[90:93], v[172:175], v[196:199], v[90:93]
	v_mfma_f32_16x16x32_bf16 v[78:81], v[164:167], v[204:207], v[78:81]
	v_mfma_f32_16x16x32_bf16 v[74:77], v[172:175], v[204:207], v[74:77]
	s_setprio 0
	s_barrier
	s_add_i32 s63, s41, s25
	v_lshl_add_u64 v[228:229], s[14:15], 0, v[132:133]
	s_mov_b32 m0, s63
	ds_read_b128 v[208:211], v154
	ds_read_b128 v[212:215], v154 offset:1024
	ds_read_b128 v[220:223], v154 offset:2048
	ds_read_b128 v[224:227], v154 offset:3072
	global_load_lds_dwordx4 v[228:229], off
	v_lshl_add_u64 v[230:231], s[14:15], 0, v[130:131]
	s_add_i32 m0, s63, 0x2000
	s_nop 0
	global_load_lds_dwordx4 v[230:231], off
	s_barrier
	s_waitcnt lgkmcnt(0)
	s_setprio 1
	s_waitcnt lgkmcnt(0)
	v_mfma_f32_16x16x32_bf16 v[118:121], v[208:211], v[176:179], v[118:121]
	v_mfma_f32_16x16x32_bf16 v[114:117], v[220:223], v[176:179], v[114:117]
	v_mfma_f32_16x16x32_bf16 v[102:105], v[208:211], v[184:187], v[102:105]
	v_mfma_f32_16x16x32_bf16 v[98:101], v[220:223], v[184:187], v[98:101]
	v_mfma_f32_16x16x32_bf16 v[86:89], v[208:211], v[192:195], v[86:89]
	v_mfma_f32_16x16x32_bf16 v[82:85], v[220:223], v[192:195], v[82:85]
	v_mfma_f32_16x16x32_bf16 v[70:73], v[208:211], v[200:203], v[70:73]
	v_mfma_f32_16x16x32_bf16 v[66:69], v[220:223], v[200:203], v[66:69]
	v_mfma_f32_16x16x32_bf16 v[118:121], v[212:215], v[180:183], v[118:121]
	v_mfma_f32_16x16x32_bf16 v[114:117], v[224:227], v[180:183], v[114:117]
	v_mfma_f32_16x16x32_bf16 v[102:105], v[212:215], v[188:191], v[102:105]
	v_mfma_f32_16x16x32_bf16 v[98:101], v[224:227], v[188:191], v[98:101]
	v_mfma_f32_16x16x32_bf16 v[86:89], v[212:215], v[196:199], v[86:89]
	v_mfma_f32_16x16x32_bf16 v[82:85], v[224:227], v[196:199], v[82:85]
	v_mfma_f32_16x16x32_bf16 v[70:73], v[212:215], v[204:207], v[70:73]
	v_mfma_f32_16x16x32_bf16 v[66:69], v[224:227], v[204:207], v[66:69]
	s_setprio 0
	s_mov_b32 m0, s26
	s_barrier
	ds_read_b128 v[176:179], v153 offset:16384
	ds_read_b128 v[180:183], v153 offset:17408
	ds_read_b128 v[184:187], v153 offset:18432
	ds_read_b128 v[188:191], v153 offset:19456
	ds_read_b128 v[192:195], v153 offset:20480
	ds_read_b128 v[196:199], v153 offset:21504
	ds_read_b128 v[200:203], v153 offset:22528
	ds_read_b128 v[204:207], v153 offset:23552
	global_load_lds_dwordx4 v134, s[16:17]
	s_mov_b32 m0, s27
	v_mov_b32_e32 v217, v135
	global_load_lds_dwordx4 v216, s[16:17]
	s_barrier
	s_waitcnt lgkmcnt(0)
	v_lshl_add_u64 v[232:233], s[16:17], 0, v[134:135]
	v_lshl_add_u64 v[216:217], s[16:17], 0, v[216:217]
	s_setprio 1
	s_waitcnt lgkmcnt(0)
	v_mfma_f32_16x16x32_bf16 v[62:65], v[160:163], v[176:179], v[62:65]
	v_mfma_f32_16x16x32_bf16 v[58:61], v[168:171], v[176:179], v[58:61]
	v_mfma_f32_16x16x32_bf16 v[46:49], v[160:163], v[184:187], v[46:49]
	v_mfma_f32_16x16x32_bf16 v[42:45], v[168:171], v[184:187], v[42:45]
	v_mfma_f32_16x16x32_bf16 v[30:33], v[160:163], v[192:195], v[30:33]
	v_mfma_f32_16x16x32_bf16 v[26:29], v[168:171], v[192:195], v[26:29]
	v_mfma_f32_16x16x32_bf16 v[14:17], v[160:163], v[200:203], v[14:17]
	v_mfma_f32_16x16x32_bf16 v[10:13], v[168:171], v[200:203], v[10:13]
	v_mfma_f32_16x16x32_bf16 v[62:65], v[164:167], v[180:183], v[62:65]
	v_mfma_f32_16x16x32_bf16 v[58:61], v[172:175], v[180:183], v[58:61]
	v_mfma_f32_16x16x32_bf16 v[46:49], v[164:167], v[188:191], v[46:49]
	v_mfma_f32_16x16x32_bf16 v[42:45], v[172:175], v[188:191], v[42:45]
	v_mfma_f32_16x16x32_bf16 v[30:33], v[164:167], v[196:199], v[30:33]
	v_mfma_f32_16x16x32_bf16 v[26:29], v[172:175], v[196:199], v[26:29]
	v_mfma_f32_16x16x32_bf16 v[14:17], v[164:167], v[204:207], v[14:17]
	v_mfma_f32_16x16x32_bf16 v[10:13], v[172:175], v[204:207], v[10:13]
	s_setprio 0
	s_barrier
	s_add_u32 s64, s14, 0x80000
	s_addc_u32 s65, s15, 0
	s_add_i32 s63, s48, s25
	s_mov_b32 m0, s63
	s_nop 0
	global_load_lds_dwordx4 v132, s[64:65]
	s_add_i32 m0, s63, 0x2000
	s_nop 0
	global_load_lds_dwordx4 v130, s[64:65]
	s_waitcnt vmcnt(6)
	s_barrier
	s_setprio 1
	v_mfma_f32_16x16x32_bf16 v[54:57], v[208:211], v[176:179], v[54:57]
	v_mfma_f32_16x16x32_bf16 v[50:53], v[220:223], v[176:179], v[50:53]
	v_mfma_f32_16x16x32_bf16 v[38:41], v[208:211], v[184:187], v[38:41]
	v_mfma_f32_16x16x32_bf16 v[34:37], v[220:223], v[184:187], v[34:37]
	v_mfma_f32_16x16x32_bf16 v[22:25], v[208:211], v[192:195], v[22:25]
	v_mfma_f32_16x16x32_bf16 v[18:21], v[220:223], v[192:195], v[18:21]
	v_mfma_f32_16x16x32_bf16 v[6:9], v[208:211], v[200:203], v[6:9]
	v_mfma_f32_16x16x32_bf16 v[2:5], v[220:223], v[200:203], v[2:5]
	v_mfma_f32_16x16x32_bf16 v[54:57], v[212:215], v[180:183], v[54:57]
	v_mfma_f32_16x16x32_bf16 v[50:53], v[224:227], v[180:183], v[50:53]
	v_mfma_f32_16x16x32_bf16 v[38:41], v[212:215], v[188:191], v[38:41]
	v_mfma_f32_16x16x32_bf16 v[34:37], v[224:227], v[188:191], v[34:37]
	v_mfma_f32_16x16x32_bf16 v[22:25], v[212:215], v[196:199], v[22:25]
	v_mfma_f32_16x16x32_bf16 v[18:21], v[224:227], v[196:199], v[18:21]
	v_mfma_f32_16x16x32_bf16 v[6:9], v[212:215], v[204:207], v[6:9]
	v_mfma_f32_16x16x32_bf16 v[2:5], v[224:227], v[204:207], v[2:5]
	s_setprio 0
	s_add_i32 s63, 0, 0x18000
	v_add_u32_e32 v134, s63, v150
	s_barrier
	ds_read_b128 v[160:163], v134
	ds_read_b128 v[164:167], v134 offset:1024
	ds_read_b128 v[168:171], v134 offset:2048
	ds_read_b128 v[172:175], v134 offset:3072
	s_mov_b32 m0, s33
	ds_read_b128 v[176:179], v153 offset:32768
	ds_read_b128 v[180:183], v153 offset:33792
	ds_read_b128 v[184:187], v153 offset:34816
	ds_read_b128 v[188:191], v153 offset:35840
	ds_read_b128 v[192:195], v153 offset:36864
	ds_read_b128 v[196:199], v153 offset:37888
	ds_read_b128 v[200:203], v153 offset:38912
	ds_read_b128 v[204:207], v153 offset:39936
	global_load_lds_dwordx4 v1, s[16:17]
	s_mov_b32 m0, s34
	s_nop 0
	global_load_lds_dwordx4 v139, s[16:17]
	s_waitcnt lgkmcnt(8)
	s_barrier
	s_waitcnt lgkmcnt(0)
	s_setprio 1
	s_waitcnt lgkmcnt(0)
	v_mfma_f32_16x16x32_bf16 v[126:129], v[160:163], v[176:179], v[126:129]
	v_mfma_f32_16x16x32_bf16 v[122:125], v[168:171], v[176:179], v[122:125]
	v_mfma_f32_16x16x32_bf16 v[110:113], v[160:163], v[184:187], v[110:113]
	v_mfma_f32_16x16x32_bf16 v[106:109], v[168:171], v[184:187], v[106:109]
	v_mfma_f32_16x16x32_bf16 v[94:97], v[160:163], v[192:195], v[94:97]
	v_mfma_f32_16x16x32_bf16 v[90:93], v[168:171], v[192:195], v[90:93]
	v_mfma_f32_16x16x32_bf16 v[78:81], v[160:163], v[200:203], v[78:81]
	v_mfma_f32_16x16x32_bf16 v[74:77], v[168:171], v[200:203], v[74:77]
	v_mfma_f32_16x16x32_bf16 v[126:129], v[164:167], v[180:183], v[126:129]
	v_mfma_f32_16x16x32_bf16 v[122:125], v[172:175], v[180:183], v[122:125]
	v_mfma_f32_16x16x32_bf16 v[110:113], v[164:167], v[188:191], v[110:113]
	v_mfma_f32_16x16x32_bf16 v[106:109], v[172:175], v[188:191], v[106:109]
	v_mfma_f32_16x16x32_bf16 v[94:97], v[164:167], v[196:199], v[94:97]
	v_mfma_f32_16x16x32_bf16 v[90:93], v[172:175], v[196:199], v[90:93]
	v_mfma_f32_16x16x32_bf16 v[78:81], v[164:167], v[204:207], v[78:81]
	v_mfma_f32_16x16x32_bf16 v[74:77], v[172:175], v[204:207], v[74:77]
	s_setprio 0
	s_barrier
	s_add_i32 s16, 0, 0x1c000
	s_add_i32 s17, s63, s25
	v_add_u32_e32 v1, s16, v150
	v_lshl_add_u64 v[228:229], v[228:229], 0, s[0:1]
	s_mov_b32 m0, s17
	ds_read_b128 v[208:211], v1
	ds_read_b128 v[212:215], v1 offset:1024
	ds_read_b128 v[220:223], v1 offset:2048
	ds_read_b128 v[224:227], v1 offset:3072
	global_load_lds_dwordx4 v[228:229], off
	v_lshl_add_u64 v[228:229], v[230:231], 0, s[0:1]
	s_add_i32 m0, s17, 0x2000
	s_nop 0
	global_load_lds_dwordx4 v[228:229], off
	s_barrier
	s_waitcnt lgkmcnt(0)
	s_setprio 1
	s_waitcnt lgkmcnt(0)
	v_mfma_f32_16x16x32_bf16 v[118:121], v[208:211], v[176:179], v[118:121]
	v_mfma_f32_16x16x32_bf16 v[114:117], v[220:223], v[176:179], v[114:117]
	v_mfma_f32_16x16x32_bf16 v[102:105], v[208:211], v[184:187], v[102:105]
	v_mfma_f32_16x16x32_bf16 v[98:101], v[220:223], v[184:187], v[98:101]
	v_mfma_f32_16x16x32_bf16 v[86:89], v[208:211], v[192:195], v[86:89]
	v_mfma_f32_16x16x32_bf16 v[82:85], v[220:223], v[192:195], v[82:85]
	v_mfma_f32_16x16x32_bf16 v[70:73], v[208:211], v[200:203], v[70:73]
	v_mfma_f32_16x16x32_bf16 v[66:69], v[220:223], v[200:203], v[66:69]
	v_mfma_f32_16x16x32_bf16 v[118:121], v[212:215], v[180:183], v[118:121]
	v_mfma_f32_16x16x32_bf16 v[114:117], v[224:227], v[180:183], v[114:117]
	v_mfma_f32_16x16x32_bf16 v[102:105], v[212:215], v[188:191], v[102:105]
	v_mfma_f32_16x16x32_bf16 v[98:101], v[224:227], v[188:191], v[98:101]
	v_mfma_f32_16x16x32_bf16 v[86:89], v[212:215], v[196:199], v[86:89]
	v_mfma_f32_16x16x32_bf16 v[82:85], v[224:227], v[196:199], v[82:85]
	v_mfma_f32_16x16x32_bf16 v[70:73], v[212:215], v[204:207], v[70:73]
	v_mfma_f32_16x16x32_bf16 v[66:69], v[224:227], v[204:207], v[66:69]
	s_setprio 0
	s_mov_b32 m0, s35
	v_lshl_add_u64 v[228:229], v[232:233], 0, s[0:1]
	s_barrier
	ds_read_b128 v[176:179], v153 offset:49152
	ds_read_b128 v[180:183], v153 offset:50176
	ds_read_b128 v[184:187], v153 offset:51200
	ds_read_b128 v[188:191], v153 offset:52224
	ds_read_b128 v[192:195], v153 offset:53248
	ds_read_b128 v[196:199], v153 offset:54272
	ds_read_b128 v[200:203], v153 offset:55296
	ds_read_b128 v[204:207], v153 offset:56320
	global_load_lds_dwordx4 v[228:229], off
	v_lshl_add_u64 v[216:217], v[216:217], 0, s[0:1]
	s_mov_b32 m0, s40
	s_nop 0
	global_load_lds_dwordx4 v[216:217], off
	s_barrier
	s_waitcnt lgkmcnt(0)
	s_setprio 1
	s_waitcnt lgkmcnt(0)
	v_mfma_f32_16x16x32_bf16 v[62:65], v[160:163], v[176:179], v[62:65]
	v_mfma_f32_16x16x32_bf16 v[58:61], v[168:171], v[176:179], v[58:61]
	v_mfma_f32_16x16x32_bf16 v[46:49], v[160:163], v[184:187], v[46:49]
	v_mfma_f32_16x16x32_bf16 v[42:45], v[168:171], v[184:187], v[42:45]
	v_mfma_f32_16x16x32_bf16 v[30:33], v[160:163], v[192:195], v[30:33]
	v_mfma_f32_16x16x32_bf16 v[26:29], v[168:171], v[192:195], v[26:29]
	v_mfma_f32_16x16x32_bf16 v[14:17], v[160:163], v[200:203], v[14:17]
	v_mfma_f32_16x16x32_bf16 v[10:13], v[168:171], v[200:203], v[10:13]
	v_mfma_f32_16x16x32_bf16 v[62:65], v[164:167], v[180:183], v[62:65]
	v_mfma_f32_16x16x32_bf16 v[58:61], v[172:175], v[180:183], v[58:61]
	v_mfma_f32_16x16x32_bf16 v[46:49], v[164:167], v[188:191], v[46:49]
	v_mfma_f32_16x16x32_bf16 v[42:45], v[172:175], v[188:191], v[42:45]
	v_mfma_f32_16x16x32_bf16 v[30:33], v[164:167], v[196:199], v[30:33]
	v_mfma_f32_16x16x32_bf16 v[26:29], v[172:175], v[196:199], v[26:29]
	v_mfma_f32_16x16x32_bf16 v[14:17], v[164:167], v[204:207], v[14:17]
	v_mfma_f32_16x16x32_bf16 v[10:13], v[172:175], v[204:207], v[10:13]
	s_setprio 0
	s_barrier
	s_add_u32 s14, s14, 0x80080
	s_addc_u32 s15, s15, 0
	s_add_i32 s16, s16, s25
	s_mov_b32 m0, s16
	s_nop 0
	global_load_lds_dwordx4 v132, s[14:15]
	s_add_i32 m0, s16, 0x2000
	s_nop 0
	global_load_lds_dwordx4 v130, s[14:15]
	s_waitcnt vmcnt(6)
	s_barrier
	s_setprio 1
	v_mfma_f32_16x16x32_bf16 v[54:57], v[208:211], v[176:179], v[54:57]
	v_mfma_f32_16x16x32_bf16 v[50:53], v[220:223], v[176:179], v[50:53]
	v_mfma_f32_16x16x32_bf16 v[38:41], v[208:211], v[184:187], v[38:41]
	v_mfma_f32_16x16x32_bf16 v[34:37], v[220:223], v[184:187], v[34:37]
	v_mfma_f32_16x16x32_bf16 v[22:25], v[208:211], v[192:195], v[22:25]
	v_mfma_f32_16x16x32_bf16 v[18:21], v[220:223], v[192:195], v[18:21]
	v_mfma_f32_16x16x32_bf16 v[6:9], v[208:211], v[200:203], v[6:9]
	v_mfma_f32_16x16x32_bf16 v[2:5], v[220:223], v[200:203], v[2:5]
	v_mfma_f32_16x16x32_bf16 v[54:57], v[212:215], v[180:183], v[54:57]
	v_mfma_f32_16x16x32_bf16 v[50:53], v[224:227], v[180:183], v[50:53]
	v_mfma_f32_16x16x32_bf16 v[38:41], v[212:215], v[188:191], v[38:41]
	v_mfma_f32_16x16x32_bf16 v[34:37], v[224:227], v[188:191], v[34:37]
	v_mfma_f32_16x16x32_bf16 v[22:25], v[212:215], v[196:199], v[22:25]
	v_mfma_f32_16x16x32_bf16 v[18:21], v[224:227], v[196:199], v[18:21]
	v_mfma_f32_16x16x32_bf16 v[6:9], v[212:215], v[204:207], v[6:9]
	v_mfma_f32_16x16x32_bf16 v[2:5], v[224:227], v[204:207], v[2:5]
	s_setprio 0
	s_add_i32 s62, s62, 2
	s_add_u32 s12, s12, 0x100
	s_addc_u32 s13, s13, 0
	s_cmp_gt_u32 s62, 29
	s_barrier
	s_cbranch_scc0 .LBB0_811

.LBB0_916:
	s_add_u32 s14, s14, 0x30080
	s_addc_u32 s15, s15, 0
	s_add_u32 s65, s16, 0x100
	v_mov_b32_e32 v2, 0
	s_addc_u32 s66, s17, 0
	s_mov_b32 s67, -2
	ds_read_b128 v[148:151], v145
	ds_read_b128 v[152:155], v145 offset:1024
	ds_read_b128 v[156:159], v145 offset:2048
	ds_read_b128 v[160:163], v145 offset:3072
	s_add_u32 s16, s14, 0xfffd0080
	s_addc_u32 s17, s15, -1
	s_cmp_eq_u32 s67, 8
	s_cselect_b32 s19, s13, s17
	s_cselect_b32 s18, s12, s16
	s_cselect_b32 s17, s1, s66
	s_cselect_b32 s16, s0, s65
	s_add_i32 m0, s33, 0xc000
	ds_read_b128 v[164:167], v146
	ds_read_b128 v[168:171], v146 offset:1024
	ds_read_b128 v[172:175], v146 offset:2048
	ds_read_b128 v[176:179], v146 offset:3072
	ds_read_b128 v[180:183], v146 offset:4096
	ds_read_b128 v[184:187], v146 offset:5120
	ds_read_b128 v[188:191], v146 offset:6144
	ds_read_b128 v[192:195], v146 offset:7168
	global_load_lds_dwordx4 v138, s[14:15]
	s_add_i32 m0, s33, 0xe000
	s_nop 0
	global_load_lds_dwordx4 v140, s[14:15]
	s_waitcnt lgkmcnt(8)
	s_barrier
	s_waitcnt lgkmcnt(0)
	s_setprio 1
	s_waitcnt lgkmcnt(0)
	v_mfma_f32_16x16x32_bf16 v[126:129], v[148:151], v[164:167], 0
	v_mfma_f32_16x16x32_bf16 v[122:125], v[156:159], v[164:167], 0
	v_mfma_f32_16x16x32_bf16 v[118:121], v[148:151], v[172:175], 0
	v_mfma_f32_16x16x32_bf16 v[114:117], v[156:159], v[172:175], 0
	v_mfma_f32_16x16x32_bf16 v[102:105], v[148:151], v[180:183], 0
	v_mfma_f32_16x16x32_bf16 v[98:101], v[156:159], v[180:183], 0
	v_mfma_f32_16x16x32_bf16 v[86:89], v[148:151], v[188:191], 0
	v_mfma_f32_16x16x32_bf16 v[82:85], v[156:159], v[188:191], 0
	v_mfma_f32_16x16x32_bf16 v[126:129], v[152:155], v[168:171], v[126:129]
	v_mfma_f32_16x16x32_bf16 v[122:125], v[160:163], v[168:171], v[122:125]
	v_mfma_f32_16x16x32_bf16 v[118:121], v[152:155], v[176:179], v[118:121]
	v_mfma_f32_16x16x32_bf16 v[114:117], v[160:163], v[176:179], v[114:117]
	v_mfma_f32_16x16x32_bf16 v[102:105], v[152:155], v[184:187], v[102:105]
	v_mfma_f32_16x16x32_bf16 v[98:101], v[160:163], v[184:187], v[98:101]
	v_mfma_f32_16x16x32_bf16 v[86:89], v[152:155], v[192:195], v[86:89]
	v_mfma_f32_16x16x32_bf16 v[82:85], v[160:163], v[192:195], v[82:85]
	s_setprio 0
	s_barrier
	s_add_i32 s68, s55, s27
	v_lshl_add_u64 v[212:213], s[16:17], 0, v[134:135]
	s_mov_b32 m0, s68
	ds_read_b128 v[196:199], v147
	ds_read_b128 v[200:203], v147 offset:1024
	ds_read_b128 v[204:207], v147 offset:2048
	ds_read_b128 v[208:211], v147 offset:3072
	global_load_lds_dwordx4 v[212:213], off
	v_lshl_add_u64 v[214:215], s[16:17], 0, v[130:131]
	s_add_i32 m0, s68, 0x2000
	s_nop 0
	global_load_lds_dwordx4 v[214:215], off
	s_barrier
	s_waitcnt lgkmcnt(0)
	s_setprio 1
	s_waitcnt lgkmcnt(0)
	v_mfma_f32_16x16x32_bf16 v[110:113], v[196:199], v[164:167], 0
	v_mfma_f32_16x16x32_bf16 v[106:109], v[204:207], v[164:167], 0
	v_mfma_f32_16x16x32_bf16 v[94:97], v[196:199], v[172:175], 0
	v_mfma_f32_16x16x32_bf16 v[90:93], v[204:207], v[172:175], 0
	v_mfma_f32_16x16x32_bf16 v[78:81], v[196:199], v[180:183], 0
	v_mfma_f32_16x16x32_bf16 v[74:77], v[204:207], v[180:183], 0
	v_mfma_f32_16x16x32_bf16 v[70:73], v[196:199], v[188:191], 0
	v_mfma_f32_16x16x32_bf16 v[66:69], v[204:207], v[188:191], 0
	v_mfma_f32_16x16x32_bf16 v[110:113], v[200:203], v[168:171], v[110:113]
	v_mfma_f32_16x16x32_bf16 v[106:109], v[208:211], v[168:171], v[106:109]
	v_mfma_f32_16x16x32_bf16 v[94:97], v[200:203], v[176:179], v[94:97]
	v_mfma_f32_16x16x32_bf16 v[90:93], v[208:211], v[176:179], v[90:93]
	v_mfma_f32_16x16x32_bf16 v[78:81], v[200:203], v[184:187], v[78:81]
	v_mfma_f32_16x16x32_bf16 v[74:77], v[208:211], v[184:187], v[74:77]
	v_mfma_f32_16x16x32_bf16 v[70:73], v[200:203], v[192:195], v[70:73]
	v_mfma_f32_16x16x32_bf16 v[66:69], v[208:211], v[192:195], v[66:69]
	s_setprio 0
	s_mov_b32 m0, s33
	v_lshl_add_u64 v[216:217], s[18:19], 0, v[136:137]
	s_barrier
	ds_read_b128 v[164:167], v146 offset:16384
	ds_read_b128 v[168:171], v146 offset:17408
	ds_read_b128 v[172:175], v146 offset:18432
	ds_read_b128 v[176:179], v146 offset:19456
	ds_read_b128 v[180:183], v146 offset:20480
	ds_read_b128 v[184:187], v146 offset:21504
	ds_read_b128 v[188:191], v146 offset:22528
	ds_read_b128 v[192:195], v146 offset:23552
	global_load_lds_dwordx4 v[216:217], off
	v_lshl_add_u64 v[220:221], s[18:19], 0, v[132:133]
	s_mov_b32 m0, s34
	s_nop 0
	global_load_lds_dwordx4 v[220:221], off
	s_barrier
	s_waitcnt lgkmcnt(0)
	s_setprio 1
	s_waitcnt lgkmcnt(0)
	v_mfma_f32_16x16x32_bf16 v[62:65], v[148:151], v[164:167], 0
	v_mfma_f32_16x16x32_bf16 v[58:61], v[156:159], v[164:167], 0
	v_mfma_f32_16x16x32_bf16 v[54:57], v[148:151], v[172:175], 0
	v_mfma_f32_16x16x32_bf16 v[50:53], v[156:159], v[172:175], 0
	v_mfma_f32_16x16x32_bf16 v[38:41], v[148:151], v[180:183], 0
	v_mfma_f32_16x16x32_bf16 v[34:37], v[156:159], v[180:183], 0
	v_mfma_f32_16x16x32_bf16 v[22:25], v[148:151], v[188:191], 0
	v_mfma_f32_16x16x32_bf16 v[18:21], v[156:159], v[188:191], 0
	v_mfma_f32_16x16x32_bf16 v[62:65], v[152:155], v[168:171], v[62:65]
	v_mfma_f32_16x16x32_bf16 v[58:61], v[160:163], v[168:171], v[58:61]
	v_mfma_f32_16x16x32_bf16 v[54:57], v[152:155], v[176:179], v[54:57]
	v_mfma_f32_16x16x32_bf16 v[50:53], v[160:163], v[176:179], v[50:53]
	v_mfma_f32_16x16x32_bf16 v[38:41], v[152:155], v[184:187], v[38:41]
	v_mfma_f32_16x16x32_bf16 v[34:37], v[160:163], v[184:187], v[34:37]
	v_mfma_f32_16x16x32_bf16 v[22:25], v[152:155], v[192:195], v[22:25]
	v_mfma_f32_16x16x32_bf16 v[18:21], v[160:163], v[192:195], v[18:21]
	s_setprio 0
	s_barrier
	s_add_u32 s68, s16, 0x30000
	s_addc_u32 s69, s17, 0
	s_add_i32 s72, s56, s27
	s_mov_b32 m0, s72
	s_nop 0
	global_load_lds_dwordx4 v134, s[68:69]
	s_add_i32 m0, s72, 0x2000
	s_nop 0
	global_load_lds_dwordx4 v130, s[68:69]
	s_waitcnt vmcnt(6)
	s_barrier
	s_setprio 1
	v_mfma_f32_16x16x32_bf16 v[46:49], v[196:199], v[164:167], 0
	v_mfma_f32_16x16x32_bf16 v[42:45], v[204:207], v[164:167], 0
	v_mfma_f32_16x16x32_bf16 v[30:33], v[196:199], v[172:175], 0
	v_mfma_f32_16x16x32_bf16 v[26:29], v[204:207], v[172:175], 0
	v_mfma_f32_16x16x32_bf16 v[14:17], v[196:199], v[180:183], 0
	v_mfma_f32_16x16x32_bf16 v[10:13], v[204:207], v[180:183], 0
	v_mfma_f32_16x16x32_bf16 v[6:9], v[196:199], v[188:191], 0
	v_mfma_f32_16x16x32_bf16 v[2:5], v[204:207], v[188:191], 0
	v_mfma_f32_16x16x32_bf16 v[46:49], v[200:203], v[168:171], v[46:49]
	v_mfma_f32_16x16x32_bf16 v[42:45], v[208:211], v[168:171], v[42:45]
	v_mfma_f32_16x16x32_bf16 v[30:33], v[200:203], v[176:179], v[30:33]
	v_mfma_f32_16x16x32_bf16 v[26:29], v[208:211], v[176:179], v[26:29]
	v_mfma_f32_16x16x32_bf16 v[14:17], v[200:203], v[184:187], v[14:17]
	v_mfma_f32_16x16x32_bf16 v[10:13], v[208:211], v[184:187], v[10:13]
	v_mfma_f32_16x16x32_bf16 v[6:9], v[200:203], v[192:195], v[6:9]
	v_mfma_f32_16x16x32_bf16 v[2:5], v[208:211], v[192:195], v[2:5]
	s_setprio 0
	s_add_i32 s68, 0, 0x18000
	v_add_u32_e32 v1, s68, v143
	s_barrier
	ds_read_b128 v[148:151], v1
	ds_read_b128 v[152:155], v1 offset:1024
	ds_read_b128 v[156:159], v1 offset:2048
	ds_read_b128 v[160:163], v1 offset:3072
	s_add_u32 s18, s18, 0x30000
	s_addc_u32 s19, s19, 0
	s_mov_b32 m0, s35
	ds_read_b128 v[164:167], v146 offset:32768
	ds_read_b128 v[168:171], v146 offset:33792
	ds_read_b128 v[172:175], v146 offset:34816
	ds_read_b128 v[176:179], v146 offset:35840
	ds_read_b128 v[180:183], v146 offset:36864
	ds_read_b128 v[184:187], v146 offset:37888
	ds_read_b128 v[188:191], v146 offset:38912
	ds_read_b128 v[192:195], v146 offset:39936
	global_load_lds_dwordx4 v136, s[18:19]
	s_mov_b32 m0, s40
	s_nop 0
	global_load_lds_dwordx4 v132, s[18:19]
	s_waitcnt lgkmcnt(8)
	s_barrier
	s_waitcnt lgkmcnt(0)
	s_setprio 1
	s_waitcnt lgkmcnt(0)
	v_mfma_f32_16x16x32_bf16 v[126:129], v[148:151], v[164:167], v[126:129]
	v_mfma_f32_16x16x32_bf16 v[122:125], v[156:159], v[164:167], v[122:125]
	v_mfma_f32_16x16x32_bf16 v[118:121], v[148:151], v[172:175], v[118:121]
	v_mfma_f32_16x16x32_bf16 v[114:117], v[156:159], v[172:175], v[114:117]
	v_mfma_f32_16x16x32_bf16 v[102:105], v[148:151], v[180:183], v[102:105]
	v_mfma_f32_16x16x32_bf16 v[98:101], v[156:159], v[180:183], v[98:101]
	v_mfma_f32_16x16x32_bf16 v[86:89], v[148:151], v[188:191], v[86:89]
	v_mfma_f32_16x16x32_bf16 v[82:85], v[156:159], v[188:191], v[82:85]
	v_mfma_f32_16x16x32_bf16 v[126:129], v[152:155], v[168:171], v[126:129]
	v_mfma_f32_16x16x32_bf16 v[122:125], v[160:163], v[168:171], v[122:125]
	v_mfma_f32_16x16x32_bf16 v[118:121], v[152:155], v[176:179], v[118:121]
	v_mfma_f32_16x16x32_bf16 v[114:117], v[160:163], v[176:179], v[114:117]
	v_mfma_f32_16x16x32_bf16 v[102:105], v[152:155], v[184:187], v[102:105]
	v_mfma_f32_16x16x32_bf16 v[98:101], v[160:163], v[184:187], v[98:101]
	v_mfma_f32_16x16x32_bf16 v[86:89], v[152:155], v[192:195], v[86:89]
	v_mfma_f32_16x16x32_bf16 v[82:85], v[160:163], v[192:195], v[82:85]
	s_setprio 0
	s_barrier
	s_add_i32 s18, 0, 0x1c000
	s_add_i32 s19, s68, s27
	v_add_u32_e32 v1, s18, v143
	v_lshl_add_u64 v[212:213], v[212:213], 0, s[6:7]
	s_mov_b32 m0, s19
	ds_read_b128 v[196:199], v1
	ds_read_b128 v[200:203], v1 offset:1024
	ds_read_b128 v[204:207], v1 offset:2048
	ds_read_b128 v[208:211], v1 offset:3072
	global_load_lds_dwordx4 v[212:213], off
	v_lshl_add_u64 v[212:213], v[214:215], 0, s[6:7]
	s_add_i32 m0, s19, 0x2000
	s_nop 0
	global_load_lds_dwordx4 v[212:213], off
	s_barrier
	s_waitcnt lgkmcnt(0)
	s_setprio 1
	s_waitcnt lgkmcnt(0)
	v_mfma_f32_16x16x32_bf16 v[110:113], v[196:199], v[164:167], v[110:113]
	v_mfma_f32_16x16x32_bf16 v[106:109], v[204:207], v[164:167], v[106:109]
	v_mfma_f32_16x16x32_bf16 v[94:97], v[196:199], v[172:175], v[94:97]
	v_mfma_f32_16x16x32_bf16 v[90:93], v[204:207], v[172:175], v[90:93]
	v_mfma_f32_16x16x32_bf16 v[78:81], v[196:199], v[180:183], v[78:81]
	v_mfma_f32_16x16x32_bf16 v[74:77], v[204:207], v[180:183], v[74:77]
	v_mfma_f32_16x16x32_bf16 v[70:73], v[196:199], v[188:191], v[70:73]
	v_mfma_f32_16x16x32_bf16 v[66:69], v[204:207], v[188:191], v[66:69]
	v_mfma_f32_16x16x32_bf16 v[110:113], v[200:203], v[168:171], v[110:113]
	v_mfma_f32_16x16x32_bf16 v[106:109], v[208:211], v[168:171], v[106:109]
	v_mfma_f32_16x16x32_bf16 v[94:97], v[200:203], v[176:179], v[94:97]
	v_mfma_f32_16x16x32_bf16 v[90:93], v[208:211], v[176:179], v[90:93]
	v_mfma_f32_16x16x32_bf16 v[78:81], v[200:203], v[184:187], v[78:81]
	v_mfma_f32_16x16x32_bf16 v[74:77], v[208:211], v[184:187], v[74:77]
	v_mfma_f32_16x16x32_bf16 v[70:73], v[200:203], v[192:195], v[70:73]
	v_mfma_f32_16x16x32_bf16 v[66:69], v[208:211], v[192:195], v[66:69]
	s_setprio 0
	s_mov_b32 m0, s41
	v_lshl_add_u64 v[212:213], v[216:217], 0, s[6:7]
	s_barrier
	ds_read_b128 v[164:167], v146 offset:49152
	ds_read_b128 v[168:171], v146 offset:50176
	ds_read_b128 v[172:175], v146 offset:51200
	ds_read_b128 v[176:179], v146 offset:52224
	ds_read_b128 v[180:183], v146 offset:53248
	ds_read_b128 v[184:187], v146 offset:54272
	ds_read_b128 v[188:191], v146 offset:55296
	ds_read_b128 v[192:195], v146 offset:56320
	global_load_lds_dwordx4 v[212:213], off
	v_lshl_add_u64 v[212:213], v[220:221], 0, s[6:7]
	s_mov_b32 m0, s54
	s_nop 0
	global_load_lds_dwordx4 v[212:213], off
	s_barrier
	s_waitcnt lgkmcnt(0)
	s_setprio 1
	s_waitcnt lgkmcnt(0)
	v_mfma_f32_16x16x32_bf16 v[62:65], v[148:151], v[164:167], v[62:65]
	v_mfma_f32_16x16x32_bf16 v[58:61], v[156:159], v[164:167], v[58:61]
	v_mfma_f32_16x16x32_bf16 v[54:57], v[148:151], v[172:175], v[54:57]
	v_mfma_f32_16x16x32_bf16 v[50:53], v[156:159], v[172:175], v[50:53]
	v_mfma_f32_16x16x32_bf16 v[38:41], v[148:151], v[180:183], v[38:41]
	v_mfma_f32_16x16x32_bf16 v[34:37], v[156:159], v[180:183], v[34:37]
	v_mfma_f32_16x16x32_bf16 v[22:25], v[148:151], v[188:191], v[22:25]
	v_mfma_f32_16x16x32_bf16 v[18:21], v[156:159], v[188:191], v[18:21]
	v_mfma_f32_16x16x32_bf16 v[62:65], v[152:155], v[168:171], v[62:65]
	v_mfma_f32_16x16x32_bf16 v[58:61], v[160:163], v[168:171], v[58:61]
	v_mfma_f32_16x16x32_bf16 v[54:57], v[152:155], v[176:179], v[54:57]
	v_mfma_f32_16x16x32_bf16 v[50:53], v[160:163], v[176:179], v[50:53]
	v_mfma_f32_16x16x32_bf16 v[38:41], v[152:155], v[184:187], v[38:41]
	v_mfma_f32_16x16x32_bf16 v[34:37], v[160:163], v[184:187], v[34:37]
	v_mfma_f32_16x16x32_bf16 v[22:25], v[152:155], v[192:195], v[22:25]
	v_mfma_f32_16x16x32_bf16 v[18:21], v[160:163], v[192:195], v[18:21]
	s_setprio 0
	s_barrier
	s_add_u32 s16, s16, 0x30080
	s_addc_u32 s17, s17, 0
	s_add_i32 s18, s18, s27
	s_mov_b32 m0, s18
	s_nop 0
	global_load_lds_dwordx4 v134, s[16:17]
	s_add_i32 m0, s18, 0x2000
	s_nop 0
	global_load_lds_dwordx4 v130, s[16:17]
	s_waitcnt vmcnt(6)
	s_barrier
	s_setprio 1
	v_mfma_f32_16x16x32_bf16 v[46:49], v[196:199], v[164:167], v[46:49]
	v_mfma_f32_16x16x32_bf16 v[42:45], v[204:207], v[164:167], v[42:45]
	v_mfma_f32_16x16x32_bf16 v[30:33], v[196:199], v[172:175], v[30:33]
	v_mfma_f32_16x16x32_bf16 v[26:29], v[204:207], v[172:175], v[26:29]
	v_mfma_f32_16x16x32_bf16 v[14:17], v[196:199], v[180:183], v[14:17]
	v_mfma_f32_16x16x32_bf16 v[10:13], v[204:207], v[180:183], v[10:13]
	v_mfma_f32_16x16x32_bf16 v[6:9], v[196:199], v[188:191], v[6:9]
	v_mfma_f32_16x16x32_bf16 v[2:5], v[204:207], v[188:191], v[2:5]
	v_mfma_f32_16x16x32_bf16 v[46:49], v[200:203], v[168:171], v[46:49]
	v_mfma_f32_16x16x32_bf16 v[42:45], v[208:211], v[168:171], v[42:45]
	v_mfma_f32_16x16x32_bf16 v[30:33], v[200:203], v[176:179], v[30:33]
	v_mfma_f32_16x16x32_bf16 v[26:29], v[208:211], v[176:179], v[26:29]
	v_mfma_f32_16x16x32_bf16 v[14:17], v[200:203], v[184:187], v[14:17]
	v_mfma_f32_16x16x32_bf16 v[10:13], v[208:211], v[184:187], v[10:13]
	v_mfma_f32_16x16x32_bf16 v[6:9], v[200:203], v[192:195], v[6:9]
	v_mfma_f32_16x16x32_bf16 v[2:5], v[208:211], v[192:195], v[2:5]
	s_setprio 0
	s_add_i32 s67, s67, 2
	s_add_u32 s14, s14, 0x100
	s_addc_u32 s15, s15, 0
	s_add_u32 s65, s65, 0x100
	s_addc_u32 s66, s66, 0
	s_cmp_gt_u32 s67, 9
	s_barrier
	s_cbranch_scc1 .Lpeel_917_after
.LBB0_917:
	ds_read_b128 v[148:151], v145
	ds_read_b128 v[152:155], v145 offset:1024
	ds_read_b128 v[156:159], v145 offset:2048
	ds_read_b128 v[160:163], v145 offset:3072
	s_add_u32 s16, s14, 0xfffd0080
	s_addc_u32 s17, s15, -1
	s_cmp_eq_u32 s67, 8
	s_cselect_b32 s19, s13, s17
	s_cselect_b32 s18, s12, s16
	s_cselect_b32 s17, s1, s66
	s_cselect_b32 s16, s0, s65
	s_add_i32 m0, s33, 0xc000
	ds_read_b128 v[164:167], v146
	ds_read_b128 v[168:171], v146 offset:1024
	ds_read_b128 v[172:175], v146 offset:2048
	ds_read_b128 v[176:179], v146 offset:3072
	ds_read_b128 v[180:183], v146 offset:4096
	ds_read_b128 v[184:187], v146 offset:5120
	ds_read_b128 v[188:191], v146 offset:6144
	ds_read_b128 v[192:195], v146 offset:7168
	global_load_lds_dwordx4 v138, s[14:15]
	s_add_i32 m0, s33, 0xe000
	s_nop 0
	global_load_lds_dwordx4 v140, s[14:15]
	s_waitcnt lgkmcnt(8)
	s_barrier
	s_waitcnt lgkmcnt(0)
	s_setprio 1
	s_waitcnt lgkmcnt(0)
	v_mfma_f32_16x16x32_bf16 v[126:129], v[148:151], v[164:167], v[126:129]
	v_mfma_f32_16x16x32_bf16 v[122:125], v[156:159], v[164:167], v[122:125]
	v_mfma_f32_16x16x32_bf16 v[118:121], v[148:151], v[172:175], v[118:121]
	v_mfma_f32_16x16x32_bf16 v[114:117], v[156:159], v[172:175], v[114:117]
	v_mfma_f32_16x16x32_bf16 v[102:105], v[148:151], v[180:183], v[102:105]
	v_mfma_f32_16x16x32_bf16 v[98:101], v[156:159], v[180:183], v[98:101]
	v_mfma_f32_16x16x32_bf16 v[86:89], v[148:151], v[188:191], v[86:89]
	v_mfma_f32_16x16x32_bf16 v[82:85], v[156:159], v[188:191], v[82:85]
	v_mfma_f32_16x16x32_bf16 v[126:129], v[152:155], v[168:171], v[126:129]
	v_mfma_f32_16x16x32_bf16 v[122:125], v[160:163], v[168:171], v[122:125]
	v_mfma_f32_16x16x32_bf16 v[118:121], v[152:155], v[176:179], v[118:121]
	v_mfma_f32_16x16x32_bf16 v[114:117], v[160:163], v[176:179], v[114:117]
	v_mfma_f32_16x16x32_bf16 v[102:105], v[152:155], v[184:187], v[102:105]
	v_mfma_f32_16x16x32_bf16 v[98:101], v[160:163], v[184:187], v[98:101]
	v_mfma_f32_16x16x32_bf16 v[86:89], v[152:155], v[192:195], v[86:89]
	v_mfma_f32_16x16x32_bf16 v[82:85], v[160:163], v[192:195], v[82:85]
	s_setprio 0
	s_barrier
	s_add_i32 s68, s55, s27
	v_lshl_add_u64 v[212:213], s[16:17], 0, v[134:135]
	s_mov_b32 m0, s68
	ds_read_b128 v[196:199], v147
	ds_read_b128 v[200:203], v147 offset:1024
	ds_read_b128 v[204:207], v147 offset:2048
	ds_read_b128 v[208:211], v147 offset:3072
	global_load_lds_dwordx4 v[212:213], off
	v_lshl_add_u64 v[214:215], s[16:17], 0, v[130:131]
	s_add_i32 m0, s68, 0x2000
	s_nop 0
	global_load_lds_dwordx4 v[214:215], off
	s_barrier
	s_waitcnt lgkmcnt(0)
	s_setprio 1
	s_waitcnt lgkmcnt(0)
	v_mfma_f32_16x16x32_bf16 v[110:113], v[196:199], v[164:167], v[110:113]
	v_mfma_f32_16x16x32_bf16 v[106:109], v[204:207], v[164:167], v[106:109]
	v_mfma_f32_16x16x32_bf16 v[94:97], v[196:199], v[172:175], v[94:97]
	v_mfma_f32_16x16x32_bf16 v[90:93], v[204:207], v[172:175], v[90:93]
	v_mfma_f32_16x16x32_bf16 v[78:81], v[196:199], v[180:183], v[78:81]
	v_mfma_f32_16x16x32_bf16 v[74:77], v[204:207], v[180:183], v[74:77]
	v_mfma_f32_16x16x32_bf16 v[70:73], v[196:199], v[188:191], v[70:73]
	v_mfma_f32_16x16x32_bf16 v[66:69], v[204:207], v[188:191], v[66:69]
	v_mfma_f32_16x16x32_bf16 v[110:113], v[200:203], v[168:171], v[110:113]
	v_mfma_f32_16x16x32_bf16 v[106:109], v[208:211], v[168:171], v[106:109]
	v_mfma_f32_16x16x32_bf16 v[94:97], v[200:203], v[176:179], v[94:97]
	v_mfma_f32_16x16x32_bf16 v[90:93], v[208:211], v[176:179], v[90:93]
	v_mfma_f32_16x16x32_bf16 v[78:81], v[200:203], v[184:187], v[78:81]
	v_mfma_f32_16x16x32_bf16 v[74:77], v[208:211], v[184:187], v[74:77]
	v_mfma_f32_16x16x32_bf16 v[70:73], v[200:203], v[192:195], v[70:73]
	v_mfma_f32_16x16x32_bf16 v[66:69], v[208:211], v[192:195], v[66:69]
	s_setprio 0
	s_mov_b32 m0, s33
	v_lshl_add_u64 v[216:217], s[18:19], 0, v[136:137]
	s_barrier
	ds_read_b128 v[164:167], v146 offset:16384
	ds_read_b128 v[168:171], v146 offset:17408
	ds_read_b128 v[172:175], v146 offset:18432
	ds_read_b128 v[176:179], v146 offset:19456
	ds_read_b128 v[180:183], v146 offset:20480
	ds_read_b128 v[184:187], v146 offset:21504
	ds_read_b128 v[188:191], v146 offset:22528
	ds_read_b128 v[192:195], v146 offset:23552
	global_load_lds_dwordx4 v[216:217], off
	v_lshl_add_u64 v[220:221], s[18:19], 0, v[132:133]
	s_mov_b32 m0, s34
	s_nop 0
	global_load_lds_dwordx4 v[220:221], off
	s_barrier
	s_waitcnt lgkmcnt(0)
	s_setprio 1
	s_waitcnt lgkmcnt(0)
	v_mfma_f32_16x16x32_bf16 v[62:65], v[148:151], v[164:167], v[62:65]
	v_mfma_f32_16x16x32_bf16 v[58:61], v[156:159], v[164:167], v[58:61]
	v_mfma_f32_16x16x32_bf16 v[54:57], v[148:151], v[172:175], v[54:57]
	v_mfma_f32_16x16x32_bf16 v[50:53], v[156:159], v[172:175], v[50:53]
	v_mfma_f32_16x16x32_bf16 v[38:41], v[148:151], v[180:183], v[38:41]
	v_mfma_f32_16x16x32_bf16 v[34:37], v[156:159], v[180:183], v[34:37]
	v_mfma_f32_16x16x32_bf16 v[22:25], v[148:151], v[188:191], v[22:25]
	v_mfma_f32_16x16x32_bf16 v[18:21], v[156:159], v[188:191], v[18:21]
	v_mfma_f32_16x16x32_bf16 v[62:65], v[152:155], v[168:171], v[62:65]
	v_mfma_f32_16x16x32_bf16 v[58:61], v[160:163], v[168:171], v[58:61]
	v_mfma_f32_16x16x32_bf16 v[54:57], v[152:155], v[176:179], v[54:57]
	v_mfma_f32_16x16x32_bf16 v[50:53], v[160:163], v[176:179], v[50:53]
	v_mfma_f32_16x16x32_bf16 v[38:41], v[152:155], v[184:187], v[38:41]
	v_mfma_f32_16x16x32_bf16 v[34:37], v[160:163], v[184:187], v[34:37]
	v_mfma_f32_16x16x32_bf16 v[22:25], v[152:155], v[192:195], v[22:25]
	v_mfma_f32_16x16x32_bf16 v[18:21], v[160:163], v[192:195], v[18:21]
	s_setprio 0
	s_barrier
	s_add_u32 s68, s16, 0x30000
	s_addc_u32 s69, s17, 0
	s_add_i32 s72, s56, s27
	s_mov_b32 m0, s72
	s_nop 0
	global_load_lds_dwordx4 v134, s[68:69]
	s_add_i32 m0, s72, 0x2000
	s_nop 0
	global_load_lds_dwordx4 v130, s[68:69]
	s_waitcnt vmcnt(6)
	s_barrier
	s_setprio 1
	v_mfma_f32_16x16x32_bf16 v[46:49], v[196:199], v[164:167], v[46:49]
	v_mfma_f32_16x16x32_bf16 v[42:45], v[204:207], v[164:167], v[42:45]
	v_mfma_f32_16x16x32_bf16 v[30:33], v[196:199], v[172:175], v[30:33]
	v_mfma_f32_16x16x32_bf16 v[26:29], v[204:207], v[172:175], v[26:29]
	v_mfma_f32_16x16x32_bf16 v[14:17], v[196:199], v[180:183], v[14:17]
	v_mfma_f32_16x16x32_bf16 v[10:13], v[204:207], v[180:183], v[10:13]
	v_mfma_f32_16x16x32_bf16 v[6:9], v[196:199], v[188:191], v[6:9]
	v_mfma_f32_16x16x32_bf16 v[2:5], v[204:207], v[188:191], v[2:5]
	v_mfma_f32_16x16x32_bf16 v[46:49], v[200:203], v[168:171], v[46:49]
	v_mfma_f32_16x16x32_bf16 v[42:45], v[208:211], v[168:171], v[42:45]
	v_mfma_f32_16x16x32_bf16 v[30:33], v[200:203], v[176:179], v[30:33]
	v_mfma_f32_16x16x32_bf16 v[26:29], v[208:211], v[176:179], v[26:29]
	v_mfma_f32_16x16x32_bf16 v[14:17], v[200:203], v[184:187], v[14:17]
	v_mfma_f32_16x16x32_bf16 v[10:13], v[208:211], v[184:187], v[10:13]
	v_mfma_f32_16x16x32_bf16 v[6:9], v[200:203], v[192:195], v[6:9]
	v_mfma_f32_16x16x32_bf16 v[2:5], v[208:211], v[192:195], v[2:5]
	s_setprio 0
	s_add_i32 s68, 0, 0x18000
	v_add_u32_e32 v1, s68, v143
	s_barrier
	ds_read_b128 v[148:151], v1
	ds_read_b128 v[152:155], v1 offset:1024
	ds_read_b128 v[156:159], v1 offset:2048
	ds_read_b128 v[160:163], v1 offset:3072
	s_add_u32 s18, s18, 0x30000
	s_addc_u32 s19, s19, 0
	s_mov_b32 m0, s35
	ds_read_b128 v[164:167], v146 offset:32768
	ds_read_b128 v[168:171], v146 offset:33792
	ds_read_b128 v[172:175], v146 offset:34816
	ds_read_b128 v[176:179], v146 offset:35840
	ds_read_b128 v[180:183], v146 offset:36864
	ds_read_b128 v[184:187], v146 offset:37888
	ds_read_b128 v[188:191], v146 offset:38912
	ds_read_b128 v[192:195], v146 offset:39936
	global_load_lds_dwordx4 v136, s[18:19]
	s_mov_b32 m0, s40
	s_nop 0
	global_load_lds_dwordx4 v132, s[18:19]
	s_waitcnt lgkmcnt(8)
	s_barrier
	s_waitcnt lgkmcnt(0)
	s_setprio 1
	s_waitcnt lgkmcnt(0)
	v_mfma_f32_16x16x32_bf16 v[126:129], v[148:151], v[164:167], v[126:129]
	v_mfma_f32_16x16x32_bf16 v[122:125], v[156:159], v[164:167], v[122:125]
	v_mfma_f32_16x16x32_bf16 v[118:121], v[148:151], v[172:175], v[118:121]
	v_mfma_f32_16x16x32_bf16 v[114:117], v[156:159], v[172:175], v[114:117]
	v_mfma_f32_16x16x32_bf16 v[102:105], v[148:151], v[180:183], v[102:105]
	v_mfma_f32_16x16x32_bf16 v[98:101], v[156:159], v[180:183], v[98:101]
	v_mfma_f32_16x16x32_bf16 v[86:89], v[148:151], v[188:191], v[86:89]
	v_mfma_f32_16x16x32_bf16 v[82:85], v[156:159], v[188:191], v[82:85]
	v_mfma_f32_16x16x32_bf16 v[126:129], v[152:155], v[168:171], v[126:129]
	v_mfma_f32_16x16x32_bf16 v[122:125], v[160:163], v[168:171], v[122:125]
	v_mfma_f32_16x16x32_bf16 v[118:121], v[152:155], v[176:179], v[118:121]
	v_mfma_f32_16x16x32_bf16 v[114:117], v[160:163], v[176:179], v[114:117]
	v_mfma_f32_16x16x32_bf16 v[102:105], v[152:155], v[184:187], v[102:105]
	v_mfma_f32_16x16x32_bf16 v[98:101], v[160:163], v[184:187], v[98:101]
	v_mfma_f32_16x16x32_bf16 v[86:89], v[152:155], v[192:195], v[86:89]
	v_mfma_f32_16x16x32_bf16 v[82:85], v[160:163], v[192:195], v[82:85]
	s_setprio 0
	s_barrier
	s_add_i32 s18, 0, 0x1c000
	s_add_i32 s19, s68, s27
	v_add_u32_e32 v1, s18, v143
	v_lshl_add_u64 v[212:213], v[212:213], 0, s[6:7]
	s_mov_b32 m0, s19
	ds_read_b128 v[196:199], v1
	ds_read_b128 v[200:203], v1 offset:1024
	ds_read_b128 v[204:207], v1 offset:2048
	ds_read_b128 v[208:211], v1 offset:3072
	global_load_lds_dwordx4 v[212:213], off
	v_lshl_add_u64 v[212:213], v[214:215], 0, s[6:7]
	s_add_i32 m0, s19, 0x2000
	s_nop 0
	global_load_lds_dwordx4 v[212:213], off
	s_barrier
	s_waitcnt lgkmcnt(0)
	s_setprio 1
	s_waitcnt lgkmcnt(0)
	v_mfma_f32_16x16x32_bf16 v[110:113], v[196:199], v[164:167], v[110:113]
	v_mfma_f32_16x16x32_bf16 v[106:109], v[204:207], v[164:167], v[106:109]
	v_mfma_f32_16x16x32_bf16 v[94:97], v[196:199], v[172:175], v[94:97]
	v_mfma_f32_16x16x32_bf16 v[90:93], v[204:207], v[172:175], v[90:93]
	v_mfma_f32_16x16x32_bf16 v[78:81], v[196:199], v[180:183], v[78:81]
	v_mfma_f32_16x16x32_bf16 v[74:77], v[204:207], v[180:183], v[74:77]
	v_mfma_f32_16x16x32_bf16 v[70:73], v[196:199], v[188:191], v[70:73]
	v_mfma_f32_16x16x32_bf16 v[66:69], v[204:207], v[188:191], v[66:69]
	v_mfma_f32_16x16x32_bf16 v[110:113], v[200:203], v[168:171], v[110:113]
	v_mfma_f32_16x16x32_bf16 v[106:109], v[208:211], v[168:171], v[106:109]
	v_mfma_f32_16x16x32_bf16 v[94:97], v[200:203], v[176:179], v[94:97]
	v_mfma_f32_16x16x32_bf16 v[90:93], v[208:211], v[176:179], v[90:93]
	v_mfma_f32_16x16x32_bf16 v[78:81], v[200:203], v[184:187], v[78:81]
	v_mfma_f32_16x16x32_bf16 v[74:77], v[208:211], v[184:187], v[74:77]
	v_mfma_f32_16x16x32_bf16 v[70:73], v[200:203], v[192:195], v[70:73]
	v_mfma_f32_16x16x32_bf16 v[66:69], v[208:211], v[192:195], v[66:69]
	s_setprio 0
	s_mov_b32 m0, s41
	v_lshl_add_u64 v[212:213], v[216:217], 0, s[6:7]
	s_barrier
	ds_read_b128 v[164:167], v146 offset:49152
	ds_read_b128 v[168:171], v146 offset:50176
	ds_read_b128 v[172:175], v146 offset:51200
	ds_read_b128 v[176:179], v146 offset:52224
	ds_read_b128 v[180:183], v146 offset:53248
	ds_read_b128 v[184:187], v146 offset:54272
	ds_read_b128 v[188:191], v146 offset:55296
	ds_read_b128 v[192:195], v146 offset:56320
	global_load_lds_dwordx4 v[212:213], off
	v_lshl_add_u64 v[212:213], v[220:221], 0, s[6:7]
	s_mov_b32 m0, s54
	s_nop 0
	global_load_lds_dwordx4 v[212:213], off
	s_barrier
	s_waitcnt lgkmcnt(0)
	s_setprio 1
	s_waitcnt lgkmcnt(0)
	v_mfma_f32_16x16x32_bf16 v[62:65], v[148:151], v[164:167], v[62:65]
	v_mfma_f32_16x16x32_bf16 v[58:61], v[156:159], v[164:167], v[58:61]
	v_mfma_f32_16x16x32_bf16 v[54:57], v[148:151], v[172:175], v[54:57]
	v_mfma_f32_16x16x32_bf16 v[50:53], v[156:159], v[172:175], v[50:53]
	v_mfma_f32_16x16x32_bf16 v[38:41], v[148:151], v[180:183], v[38:41]
	v_mfma_f32_16x16x32_bf16 v[34:37], v[156:159], v[180:183], v[34:37]
	v_mfma_f32_16x16x32_bf16 v[22:25], v[148:151], v[188:191], v[22:25]
	v_mfma_f32_16x16x32_bf16 v[18:21], v[156:159], v[188:191], v[18:21]
	v_mfma_f32_16x16x32_bf16 v[62:65], v[152:155], v[168:171], v[62:65]
	v_mfma_f32_16x16x32_bf16 v[58:61], v[160:163], v[168:171], v[58:61]
	v_mfma_f32_16x16x32_bf16 v[54:57], v[152:155], v[176:179], v[54:57]
	v_mfma_f32_16x16x32_bf16 v[50:53], v[160:163], v[176:179], v[50:53]
	v_mfma_f32_16x16x32_bf16 v[38:41], v[152:155], v[184:187], v[38:41]
	v_mfma_f32_16x16x32_bf16 v[34:37], v[160:163], v[184:187], v[34:37]
	v_mfma_f32_16x16x32_bf16 v[22:25], v[152:155], v[192:195], v[22:25]
	v_mfma_f32_16x16x32_bf16 v[18:21], v[160:163], v[192:195], v[18:21]
	s_setprio 0
	s_barrier
	s_add_u32 s16, s16, 0x30080
	s_addc_u32 s17, s17, 0
	s_add_i32 s18, s18, s27
	s_mov_b32 m0, s18
	s_nop 0
	global_load_lds_dwordx4 v134, s[16:17]
	s_add_i32 m0, s18, 0x2000
	s_nop 0
	global_load_lds_dwordx4 v130, s[16:17]
	s_waitcnt vmcnt(6)
	s_barrier
	s_setprio 1
	v_mfma_f32_16x16x32_bf16 v[46:49], v[196:199], v[164:167], v[46:49]
	v_mfma_f32_16x16x32_bf16 v[42:45], v[204:207], v[164:167], v[42:45]
	v_mfma_f32_16x16x32_bf16 v[30:33], v[196:199], v[172:175], v[30:33]
	v_mfma_f32_16x16x32_bf16 v[26:29], v[204:207], v[172:175], v[26:29]
	v_mfma_f32_16x16x32_bf16 v[14:17], v[196:199], v[180:183], v[14:17]
	v_mfma_f32_16x16x32_bf16 v[10:13], v[204:207], v[180:183], v[10:13]
	v_mfma_f32_16x16x32_bf16 v[6:9], v[196:199], v[188:191], v[6:9]
	v_mfma_f32_16x16x32_bf16 v[2:5], v[204:207], v[188:191], v[2:5]
	v_mfma_f32_16x16x32_bf16 v[46:49], v[200:203], v[168:171], v[46:49]
	v_mfma_f32_16x16x32_bf16 v[42:45], v[208:211], v[168:171], v[42:45]
	v_mfma_f32_16x16x32_bf16 v[30:33], v[200:203], v[176:179], v[30:33]
	v_mfma_f32_16x16x32_bf16 v[26:29], v[208:211], v[176:179], v[26:29]
	v_mfma_f32_16x16x32_bf16 v[14:17], v[200:203], v[184:187], v[14:17]
	v_mfma_f32_16x16x32_bf16 v[10:13], v[208:211], v[184:187], v[10:13]
	v_mfma_f32_16x16x32_bf16 v[6:9], v[200:203], v[192:195], v[6:9]
	v_mfma_f32_16x16x32_bf16 v[2:5], v[208:211], v[192:195], v[2:5]
	s_setprio 0
	s_add_i32 s67, s67, 2
	s_add_u32 s14, s14, 0x100
	s_addc_u32 s15, s15, 0
	s_add_u32 s65, s65, 0x100
	s_addc_u32 s66, s66, 0
	s_cmp_gt_u32 s67, 9
	s_barrier
	s_cbranch_scc0 .LBB0_917

.LBB0_1036:
	v_mov_b64_e32 v[2:3], 0x600
	s_ashr_i32 s17, s16, 31
	v_cmp_lt_i64_e32 vcc, s[18:19], v[2:3]
	s_lshl_b64 s[18:19], s[16:17], 20
	s_add_u32 s18, s36, s18
	s_addc_u32 s19, s37, s19
	s_and_b64 s[20:21], vcc, exec
	s_cselect_b32 s17, s19, s5
	s_cselect_b32 s63, s18, s4
	s_ashr_i32 s15, s14, 31
	s_lshl_b64 s[20:21], s[14:15], 20
	v_readlane_b32 s54, v254, 30
	v_readlane_b32 s55, v254, 31
	s_add_u32 s20, s54, s20
	s_addc_u32 s21, s55, s21
	s_and_b64 s[54:55], vcc, exec
	s_cselect_b32 s15, s21, s9
	s_cselect_b32 s64, s20, s8
	s_add_u32 s4, s4, 0x80080
	s_addc_u32 s5, s5, 0
	s_add_u32 s65, s8, 0x100
	v_mov_b32_e32 v2, 0
	s_addc_u32 s66, s9, 0
	s_mov_b32 s67, -2
	s_waitcnt vmcnt(0)
	ds_read_b128 v[130:133], v192
	ds_read_b128 v[134:137], v192 offset:1024
	ds_read_b128 v[200:203], v192 offset:2048
	ds_read_b128 v[204:207], v192 offset:3072
	s_add_u32 s8, s4, 0xfff80080
	s_addc_u32 s9, s5, -1
	s_cmp_eq_u32 s67, 28
	s_cselect_b32 s55, s17, s9
	s_cselect_b32 s54, s63, s8
	s_cselect_b32 s9, s15, s66
	s_cselect_b32 s8, s64, s65
	s_add_i32 m0, s23, 0xc000
	ds_read_b128 v[208:211], v193
	ds_read_b128 v[212:215], v193 offset:1024
	ds_read_b128 v[220:223], v193 offset:2048
	ds_read_b128 v[224:227], v193 offset:3072
	ds_read_b128 v[228:231], v193 offset:4096
	ds_read_b128 v[232:235], v193 offset:5120
	ds_read_b128 v[236:239], v193 offset:6144
	ds_read_b128 v[240:243], v193 offset:7168
	global_load_lds_dwordx4 v146, s[4:5]
	s_add_i32 m0, s23, 0xe000
	s_nop 0
	global_load_lds_dwordx4 v148, s[4:5]
	s_waitcnt lgkmcnt(8)
	s_barrier
	s_waitcnt lgkmcnt(0)
	s_setprio 1
	s_waitcnt lgkmcnt(0)
	v_mfma_f32_16x16x32_bf16 v[126:129], v[130:133], v[208:211], 0
	v_mfma_f32_16x16x32_bf16 v[122:125], v[200:203], v[208:211], 0
	v_mfma_f32_16x16x32_bf16 v[110:113], v[130:133], v[220:223], 0
	v_mfma_f32_16x16x32_bf16 v[106:109], v[200:203], v[220:223], 0
	v_mfma_f32_16x16x32_bf16 v[94:97], v[130:133], v[228:231], 0
	v_mfma_f32_16x16x32_bf16 v[90:93], v[200:203], v[228:231], 0
	v_mfma_f32_16x16x32_bf16 v[78:81], v[130:133], v[236:239], 0
	v_mfma_f32_16x16x32_bf16 v[74:77], v[200:203], v[236:239], 0
	v_mfma_f32_16x16x32_bf16 v[126:129], v[134:137], v[212:215], v[126:129]
	v_mfma_f32_16x16x32_bf16 v[122:125], v[204:207], v[212:215], v[122:125]
	v_mfma_f32_16x16x32_bf16 v[110:113], v[134:137], v[224:227], v[110:113]
	v_mfma_f32_16x16x32_bf16 v[106:109], v[204:207], v[224:227], v[106:109]
	v_mfma_f32_16x16x32_bf16 v[94:97], v[134:137], v[232:235], v[94:97]
	v_mfma_f32_16x16x32_bf16 v[90:93], v[204:207], v[232:235], v[90:93]
	v_mfma_f32_16x16x32_bf16 v[78:81], v[134:137], v[240:243], v[78:81]
	v_mfma_f32_16x16x32_bf16 v[74:77], v[204:207], v[240:243], v[74:77]
	s_setprio 0
	s_barrier
	s_add_i32 s68, s58, s3
	v_lshl_add_u64 v[186:187], s[8:9], 0, v[140:141]
	s_mov_b32 m0, s68
	ds_read_b128 v[244:247], v194
	ds_read_b128 v[248:251], v194 offset:1024
	ds_read_b128 v[150:153], v194 offset:2048
	ds_read_b128 v[176:179], v194 offset:3072
	global_load_lds_dwordx4 v[186:187], off
	v_lshl_add_u64 v[216:217], s[8:9], 0, v[144:145]
	s_add_i32 m0, s68, 0x2000
	s_nop 0
	global_load_lds_dwordx4 v[216:217], off
	s_barrier
	s_waitcnt lgkmcnt(0)
	s_setprio 1
	s_waitcnt lgkmcnt(0)
	v_mfma_f32_16x16x32_bf16 v[118:121], v[244:247], v[208:211], 0
	v_mfma_f32_16x16x32_bf16 v[114:117], v[150:153], v[208:211], 0
	v_mfma_f32_16x16x32_bf16 v[102:105], v[244:247], v[220:223], 0
	v_mfma_f32_16x16x32_bf16 v[98:101], v[150:153], v[220:223], 0
	v_mfma_f32_16x16x32_bf16 v[86:89], v[244:247], v[228:231], 0
	v_mfma_f32_16x16x32_bf16 v[82:85], v[150:153], v[228:231], 0
	v_mfma_f32_16x16x32_bf16 v[70:73], v[244:247], v[236:239], 0
	v_mfma_f32_16x16x32_bf16 v[66:69], v[150:153], v[236:239], 0
	v_mfma_f32_16x16x32_bf16 v[118:121], v[248:251], v[212:215], v[118:121]
	v_mfma_f32_16x16x32_bf16 v[114:117], v[176:179], v[212:215], v[114:117]
	v_mfma_f32_16x16x32_bf16 v[102:105], v[248:251], v[224:227], v[102:105]
	v_mfma_f32_16x16x32_bf16 v[98:101], v[176:179], v[224:227], v[98:101]
	v_mfma_f32_16x16x32_bf16 v[86:89], v[248:251], v[232:235], v[86:89]
	v_mfma_f32_16x16x32_bf16 v[82:85], v[176:179], v[232:235], v[82:85]
	v_mfma_f32_16x16x32_bf16 v[70:73], v[248:251], v[240:243], v[70:73]
	v_mfma_f32_16x16x32_bf16 v[66:69], v[176:179], v[240:243], v[66:69]
	s_setprio 0
	s_mov_b32 m0, s23
	v_lshl_add_u64 v[252:253], s[54:55], 0, v[138:139]
	s_barrier
	ds_read_b128 v[208:211], v193 offset:16384
	ds_read_b128 v[212:215], v193 offset:17408
	ds_read_b128 v[220:223], v193 offset:18432
	ds_read_b128 v[224:227], v193 offset:19456
	ds_read_b128 v[228:231], v193 offset:20480
	ds_read_b128 v[232:235], v193 offset:21504
	ds_read_b128 v[236:239], v193 offset:22528
	ds_read_b128 v[240:243], v193 offset:23552
	global_load_lds_dwordx4 v[252:253], off
	v_lshl_add_u64 v[160:161], s[54:55], 0, v[142:143]
	s_mov_b32 m0, s25
	s_nop 0
	global_load_lds_dwordx4 v[160:161], off
	s_barrier
	s_waitcnt lgkmcnt(0)
	s_setprio 1
	s_waitcnt lgkmcnt(0)
	v_mfma_f32_16x16x32_bf16 v[62:65], v[130:133], v[208:211], 0
	v_mfma_f32_16x16x32_bf16 v[58:61], v[200:203], v[208:211], 0
	v_mfma_f32_16x16x32_bf16 v[46:49], v[130:133], v[220:223], 0
	v_mfma_f32_16x16x32_bf16 v[42:45], v[200:203], v[220:223], 0
	v_mfma_f32_16x16x32_bf16 v[30:33], v[130:133], v[228:231], 0
	v_mfma_f32_16x16x32_bf16 v[26:29], v[200:203], v[228:231], 0
	v_mfma_f32_16x16x32_bf16 v[14:17], v[130:133], v[236:239], 0
	v_mfma_f32_16x16x32_bf16 v[10:13], v[200:203], v[236:239], 0
	v_mfma_f32_16x16x32_bf16 v[62:65], v[134:137], v[212:215], v[62:65]
	v_mfma_f32_16x16x32_bf16 v[58:61], v[204:207], v[212:215], v[58:61]
	v_mfma_f32_16x16x32_bf16 v[46:49], v[134:137], v[224:227], v[46:49]
	v_mfma_f32_16x16x32_bf16 v[42:45], v[204:207], v[224:227], v[42:45]
	v_mfma_f32_16x16x32_bf16 v[30:33], v[134:137], v[232:235], v[30:33]
	v_mfma_f32_16x16x32_bf16 v[26:29], v[204:207], v[232:235], v[26:29]
	v_mfma_f32_16x16x32_bf16 v[14:17], v[134:137], v[240:243], v[14:17]
	v_mfma_f32_16x16x32_bf16 v[10:13], v[204:207], v[240:243], v[10:13]
	s_setprio 0
	s_barrier
	s_add_u32 s68, s8, 0x80000
	s_addc_u32 s69, s9, 0
	s_add_i32 s72, s59, s3
	s_mov_b32 m0, s72
	s_nop 0
	global_load_lds_dwordx4 v140, s[68:69]
	s_add_i32 m0, s72, 0x2000
	s_nop 0
	global_load_lds_dwordx4 v144, s[68:69]
	s_waitcnt vmcnt(6)
	s_barrier
	s_setprio 1
	v_mfma_f32_16x16x32_bf16 v[54:57], v[244:247], v[208:211], 0
	v_mfma_f32_16x16x32_bf16 v[50:53], v[150:153], v[208:211], 0
	v_mfma_f32_16x16x32_bf16 v[38:41], v[244:247], v[220:223], 0
	v_mfma_f32_16x16x32_bf16 v[34:37], v[150:153], v[220:223], 0
	v_mfma_f32_16x16x32_bf16 v[22:25], v[244:247], v[228:231], 0
	v_mfma_f32_16x16x32_bf16 v[18:21], v[150:153], v[228:231], 0
	v_mfma_f32_16x16x32_bf16 v[6:9], v[244:247], v[236:239], 0
	v_mfma_f32_16x16x32_bf16 v[2:5], v[150:153], v[236:239], 0
	v_mfma_f32_16x16x32_bf16 v[54:57], v[248:251], v[212:215], v[54:57]
	v_mfma_f32_16x16x32_bf16 v[50:53], v[176:179], v[212:215], v[50:53]
	v_mfma_f32_16x16x32_bf16 v[38:41], v[248:251], v[224:227], v[38:41]
	v_mfma_f32_16x16x32_bf16 v[34:37], v[176:179], v[224:227], v[34:37]
	v_mfma_f32_16x16x32_bf16 v[22:25], v[248:251], v[232:235], v[22:25]
	v_mfma_f32_16x16x32_bf16 v[18:21], v[176:179], v[232:235], v[18:21]
	v_mfma_f32_16x16x32_bf16 v[6:9], v[248:251], v[240:243], v[6:9]
	v_mfma_f32_16x16x32_bf16 v[2:5], v[176:179], v[240:243], v[2:5]
	s_setprio 0
	s_add_i32 s68, 0, 0x18000
	v_add_u32_e32 v154, s68, v157
	s_barrier
	ds_read_b128 v[130:133], v154
	ds_read_b128 v[134:137], v154 offset:1024
	ds_read_b128 v[150:153], v154 offset:2048
	ds_read_b128 v[176:179], v154 offset:3072
	s_add_u32 s54, s54, 0x80000
	s_addc_u32 s55, s55, 0
	s_mov_b32 m0, s26
	ds_read_b128 v[200:203], v193 offset:32768
	ds_read_b128 v[204:207], v193 offset:33792
	ds_read_b128 v[208:211], v193 offset:34816
	ds_read_b128 v[212:215], v193 offset:35840
	ds_read_b128 v[220:223], v193 offset:36864
	ds_read_b128 v[224:227], v193 offset:37888
	ds_read_b128 v[228:231], v193 offset:38912
	ds_read_b128 v[232:235], v193 offset:39936
	global_load_lds_dwordx4 v138, s[54:55]
	s_mov_b32 m0, s33
	s_nop 0
	global_load_lds_dwordx4 v142, s[54:55]
	s_waitcnt lgkmcnt(8)
	s_barrier
	s_waitcnt lgkmcnt(0)
	s_setprio 1
	s_waitcnt lgkmcnt(0)
	v_mfma_f32_16x16x32_bf16 v[126:129], v[130:133], v[200:203], v[126:129]
	v_mfma_f32_16x16x32_bf16 v[122:125], v[150:153], v[200:203], v[122:125]
	v_mfma_f32_16x16x32_bf16 v[110:113], v[130:133], v[208:211], v[110:113]
	v_mfma_f32_16x16x32_bf16 v[106:109], v[150:153], v[208:211], v[106:109]
	v_mfma_f32_16x16x32_bf16 v[94:97], v[130:133], v[220:223], v[94:97]
	v_mfma_f32_16x16x32_bf16 v[90:93], v[150:153], v[220:223], v[90:93]
	v_mfma_f32_16x16x32_bf16 v[78:81], v[130:133], v[228:231], v[78:81]
	v_mfma_f32_16x16x32_bf16 v[74:77], v[150:153], v[228:231], v[74:77]
	v_mfma_f32_16x16x32_bf16 v[126:129], v[134:137], v[204:207], v[126:129]
	v_mfma_f32_16x16x32_bf16 v[122:125], v[176:179], v[204:207], v[122:125]
	v_mfma_f32_16x16x32_bf16 v[110:113], v[134:137], v[212:215], v[110:113]
	v_mfma_f32_16x16x32_bf16 v[106:109], v[176:179], v[212:215], v[106:109]
	v_mfma_f32_16x16x32_bf16 v[94:97], v[134:137], v[224:227], v[94:97]
	v_mfma_f32_16x16x32_bf16 v[90:93], v[176:179], v[224:227], v[90:93]
	v_mfma_f32_16x16x32_bf16 v[78:81], v[134:137], v[232:235], v[78:81]
	v_mfma_f32_16x16x32_bf16 v[74:77], v[176:179], v[232:235], v[74:77]
	s_setprio 0
	s_barrier
	s_add_i32 s54, 0, 0x1c000
	s_add_i32 s55, s68, s3
	v_add_u32_e32 v154, s54, v157
	v_lshl_add_u64 v[186:187], v[186:187], 0, s[12:13]
	s_mov_b32 m0, s55
	ds_read_b128 v[236:239], v154
	ds_read_b128 v[240:243], v154 offset:1024
	ds_read_b128 v[244:247], v154 offset:2048
	ds_read_b128 v[248:251], v154 offset:3072
	global_load_lds_dwordx4 v[186:187], off
	v_lshl_add_u64 v[186:187], v[216:217], 0, s[12:13]
	s_add_i32 m0, s55, 0x2000
	s_nop 0
	global_load_lds_dwordx4 v[186:187], off
	s_barrier
	s_waitcnt lgkmcnt(0)
	s_setprio 1
	s_waitcnt lgkmcnt(0)
	v_mfma_f32_16x16x32_bf16 v[118:121], v[236:239], v[200:203], v[118:121]
	v_mfma_f32_16x16x32_bf16 v[114:117], v[244:247], v[200:203], v[114:117]
	v_mfma_f32_16x16x32_bf16 v[102:105], v[236:239], v[208:211], v[102:105]
	v_mfma_f32_16x16x32_bf16 v[98:101], v[244:247], v[208:211], v[98:101]
	v_mfma_f32_16x16x32_bf16 v[86:89], v[236:239], v[220:223], v[86:89]
	v_mfma_f32_16x16x32_bf16 v[82:85], v[244:247], v[220:223], v[82:85]
	v_mfma_f32_16x16x32_bf16 v[70:73], v[236:239], v[228:231], v[70:73]
	v_mfma_f32_16x16x32_bf16 v[66:69], v[244:247], v[228:231], v[66:69]
	v_mfma_f32_16x16x32_bf16 v[118:121], v[240:243], v[204:207], v[118:121]
	v_mfma_f32_16x16x32_bf16 v[114:117], v[248:251], v[204:207], v[114:117]
	v_mfma_f32_16x16x32_bf16 v[102:105], v[240:243], v[212:215], v[102:105]
	v_mfma_f32_16x16x32_bf16 v[98:101], v[248:251], v[212:215], v[98:101]
	v_mfma_f32_16x16x32_bf16 v[86:89], v[240:243], v[224:227], v[86:89]
	v_mfma_f32_16x16x32_bf16 v[82:85], v[248:251], v[224:227], v[82:85]
	v_mfma_f32_16x16x32_bf16 v[70:73], v[240:243], v[232:235], v[70:73]
	v_mfma_f32_16x16x32_bf16 v[66:69], v[248:251], v[232:235], v[66:69]
	s_setprio 0
	s_mov_b32 m0, s35
	v_lshl_add_u64 v[186:187], v[252:253], 0, s[12:13]
	s_barrier
	ds_read_b128 v[200:203], v193 offset:49152
	ds_read_b128 v[204:207], v193 offset:50176
	ds_read_b128 v[208:211], v193 offset:51200
	ds_read_b128 v[212:215], v193 offset:52224
	ds_read_b128 v[220:223], v193 offset:53248
	ds_read_b128 v[224:227], v193 offset:54272
	ds_read_b128 v[228:231], v193 offset:55296
	ds_read_b128 v[232:235], v193 offset:56320
	global_load_lds_dwordx4 v[186:187], off
	v_lshl_add_u64 v[160:161], v[160:161], 0, s[12:13]
	s_mov_b32 m0, s40
	s_nop 0
	global_load_lds_dwordx4 v[160:161], off
	s_barrier
	s_waitcnt lgkmcnt(0)
	s_setprio 1
	s_waitcnt lgkmcnt(0)
	v_mfma_f32_16x16x32_bf16 v[62:65], v[130:133], v[200:203], v[62:65]
	v_mfma_f32_16x16x32_bf16 v[58:61], v[150:153], v[200:203], v[58:61]
	v_mfma_f32_16x16x32_bf16 v[46:49], v[130:133], v[208:211], v[46:49]
	v_mfma_f32_16x16x32_bf16 v[42:45], v[150:153], v[208:211], v[42:45]
	v_mfma_f32_16x16x32_bf16 v[30:33], v[130:133], v[220:223], v[30:33]
	v_mfma_f32_16x16x32_bf16 v[26:29], v[150:153], v[220:223], v[26:29]
	v_mfma_f32_16x16x32_bf16 v[14:17], v[130:133], v[228:231], v[14:17]
	v_mfma_f32_16x16x32_bf16 v[10:13], v[150:153], v[228:231], v[10:13]
	v_mfma_f32_16x16x32_bf16 v[62:65], v[134:137], v[204:207], v[62:65]
	v_mfma_f32_16x16x32_bf16 v[58:61], v[176:179], v[204:207], v[58:61]
	v_mfma_f32_16x16x32_bf16 v[46:49], v[134:137], v[212:215], v[46:49]
	v_mfma_f32_16x16x32_bf16 v[42:45], v[176:179], v[212:215], v[42:45]
	v_mfma_f32_16x16x32_bf16 v[30:33], v[134:137], v[224:227], v[30:33]
	v_mfma_f32_16x16x32_bf16 v[26:29], v[176:179], v[224:227], v[26:29]
	v_mfma_f32_16x16x32_bf16 v[14:17], v[134:137], v[232:235], v[14:17]
	v_mfma_f32_16x16x32_bf16 v[10:13], v[176:179], v[232:235], v[10:13]
	s_setprio 0
	s_barrier
	s_add_u32 s8, s8, 0x80080
	s_addc_u32 s9, s9, 0
	s_add_i32 s54, s54, s3
	s_mov_b32 m0, s54
	s_nop 0
	global_load_lds_dwordx4 v140, s[8:9]
	s_add_i32 m0, s54, 0x2000
	s_nop 0
	global_load_lds_dwordx4 v144, s[8:9]
	s_waitcnt vmcnt(6)
	s_barrier
	s_setprio 1
	v_mfma_f32_16x16x32_bf16 v[54:57], v[236:239], v[200:203], v[54:57]
	v_mfma_f32_16x16x32_bf16 v[50:53], v[244:247], v[200:203], v[50:53]
	v_mfma_f32_16x16x32_bf16 v[38:41], v[236:239], v[208:211], v[38:41]
	v_mfma_f32_16x16x32_bf16 v[34:37], v[244:247], v[208:211], v[34:37]
	v_mfma_f32_16x16x32_bf16 v[22:25], v[236:239], v[220:223], v[22:25]
	v_mfma_f32_16x16x32_bf16 v[18:21], v[244:247], v[220:223], v[18:21]
	v_mfma_f32_16x16x32_bf16 v[6:9], v[236:239], v[228:231], v[6:9]
	v_mfma_f32_16x16x32_bf16 v[2:5], v[244:247], v[228:231], v[2:5]
	v_mfma_f32_16x16x32_bf16 v[54:57], v[240:243], v[204:207], v[54:57]
	v_mfma_f32_16x16x32_bf16 v[50:53], v[248:251], v[204:207], v[50:53]
	v_mfma_f32_16x16x32_bf16 v[38:41], v[240:243], v[212:215], v[38:41]
	v_mfma_f32_16x16x32_bf16 v[34:37], v[248:251], v[212:215], v[34:37]
	v_mfma_f32_16x16x32_bf16 v[22:25], v[240:243], v[224:227], v[22:25]
	v_mfma_f32_16x16x32_bf16 v[18:21], v[248:251], v[224:227], v[18:21]
	v_mfma_f32_16x16x32_bf16 v[6:9], v[240:243], v[232:235], v[6:9]
	v_mfma_f32_16x16x32_bf16 v[2:5], v[248:251], v[232:235], v[2:5]
	s_setprio 0
	s_add_i32 s67, s67, 2
	s_add_u32 s4, s4, 0x100
	s_addc_u32 s5, s5, 0
	s_add_u32 s65, s65, 0x100
	s_addc_u32 s66, s66, 0
	s_cmp_gt_u32 s67, 29
	s_barrier
	s_cbranch_scc1 .Lpeel_1037_after
.LBB0_1037:
	ds_read_b128 v[130:133], v192
	ds_read_b128 v[134:137], v192 offset:1024
	ds_read_b128 v[200:203], v192 offset:2048
	ds_read_b128 v[204:207], v192 offset:3072
	s_add_u32 s8, s4, 0xfff80080
	s_addc_u32 s9, s5, -1
	s_cmp_eq_u32 s67, 28
	s_cselect_b32 s55, s17, s9
	s_cselect_b32 s54, s63, s8
	s_cselect_b32 s9, s15, s66
	s_cselect_b32 s8, s64, s65
	s_add_i32 m0, s23, 0xc000
	ds_read_b128 v[208:211], v193
	ds_read_b128 v[212:215], v193 offset:1024
	ds_read_b128 v[220:223], v193 offset:2048
	ds_read_b128 v[224:227], v193 offset:3072
	ds_read_b128 v[228:231], v193 offset:4096
	ds_read_b128 v[232:235], v193 offset:5120
	ds_read_b128 v[236:239], v193 offset:6144
	ds_read_b128 v[240:243], v193 offset:7168
	global_load_lds_dwordx4 v146, s[4:5]
	s_add_i32 m0, s23, 0xe000
	s_nop 0
	global_load_lds_dwordx4 v148, s[4:5]
	s_waitcnt lgkmcnt(8)
	s_barrier
	s_waitcnt lgkmcnt(0)
	s_setprio 1
	s_waitcnt lgkmcnt(0)
	v_mfma_f32_16x16x32_bf16 v[126:129], v[130:133], v[208:211], v[126:129]
	v_mfma_f32_16x16x32_bf16 v[122:125], v[200:203], v[208:211], v[122:125]
	v_mfma_f32_16x16x32_bf16 v[110:113], v[130:133], v[220:223], v[110:113]
	v_mfma_f32_16x16x32_bf16 v[106:109], v[200:203], v[220:223], v[106:109]
	v_mfma_f32_16x16x32_bf16 v[94:97], v[130:133], v[228:231], v[94:97]
	v_mfma_f32_16x16x32_bf16 v[90:93], v[200:203], v[228:231], v[90:93]
	v_mfma_f32_16x16x32_bf16 v[78:81], v[130:133], v[236:239], v[78:81]
	v_mfma_f32_16x16x32_bf16 v[74:77], v[200:203], v[236:239], v[74:77]
	v_mfma_f32_16x16x32_bf16 v[126:129], v[134:137], v[212:215], v[126:129]
	v_mfma_f32_16x16x32_bf16 v[122:125], v[204:207], v[212:215], v[122:125]
	v_mfma_f32_16x16x32_bf16 v[110:113], v[134:137], v[224:227], v[110:113]
	v_mfma_f32_16x16x32_bf16 v[106:109], v[204:207], v[224:227], v[106:109]
	v_mfma_f32_16x16x32_bf16 v[94:97], v[134:137], v[232:235], v[94:97]
	v_mfma_f32_16x16x32_bf16 v[90:93], v[204:207], v[232:235], v[90:93]
	v_mfma_f32_16x16x32_bf16 v[78:81], v[134:137], v[240:243], v[78:81]
	v_mfma_f32_16x16x32_bf16 v[74:77], v[204:207], v[240:243], v[74:77]
	s_setprio 0
	s_barrier
	s_add_i32 s68, s58, s3
	v_lshl_add_u64 v[186:187], s[8:9], 0, v[140:141]
	s_mov_b32 m0, s68
	ds_read_b128 v[244:247], v194
	ds_read_b128 v[248:251], v194 offset:1024
	ds_read_b128 v[150:153], v194 offset:2048
	ds_read_b128 v[176:179], v194 offset:3072
	global_load_lds_dwordx4 v[186:187], off
	v_lshl_add_u64 v[216:217], s[8:9], 0, v[144:145]
	s_add_i32 m0, s68, 0x2000
	s_nop 0
	global_load_lds_dwordx4 v[216:217], off
	s_barrier
	s_waitcnt lgkmcnt(0)
	s_setprio 1
	s_waitcnt lgkmcnt(0)
	v_mfma_f32_16x16x32_bf16 v[118:121], v[244:247], v[208:211], v[118:121]
	v_mfma_f32_16x16x32_bf16 v[114:117], v[150:153], v[208:211], v[114:117]
	v_mfma_f32_16x16x32_bf16 v[102:105], v[244:247], v[220:223], v[102:105]
	v_mfma_f32_16x16x32_bf16 v[98:101], v[150:153], v[220:223], v[98:101]
	v_mfma_f32_16x16x32_bf16 v[86:89], v[244:247], v[228:231], v[86:89]
	v_mfma_f32_16x16x32_bf16 v[82:85], v[150:153], v[228:231], v[82:85]
	v_mfma_f32_16x16x32_bf16 v[70:73], v[244:247], v[236:239], v[70:73]
	v_mfma_f32_16x16x32_bf16 v[66:69], v[150:153], v[236:239], v[66:69]
	v_mfma_f32_16x16x32_bf16 v[118:121], v[248:251], v[212:215], v[118:121]
	v_mfma_f32_16x16x32_bf16 v[114:117], v[176:179], v[212:215], v[114:117]
	v_mfma_f32_16x16x32_bf16 v[102:105], v[248:251], v[224:227], v[102:105]
	v_mfma_f32_16x16x32_bf16 v[98:101], v[176:179], v[224:227], v[98:101]
	v_mfma_f32_16x16x32_bf16 v[86:89], v[248:251], v[232:235], v[86:89]
	v_mfma_f32_16x16x32_bf16 v[82:85], v[176:179], v[232:235], v[82:85]
	v_mfma_f32_16x16x32_bf16 v[70:73], v[248:251], v[240:243], v[70:73]
	v_mfma_f32_16x16x32_bf16 v[66:69], v[176:179], v[240:243], v[66:69]
	s_setprio 0
	s_mov_b32 m0, s23
	v_lshl_add_u64 v[252:253], s[54:55], 0, v[138:139]
	s_barrier
	ds_read_b128 v[208:211], v193 offset:16384
	ds_read_b128 v[212:215], v193 offset:17408
	ds_read_b128 v[220:223], v193 offset:18432
	ds_read_b128 v[224:227], v193 offset:19456
	ds_read_b128 v[228:231], v193 offset:20480
	ds_read_b128 v[232:235], v193 offset:21504
	ds_read_b128 v[236:239], v193 offset:22528
	ds_read_b128 v[240:243], v193 offset:23552
	global_load_lds_dwordx4 v[252:253], off
	v_lshl_add_u64 v[160:161], s[54:55], 0, v[142:143]
	s_mov_b32 m0, s25
	s_nop 0
	global_load_lds_dwordx4 v[160:161], off
	s_barrier
	s_waitcnt lgkmcnt(0)
	s_setprio 1
	s_waitcnt lgkmcnt(0)
	v_mfma_f32_16x16x32_bf16 v[62:65], v[130:133], v[208:211], v[62:65]
	v_mfma_f32_16x16x32_bf16 v[58:61], v[200:203], v[208:211], v[58:61]
	v_mfma_f32_16x16x32_bf16 v[46:49], v[130:133], v[220:223], v[46:49]
	v_mfma_f32_16x16x32_bf16 v[42:45], v[200:203], v[220:223], v[42:45]
	v_mfma_f32_16x16x32_bf16 v[30:33], v[130:133], v[228:231], v[30:33]
	v_mfma_f32_16x16x32_bf16 v[26:29], v[200:203], v[228:231], v[26:29]
	v_mfma_f32_16x16x32_bf16 v[14:17], v[130:133], v[236:239], v[14:17]
	v_mfma_f32_16x16x32_bf16 v[10:13], v[200:203], v[236:239], v[10:13]
	v_mfma_f32_16x16x32_bf16 v[62:65], v[134:137], v[212:215], v[62:65]
	v_mfma_f32_16x16x32_bf16 v[58:61], v[204:207], v[212:215], v[58:61]
	v_mfma_f32_16x16x32_bf16 v[46:49], v[134:137], v[224:227], v[46:49]
	v_mfma_f32_16x16x32_bf16 v[42:45], v[204:207], v[224:227], v[42:45]
	v_mfma_f32_16x16x32_bf16 v[30:33], v[134:137], v[232:235], v[30:33]
	v_mfma_f32_16x16x32_bf16 v[26:29], v[204:207], v[232:235], v[26:29]
	v_mfma_f32_16x16x32_bf16 v[14:17], v[134:137], v[240:243], v[14:17]
	v_mfma_f32_16x16x32_bf16 v[10:13], v[204:207], v[240:243], v[10:13]
	s_setprio 0
	s_barrier
	s_add_u32 s68, s8, 0x80000
	s_addc_u32 s69, s9, 0
	s_add_i32 s72, s59, s3
	s_mov_b32 m0, s72
	s_nop 0
	global_load_lds_dwordx4 v140, s[68:69]
	s_add_i32 m0, s72, 0x2000
	s_nop 0
	global_load_lds_dwordx4 v144, s[68:69]
	s_waitcnt vmcnt(6)
	s_barrier
	s_setprio 1
	v_mfma_f32_16x16x32_bf16 v[54:57], v[244:247], v[208:211], v[54:57]
	v_mfma_f32_16x16x32_bf16 v[50:53], v[150:153], v[208:211], v[50:53]
	v_mfma_f32_16x16x32_bf16 v[38:41], v[244:247], v[220:223], v[38:41]
	v_mfma_f32_16x16x32_bf16 v[34:37], v[150:153], v[220:223], v[34:37]
	v_mfma_f32_16x16x32_bf16 v[22:25], v[244:247], v[228:231], v[22:25]
	v_mfma_f32_16x16x32_bf16 v[18:21], v[150:153], v[228:231], v[18:21]
	v_mfma_f32_16x16x32_bf16 v[6:9], v[244:247], v[236:239], v[6:9]
	v_mfma_f32_16x16x32_bf16 v[2:5], v[150:153], v[236:239], v[2:5]
	v_mfma_f32_16x16x32_bf16 v[54:57], v[248:251], v[212:215], v[54:57]
	v_mfma_f32_16x16x32_bf16 v[50:53], v[176:179], v[212:215], v[50:53]
	v_mfma_f32_16x16x32_bf16 v[38:41], v[248:251], v[224:227], v[38:41]
	v_mfma_f32_16x16x32_bf16 v[34:37], v[176:179], v[224:227], v[34:37]
	v_mfma_f32_16x16x32_bf16 v[22:25], v[248:251], v[232:235], v[22:25]
	v_mfma_f32_16x16x32_bf16 v[18:21], v[176:179], v[232:235], v[18:21]
	v_mfma_f32_16x16x32_bf16 v[6:9], v[248:251], v[240:243], v[6:9]
	v_mfma_f32_16x16x32_bf16 v[2:5], v[176:179], v[240:243], v[2:5]
	s_setprio 0
	s_add_i32 s68, 0, 0x18000
	v_add_u32_e32 v154, s68, v157
	s_barrier
	ds_read_b128 v[130:133], v154
	ds_read_b128 v[134:137], v154 offset:1024
	ds_read_b128 v[150:153], v154 offset:2048
	ds_read_b128 v[176:179], v154 offset:3072
	s_add_u32 s54, s54, 0x80000
	s_addc_u32 s55, s55, 0
	s_mov_b32 m0, s26
	ds_read_b128 v[200:203], v193 offset:32768
	ds_read_b128 v[204:207], v193 offset:33792
	ds_read_b128 v[208:211], v193 offset:34816
	ds_read_b128 v[212:215], v193 offset:35840
	ds_read_b128 v[220:223], v193 offset:36864
	ds_read_b128 v[224:227], v193 offset:37888
	ds_read_b128 v[228:231], v193 offset:38912
	ds_read_b128 v[232:235], v193 offset:39936
	global_load_lds_dwordx4 v138, s[54:55]
	s_mov_b32 m0, s33
	s_nop 0
	global_load_lds_dwordx4 v142, s[54:55]
	s_waitcnt lgkmcnt(8)
	s_barrier
	s_waitcnt lgkmcnt(0)
	s_setprio 1
	s_waitcnt lgkmcnt(0)
	v_mfma_f32_16x16x32_bf16 v[126:129], v[130:133], v[200:203], v[126:129]
	v_mfma_f32_16x16x32_bf16 v[122:125], v[150:153], v[200:203], v[122:125]
	v_mfma_f32_16x16x32_bf16 v[110:113], v[130:133], v[208:211], v[110:113]
	v_mfma_f32_16x16x32_bf16 v[106:109], v[150:153], v[208:211], v[106:109]
	v_mfma_f32_16x16x32_bf16 v[94:97], v[130:133], v[220:223], v[94:97]
	v_mfma_f32_16x16x32_bf16 v[90:93], v[150:153], v[220:223], v[90:93]
	v_mfma_f32_16x16x32_bf16 v[78:81], v[130:133], v[228:231], v[78:81]
	v_mfma_f32_16x16x32_bf16 v[74:77], v[150:153], v[228:231], v[74:77]
	v_mfma_f32_16x16x32_bf16 v[126:129], v[134:137], v[204:207], v[126:129]
	v_mfma_f32_16x16x32_bf16 v[122:125], v[176:179], v[204:207], v[122:125]
	v_mfma_f32_16x16x32_bf16 v[110:113], v[134:137], v[212:215], v[110:113]
	v_mfma_f32_16x16x32_bf16 v[106:109], v[176:179], v[212:215], v[106:109]
	v_mfma_f32_16x16x32_bf16 v[94:97], v[134:137], v[224:227], v[94:97]
	v_mfma_f32_16x16x32_bf16 v[90:93], v[176:179], v[224:227], v[90:93]
	v_mfma_f32_16x16x32_bf16 v[78:81], v[134:137], v[232:235], v[78:81]
	v_mfma_f32_16x16x32_bf16 v[74:77], v[176:179], v[232:235], v[74:77]
	s_setprio 0
	s_barrier
	s_add_i32 s54, 0, 0x1c000
	s_add_i32 s55, s68, s3
	v_add_u32_e32 v154, s54, v157
	v_lshl_add_u64 v[186:187], v[186:187], 0, s[12:13]
	s_mov_b32 m0, s55
	ds_read_b128 v[236:239], v154
	ds_read_b128 v[240:243], v154 offset:1024
	ds_read_b128 v[244:247], v154 offset:2048
	ds_read_b128 v[248:251], v154 offset:3072
	global_load_lds_dwordx4 v[186:187], off
	v_lshl_add_u64 v[186:187], v[216:217], 0, s[12:13]
	s_add_i32 m0, s55, 0x2000
	s_nop 0
	global_load_lds_dwordx4 v[186:187], off
	s_barrier
	s_waitcnt lgkmcnt(0)
	s_setprio 1
	s_waitcnt lgkmcnt(0)
	v_mfma_f32_16x16x32_bf16 v[118:121], v[236:239], v[200:203], v[118:121]
	v_mfma_f32_16x16x32_bf16 v[114:117], v[244:247], v[200:203], v[114:117]
	v_mfma_f32_16x16x32_bf16 v[102:105], v[236:239], v[208:211], v[102:105]
	v_mfma_f32_16x16x32_bf16 v[98:101], v[244:247], v[208:211], v[98:101]
	v_mfma_f32_16x16x32_bf16 v[86:89], v[236:239], v[220:223], v[86:89]
	v_mfma_f32_16x16x32_bf16 v[82:85], v[244:247], v[220:223], v[82:85]
	v_mfma_f32_16x16x32_bf16 v[70:73], v[236:239], v[228:231], v[70:73]
	v_mfma_f32_16x16x32_bf16 v[66:69], v[244:247], v[228:231], v[66:69]
	v_mfma_f32_16x16x32_bf16 v[118:121], v[240:243], v[204:207], v[118:121]
	v_mfma_f32_16x16x32_bf16 v[114:117], v[248:251], v[204:207], v[114:117]
	v_mfma_f32_16x16x32_bf16 v[102:105], v[240:243], v[212:215], v[102:105]
	v_mfma_f32_16x16x32_bf16 v[98:101], v[248:251], v[212:215], v[98:101]
	v_mfma_f32_16x16x32_bf16 v[86:89], v[240:243], v[224:227], v[86:89]
	v_mfma_f32_16x16x32_bf16 v[82:85], v[248:251], v[224:227], v[82:85]
	v_mfma_f32_16x16x32_bf16 v[70:73], v[240:243], v[232:235], v[70:73]
	v_mfma_f32_16x16x32_bf16 v[66:69], v[248:251], v[232:235], v[66:69]
	s_setprio 0
	s_mov_b32 m0, s35
	v_lshl_add_u64 v[186:187], v[252:253], 0, s[12:13]
	s_barrier
	ds_read_b128 v[200:203], v193 offset:49152
	ds_read_b128 v[204:207], v193 offset:50176
	ds_read_b128 v[208:211], v193 offset:51200
	ds_read_b128 v[212:215], v193 offset:52224
	ds_read_b128 v[220:223], v193 offset:53248
	ds_read_b128 v[224:227], v193 offset:54272
	ds_read_b128 v[228:231], v193 offset:55296
	ds_read_b128 v[232:235], v193 offset:56320
	global_load_lds_dwordx4 v[186:187], off
	v_lshl_add_u64 v[160:161], v[160:161], 0, s[12:13]
	s_mov_b32 m0, s40
	s_nop 0
	global_load_lds_dwordx4 v[160:161], off
	s_barrier
	s_waitcnt lgkmcnt(0)
	s_setprio 1
	s_waitcnt lgkmcnt(0)
	v_mfma_f32_16x16x32_bf16 v[62:65], v[130:133], v[200:203], v[62:65]
	v_mfma_f32_16x16x32_bf16 v[58:61], v[150:153], v[200:203], v[58:61]
	v_mfma_f32_16x16x32_bf16 v[46:49], v[130:133], v[208:211], v[46:49]
	v_mfma_f32_16x16x32_bf16 v[42:45], v[150:153], v[208:211], v[42:45]
	v_mfma_f32_16x16x32_bf16 v[30:33], v[130:133], v[220:223], v[30:33]
	v_mfma_f32_16x16x32_bf16 v[26:29], v[150:153], v[220:223], v[26:29]
	v_mfma_f32_16x16x32_bf16 v[14:17], v[130:133], v[228:231], v[14:17]
	v_mfma_f32_16x16x32_bf16 v[10:13], v[150:153], v[228:231], v[10:13]
	v_mfma_f32_16x16x32_bf16 v[62:65], v[134:137], v[204:207], v[62:65]
	v_mfma_f32_16x16x32_bf16 v[58:61], v[176:179], v[204:207], v[58:61]
	v_mfma_f32_16x16x32_bf16 v[46:49], v[134:137], v[212:215], v[46:49]
	v_mfma_f32_16x16x32_bf16 v[42:45], v[176:179], v[212:215], v[42:45]
	v_mfma_f32_16x16x32_bf16 v[30:33], v[134:137], v[224:227], v[30:33]
	v_mfma_f32_16x16x32_bf16 v[26:29], v[176:179], v[224:227], v[26:29]
	v_mfma_f32_16x16x32_bf16 v[14:17], v[134:137], v[232:235], v[14:17]
	v_mfma_f32_16x16x32_bf16 v[10:13], v[176:179], v[232:235], v[10:13]
	s_setprio 0
	s_barrier
	s_add_u32 s8, s8, 0x80080
	s_addc_u32 s9, s9, 0
	s_add_i32 s54, s54, s3
	s_mov_b32 m0, s54
	s_nop 0
	global_load_lds_dwordx4 v140, s[8:9]
	s_add_i32 m0, s54, 0x2000
	s_nop 0
	global_load_lds_dwordx4 v144, s[8:9]
	s_waitcnt vmcnt(6)
	s_barrier
	s_setprio 1
	v_mfma_f32_16x16x32_bf16 v[54:57], v[236:239], v[200:203], v[54:57]
	v_mfma_f32_16x16x32_bf16 v[50:53], v[244:247], v[200:203], v[50:53]
	v_mfma_f32_16x16x32_bf16 v[38:41], v[236:239], v[208:211], v[38:41]
	v_mfma_f32_16x16x32_bf16 v[34:37], v[244:247], v[208:211], v[34:37]
	v_mfma_f32_16x16x32_bf16 v[22:25], v[236:239], v[220:223], v[22:25]
	v_mfma_f32_16x16x32_bf16 v[18:21], v[244:247], v[220:223], v[18:21]
	v_mfma_f32_16x16x32_bf16 v[6:9], v[236:239], v[228:231], v[6:9]
	v_mfma_f32_16x16x32_bf16 v[2:5], v[244:247], v[228:231], v[2:5]
	v_mfma_f32_16x16x32_bf16 v[54:57], v[240:243], v[204:207], v[54:57]
	v_mfma_f32_16x16x32_bf16 v[50:53], v[248:251], v[204:207], v[50:53]
	v_mfma_f32_16x16x32_bf16 v[38:41], v[240:243], v[212:215], v[38:41]
	v_mfma_f32_16x16x32_bf16 v[34:37], v[248:251], v[212:215], v[34:37]
	v_mfma_f32_16x16x32_bf16 v[22:25], v[240:243], v[224:227], v[22:25]
	v_mfma_f32_16x16x32_bf16 v[18:21], v[248:251], v[224:227], v[18:21]
	v_mfma_f32_16x16x32_bf16 v[6:9], v[240:243], v[232:235], v[6:9]
	v_mfma_f32_16x16x32_bf16 v[2:5], v[248:251], v[232:235], v[2:5]
	s_setprio 0
	s_add_i32 s67, s67, 2
	s_add_u32 s4, s4, 0x100
	s_addc_u32 s5, s5, 0
	s_add_u32 s65, s65, 0x100
	s_addc_u32 s66, s66, 0
	s_cmp_gt_u32 s67, 29
	s_barrier
	s_cbranch_scc0 .LBB0_1037

.LBB0_1238:
	s_ashr_i32 s21, s20, 31
	v_cmp_lt_i64_e32 vcc, s[22:23], v[138:139]
	s_lshl_b64 s[22:23], s[20:21], 20
	s_add_u32 s22, s4, s22
	s_addc_u32 s23, s5, s23
	s_and_b64 s[24:25], vcc, exec
	s_cselect_b32 s21, s23, s57
	s_cselect_b32 s71, s22, s56
	s_ashr_i32 s19, s18, 31
	s_lshl_b64 s[24:25], s[18:19], 20
	v_readlane_b32 s60, v254, 32
	v_readlane_b32 s61, v254, 33
	s_add_u32 s24, s60, s24
	s_addc_u32 s25, s61, s25
	s_and_b64 s[60:61], vcc, exec
	s_cselect_b32 s19, s25, s59
	s_cselect_b32 s72, s24, s58
	s_add_u32 s56, s56, 0x80080
	s_addc_u32 s57, s57, 0
	s_add_u32 s73, s58, 0x100
	v_mov_b32_e32 v2, 0
	s_addc_u32 s74, s59, 0
	s_mov_b32 s75, -2
	ds_read_b128 v[150:153], v147
	ds_read_b128 v[154:157], v147 offset:1024
	ds_read_b128 v[158:161], v147 offset:2048
	ds_read_b128 v[162:165], v147 offset:3072
	s_add_u32 s58, s56, 0xfff80080
	s_addc_u32 s59, s57, -1
	s_cmp_eq_u32 s75, 28
	s_cselect_b32 s61, s21, s59
	s_cselect_b32 s60, s71, s58
	s_cselect_b32 s59, s19, s74
	s_cselect_b32 s58, s72, s73
	s_add_i32 m0, s33, 0xc000
	ds_read_b128 v[166:169], v148
	ds_read_b128 v[170:173], v148 offset:1024
	ds_read_b128 v[174:177], v148 offset:2048
	ds_read_b128 v[178:181], v148 offset:3072
	ds_read_b128 v[182:185], v148 offset:4096
	ds_read_b128 v[186:189], v148 offset:5120
	ds_read_b128 v[190:193], v148 offset:6144
	ds_read_b128 v[194:197], v148 offset:7168
	global_load_lds_dwordx4 v134, s[56:57]
	s_add_i32 m0, s33, 0xe000
	s_nop 0
	global_load_lds_dwordx4 v136, s[56:57]
	s_waitcnt lgkmcnt(8)
	s_barrier
	s_waitcnt lgkmcnt(0)
	s_setprio 1
	s_waitcnt lgkmcnt(0)
	v_mfma_f32_16x16x32_bf16 v[126:129], v[150:153], v[166:169], 0
	v_mfma_f32_16x16x32_bf16 v[122:125], v[158:161], v[166:169], 0
	v_mfma_f32_16x16x32_bf16 v[118:121], v[150:153], v[174:177], 0
	v_mfma_f32_16x16x32_bf16 v[114:117], v[158:161], v[174:177], 0
	v_mfma_f32_16x16x32_bf16 v[94:97], v[150:153], v[182:185], 0
	v_mfma_f32_16x16x32_bf16 v[90:93], v[158:161], v[182:185], 0
	v_mfma_f32_16x16x32_bf16 v[86:89], v[150:153], v[190:193], 0
	v_mfma_f32_16x16x32_bf16 v[82:85], v[158:161], v[190:193], 0
	v_mfma_f32_16x16x32_bf16 v[126:129], v[154:157], v[170:173], v[126:129]
	v_mfma_f32_16x16x32_bf16 v[122:125], v[162:165], v[170:173], v[122:125]
	v_mfma_f32_16x16x32_bf16 v[118:121], v[154:157], v[178:181], v[118:121]
	v_mfma_f32_16x16x32_bf16 v[114:117], v[162:165], v[178:181], v[114:117]
	v_mfma_f32_16x16x32_bf16 v[94:97], v[154:157], v[186:189], v[94:97]
	v_mfma_f32_16x16x32_bf16 v[90:93], v[162:165], v[186:189], v[90:93]
	v_mfma_f32_16x16x32_bf16 v[86:89], v[154:157], v[194:197], v[86:89]
	v_mfma_f32_16x16x32_bf16 v[82:85], v[162:165], v[194:197], v[82:85]
	s_setprio 0
	s_barrier
	s_add_i32 s76, s64, s26
	v_lshl_add_u64 v[142:143], s[58:59], 0, v[130:131]
	s_mov_b32 m0, s76
	ds_read_b128 v[198:201], v149
	ds_read_b128 v[202:205], v149 offset:1024
	ds_read_b128 v[206:209], v149 offset:2048
	ds_read_b128 v[210:213], v149 offset:3072
	global_load_lds_dwordx4 v[142:143], off
	v_lshl_add_u64 v[214:215], s[58:59], 0, v[132:133]
	s_add_i32 m0, s76, 0x2000
	s_nop 0
	global_load_lds_dwordx4 v[214:215], off
	s_barrier
	s_waitcnt lgkmcnt(0)
	s_setprio 1
	s_waitcnt lgkmcnt(0)
	v_mfma_f32_16x16x32_bf16 v[110:113], v[198:201], v[166:169], 0
	v_mfma_f32_16x16x32_bf16 v[106:109], v[206:209], v[166:169], 0
	v_mfma_f32_16x16x32_bf16 v[102:105], v[198:201], v[174:177], 0
	v_mfma_f32_16x16x32_bf16 v[98:101], v[206:209], v[174:177], 0
	v_mfma_f32_16x16x32_bf16 v[78:81], v[198:201], v[182:185], 0
	v_mfma_f32_16x16x32_bf16 v[74:77], v[206:209], v[182:185], 0
	v_mfma_f32_16x16x32_bf16 v[70:73], v[198:201], v[190:193], 0
	v_mfma_f32_16x16x32_bf16 v[66:69], v[206:209], v[190:193], 0
	v_mfma_f32_16x16x32_bf16 v[110:113], v[202:205], v[170:173], v[110:113]
	v_mfma_f32_16x16x32_bf16 v[106:109], v[210:213], v[170:173], v[106:109]
	v_mfma_f32_16x16x32_bf16 v[102:105], v[202:205], v[178:181], v[102:105]
	v_mfma_f32_16x16x32_bf16 v[98:101], v[210:213], v[178:181], v[98:101]
	v_mfma_f32_16x16x32_bf16 v[78:81], v[202:205], v[186:189], v[78:81]
	v_mfma_f32_16x16x32_bf16 v[74:77], v[210:213], v[186:189], v[74:77]
	v_mfma_f32_16x16x32_bf16 v[70:73], v[202:205], v[194:197], v[70:73]
	v_mfma_f32_16x16x32_bf16 v[66:69], v[210:213], v[194:197], v[66:69]
	s_setprio 0
	s_mov_b32 m0, s33
	v_lshl_add_u64 v[216:217], s[60:61], 0, v[130:131]
	s_barrier
	ds_read_b128 v[166:169], v148 offset:16384
	ds_read_b128 v[170:173], v148 offset:17408
	ds_read_b128 v[174:177], v148 offset:18432
	ds_read_b128 v[178:181], v148 offset:19456
	ds_read_b128 v[182:185], v148 offset:20480
	ds_read_b128 v[186:189], v148 offset:21504
	ds_read_b128 v[190:193], v148 offset:22528
	ds_read_b128 v[194:197], v148 offset:23552
	global_load_lds_dwordx4 v[216:217], off
	v_lshl_add_u64 v[220:221], s[60:61], 0, v[132:133]
	s_mov_b32 m0, s34
	s_nop 0
	global_load_lds_dwordx4 v[220:221], off
	s_barrier
	s_waitcnt lgkmcnt(0)
	s_setprio 1
	s_waitcnt lgkmcnt(0)
	v_mfma_f32_16x16x32_bf16 v[62:65], v[150:153], v[166:169], 0
	v_mfma_f32_16x16x32_bf16 v[58:61], v[158:161], v[166:169], 0
	v_mfma_f32_16x16x32_bf16 v[54:57], v[150:153], v[174:177], 0
	v_mfma_f32_16x16x32_bf16 v[50:53], v[158:161], v[174:177], 0
	v_mfma_f32_16x16x32_bf16 v[30:33], v[150:153], v[182:185], 0
	v_mfma_f32_16x16x32_bf16 v[26:29], v[158:161], v[182:185], 0
	v_mfma_f32_16x16x32_bf16 v[22:25], v[150:153], v[190:193], 0
	v_mfma_f32_16x16x32_bf16 v[14:17], v[158:161], v[190:193], 0
	v_mfma_f32_16x16x32_bf16 v[62:65], v[154:157], v[170:173], v[62:65]
	v_mfma_f32_16x16x32_bf16 v[58:61], v[162:165], v[170:173], v[58:61]
	v_mfma_f32_16x16x32_bf16 v[54:57], v[154:157], v[178:181], v[54:57]
	v_mfma_f32_16x16x32_bf16 v[50:53], v[162:165], v[178:181], v[50:53]
	v_mfma_f32_16x16x32_bf16 v[30:33], v[154:157], v[186:189], v[30:33]
	v_mfma_f32_16x16x32_bf16 v[26:29], v[162:165], v[186:189], v[26:29]
	v_mfma_f32_16x16x32_bf16 v[22:25], v[154:157], v[194:197], v[22:25]
	v_mfma_f32_16x16x32_bf16 v[14:17], v[162:165], v[194:197], v[14:17]
	s_setprio 0
	s_barrier
	s_add_u32 s76, s58, 0x80000
	s_addc_u32 s77, s59, 0
	s_add_i32 s78, s65, s26
	s_mov_b32 m0, s78
	s_nop 0
	global_load_lds_dwordx4 v130, s[76:77]
	s_add_i32 m0, s78, 0x2000
	s_nop 0
	global_load_lds_dwordx4 v132, s[76:77]
	s_waitcnt vmcnt(6)
	s_barrier
	s_setprio 1
	v_mfma_f32_16x16x32_bf16 v[46:49], v[198:201], v[166:169], 0
	v_mfma_f32_16x16x32_bf16 v[42:45], v[206:209], v[166:169], 0
	v_mfma_f32_16x16x32_bf16 v[38:41], v[198:201], v[174:177], 0
	v_mfma_f32_16x16x32_bf16 v[34:37], v[206:209], v[174:177], 0
	v_mfma_f32_16x16x32_bf16 v[18:21], v[198:201], v[182:185], 0
	v_mfma_f32_16x16x32_bf16 v[10:13], v[206:209], v[182:185], 0
	v_mfma_f32_16x16x32_bf16 v[6:9], v[198:201], v[190:193], 0
	v_mfma_f32_16x16x32_bf16 v[2:5], v[206:209], v[190:193], 0
	v_mfma_f32_16x16x32_bf16 v[46:49], v[202:205], v[170:173], v[46:49]
	v_mfma_f32_16x16x32_bf16 v[42:45], v[210:213], v[170:173], v[42:45]
	v_mfma_f32_16x16x32_bf16 v[38:41], v[202:205], v[178:181], v[38:41]
	v_mfma_f32_16x16x32_bf16 v[34:37], v[210:213], v[178:181], v[34:37]
	v_mfma_f32_16x16x32_bf16 v[18:21], v[202:205], v[186:189], v[18:21]
	v_mfma_f32_16x16x32_bf16 v[10:13], v[210:213], v[186:189], v[10:13]
	v_mfma_f32_16x16x32_bf16 v[6:9], v[202:205], v[194:197], v[6:9]
	v_mfma_f32_16x16x32_bf16 v[2:5], v[210:213], v[194:197], v[2:5]
	s_setprio 0
	s_add_i32 s76, 0, 0x18000
	v_add_u32_e32 v1, s76, v145
	s_barrier
	ds_read_b128 v[150:153], v1
	ds_read_b128 v[154:157], v1 offset:1024
	ds_read_b128 v[158:161], v1 offset:2048
	ds_read_b128 v[162:165], v1 offset:3072
	s_add_u32 s60, s60, 0x80000
	s_addc_u32 s61, s61, 0
	s_mov_b32 m0, s35
	ds_read_b128 v[166:169], v148 offset:32768
	ds_read_b128 v[170:173], v148 offset:33792
	ds_read_b128 v[174:177], v148 offset:34816
	ds_read_b128 v[178:181], v148 offset:35840
	ds_read_b128 v[182:185], v148 offset:36864
	ds_read_b128 v[186:189], v148 offset:37888
	ds_read_b128 v[190:193], v148 offset:38912
	ds_read_b128 v[194:197], v148 offset:39936
	global_load_lds_dwordx4 v130, s[60:61]
	s_mov_b32 m0, s40
	s_nop 0
	global_load_lds_dwordx4 v132, s[60:61]
	s_waitcnt lgkmcnt(8)
	s_barrier
	s_waitcnt lgkmcnt(0)
	s_setprio 1
	s_waitcnt lgkmcnt(0)
	v_mfma_f32_16x16x32_bf16 v[126:129], v[150:153], v[166:169], v[126:129]
	v_mfma_f32_16x16x32_bf16 v[122:125], v[158:161], v[166:169], v[122:125]
	v_mfma_f32_16x16x32_bf16 v[118:121], v[150:153], v[174:177], v[118:121]
	v_mfma_f32_16x16x32_bf16 v[114:117], v[158:161], v[174:177], v[114:117]
	v_mfma_f32_16x16x32_bf16 v[94:97], v[150:153], v[182:185], v[94:97]
	v_mfma_f32_16x16x32_bf16 v[90:93], v[158:161], v[182:185], v[90:93]
	v_mfma_f32_16x16x32_bf16 v[86:89], v[150:153], v[190:193], v[86:89]
	v_mfma_f32_16x16x32_bf16 v[82:85], v[158:161], v[190:193], v[82:85]
	v_mfma_f32_16x16x32_bf16 v[126:129], v[154:157], v[170:173], v[126:129]
	v_mfma_f32_16x16x32_bf16 v[122:125], v[162:165], v[170:173], v[122:125]
	v_mfma_f32_16x16x32_bf16 v[118:121], v[154:157], v[178:181], v[118:121]
	v_mfma_f32_16x16x32_bf16 v[114:117], v[162:165], v[178:181], v[114:117]
	v_mfma_f32_16x16x32_bf16 v[94:97], v[154:157], v[186:189], v[94:97]
	v_mfma_f32_16x16x32_bf16 v[90:93], v[162:165], v[186:189], v[90:93]
	v_mfma_f32_16x16x32_bf16 v[86:89], v[154:157], v[194:197], v[86:89]
	v_mfma_f32_16x16x32_bf16 v[82:85], v[162:165], v[194:197], v[82:85]
	s_setprio 0
	s_barrier
	s_add_i32 s60, 0, 0x1c000
	s_add_i32 s61, s76, s26
	v_add_u32_e32 v1, s60, v145
	v_lshl_add_u64 v[142:143], v[142:143], 0, s[8:9]
	s_mov_b32 m0, s61
	ds_read_b128 v[198:201], v1
	ds_read_b128 v[202:205], v1 offset:1024
	ds_read_b128 v[206:209], v1 offset:2048
	ds_read_b128 v[210:213], v1 offset:3072
	global_load_lds_dwordx4 v[142:143], off
	v_lshl_add_u64 v[142:143], v[214:215], 0, s[8:9]
	s_add_i32 m0, s61, 0x2000
	s_nop 0
	global_load_lds_dwordx4 v[142:143], off
	s_barrier
	s_waitcnt lgkmcnt(0)
	s_setprio 1
	s_waitcnt lgkmcnt(0)
	v_mfma_f32_16x16x32_bf16 v[110:113], v[198:201], v[166:169], v[110:113]
	v_mfma_f32_16x16x32_bf16 v[106:109], v[206:209], v[166:169], v[106:109]
	v_mfma_f32_16x16x32_bf16 v[102:105], v[198:201], v[174:177], v[102:105]
	v_mfma_f32_16x16x32_bf16 v[98:101], v[206:209], v[174:177], v[98:101]
	v_mfma_f32_16x16x32_bf16 v[78:81], v[198:201], v[182:185], v[78:81]
	v_mfma_f32_16x16x32_bf16 v[74:77], v[206:209], v[182:185], v[74:77]
	v_mfma_f32_16x16x32_bf16 v[70:73], v[198:201], v[190:193], v[70:73]
	v_mfma_f32_16x16x32_bf16 v[66:69], v[206:209], v[190:193], v[66:69]
	v_mfma_f32_16x16x32_bf16 v[110:113], v[202:205], v[170:173], v[110:113]
	v_mfma_f32_16x16x32_bf16 v[106:109], v[210:213], v[170:173], v[106:109]
	v_mfma_f32_16x16x32_bf16 v[102:105], v[202:205], v[178:181], v[102:105]
	v_mfma_f32_16x16x32_bf16 v[98:101], v[210:213], v[178:181], v[98:101]
	v_mfma_f32_16x16x32_bf16 v[78:81], v[202:205], v[186:189], v[78:81]
	v_mfma_f32_16x16x32_bf16 v[74:77], v[210:213], v[186:189], v[74:77]
	v_mfma_f32_16x16x32_bf16 v[70:73], v[202:205], v[194:197], v[70:73]
	v_mfma_f32_16x16x32_bf16 v[66:69], v[210:213], v[194:197], v[66:69]
	s_setprio 0
	s_mov_b32 m0, s55
	v_lshl_add_u64 v[142:143], v[216:217], 0, s[8:9]
	s_barrier
	ds_read_b128 v[166:169], v148 offset:49152
	ds_read_b128 v[170:173], v148 offset:50176
	ds_read_b128 v[174:177], v148 offset:51200
	ds_read_b128 v[178:181], v148 offset:52224
	ds_read_b128 v[182:185], v148 offset:53248
	ds_read_b128 v[186:189], v148 offset:54272
	ds_read_b128 v[190:193], v148 offset:55296
	ds_read_b128 v[194:197], v148 offset:56320
	global_load_lds_dwordx4 v[142:143], off
	v_lshl_add_u64 v[142:143], v[220:221], 0, s[8:9]
	s_mov_b32 m0, s62
	s_nop 0
	global_load_lds_dwordx4 v[142:143], off
	s_barrier
	s_waitcnt lgkmcnt(0)
	s_setprio 1
	s_waitcnt lgkmcnt(0)
	v_mfma_f32_16x16x32_bf16 v[62:65], v[150:153], v[166:169], v[62:65]
	v_mfma_f32_16x16x32_bf16 v[58:61], v[158:161], v[166:169], v[58:61]
	v_mfma_f32_16x16x32_bf16 v[54:57], v[150:153], v[174:177], v[54:57]
	v_mfma_f32_16x16x32_bf16 v[50:53], v[158:161], v[174:177], v[50:53]
	v_mfma_f32_16x16x32_bf16 v[30:33], v[150:153], v[182:185], v[30:33]
	v_mfma_f32_16x16x32_bf16 v[26:29], v[158:161], v[182:185], v[26:29]
	v_mfma_f32_16x16x32_bf16 v[22:25], v[150:153], v[190:193], v[22:25]
	v_mfma_f32_16x16x32_bf16 v[14:17], v[158:161], v[190:193], v[14:17]
	v_mfma_f32_16x16x32_bf16 v[62:65], v[154:157], v[170:173], v[62:65]
	v_mfma_f32_16x16x32_bf16 v[58:61], v[162:165], v[170:173], v[58:61]
	v_mfma_f32_16x16x32_bf16 v[54:57], v[154:157], v[178:181], v[54:57]
	v_mfma_f32_16x16x32_bf16 v[50:53], v[162:165], v[178:181], v[50:53]
	v_mfma_f32_16x16x32_bf16 v[30:33], v[154:157], v[186:189], v[30:33]
	v_mfma_f32_16x16x32_bf16 v[26:29], v[162:165], v[186:189], v[26:29]
	v_mfma_f32_16x16x32_bf16 v[22:25], v[154:157], v[194:197], v[22:25]
	v_mfma_f32_16x16x32_bf16 v[14:17], v[162:165], v[194:197], v[14:17]
	s_setprio 0
	s_barrier
	s_add_u32 s58, s58, 0x80080
	s_addc_u32 s59, s59, 0
	s_add_i32 s60, s60, s26
	s_mov_b32 m0, s60
	s_nop 0
	global_load_lds_dwordx4 v130, s[58:59]
	s_add_i32 m0, s60, 0x2000
	s_nop 0
	global_load_lds_dwordx4 v132, s[58:59]
	s_waitcnt vmcnt(6)
	s_barrier
	s_setprio 1
	v_mfma_f32_16x16x32_bf16 v[46:49], v[198:201], v[166:169], v[46:49]
	v_mfma_f32_16x16x32_bf16 v[42:45], v[206:209], v[166:169], v[42:45]
	v_mfma_f32_16x16x32_bf16 v[38:41], v[198:201], v[174:177], v[38:41]
	v_mfma_f32_16x16x32_bf16 v[34:37], v[206:209], v[174:177], v[34:37]
	v_mfma_f32_16x16x32_bf16 v[18:21], v[198:201], v[182:185], v[18:21]
	v_mfma_f32_16x16x32_bf16 v[10:13], v[206:209], v[182:185], v[10:13]
	v_mfma_f32_16x16x32_bf16 v[6:9], v[198:201], v[190:193], v[6:9]
	v_mfma_f32_16x16x32_bf16 v[2:5], v[206:209], v[190:193], v[2:5]
	v_mfma_f32_16x16x32_bf16 v[46:49], v[202:205], v[170:173], v[46:49]
	v_mfma_f32_16x16x32_bf16 v[42:45], v[210:213], v[170:173], v[42:45]
	v_mfma_f32_16x16x32_bf16 v[38:41], v[202:205], v[178:181], v[38:41]
	v_mfma_f32_16x16x32_bf16 v[34:37], v[210:213], v[178:181], v[34:37]
	v_mfma_f32_16x16x32_bf16 v[18:21], v[202:205], v[186:189], v[18:21]
	v_mfma_f32_16x16x32_bf16 v[10:13], v[210:213], v[186:189], v[10:13]
	v_mfma_f32_16x16x32_bf16 v[6:9], v[202:205], v[194:197], v[6:9]
	v_mfma_f32_16x16x32_bf16 v[2:5], v[210:213], v[194:197], v[2:5]
	s_setprio 0
	s_add_i32 s75, s75, 2
	s_add_u32 s56, s56, 0x100
	s_addc_u32 s57, s57, 0
	s_add_u32 s73, s73, 0x100
	s_addc_u32 s74, s74, 0
	s_cmp_gt_u32 s75, 29
	s_barrier
	s_cbranch_scc1 .Lpeel_1239_after
.LBB0_1239:
	ds_read_b128 v[150:153], v147
	ds_read_b128 v[154:157], v147 offset:1024
	ds_read_b128 v[158:161], v147 offset:2048
	ds_read_b128 v[162:165], v147 offset:3072
	s_add_u32 s58, s56, 0xfff80080
	s_addc_u32 s59, s57, -1
	s_cmp_eq_u32 s75, 28
	s_cselect_b32 s61, s21, s59
	s_cselect_b32 s60, s71, s58
	s_cselect_b32 s59, s19, s74
	s_cselect_b32 s58, s72, s73
	s_add_i32 m0, s33, 0xc000
	ds_read_b128 v[166:169], v148
	ds_read_b128 v[170:173], v148 offset:1024
	ds_read_b128 v[174:177], v148 offset:2048
	ds_read_b128 v[178:181], v148 offset:3072
	ds_read_b128 v[182:185], v148 offset:4096
	ds_read_b128 v[186:189], v148 offset:5120
	ds_read_b128 v[190:193], v148 offset:6144
	ds_read_b128 v[194:197], v148 offset:7168
	global_load_lds_dwordx4 v134, s[56:57]
	s_add_i32 m0, s33, 0xe000
	s_nop 0
	global_load_lds_dwordx4 v136, s[56:57]
	s_waitcnt lgkmcnt(8)
	s_barrier
	s_waitcnt lgkmcnt(0)
	s_setprio 1
	s_waitcnt lgkmcnt(0)
	v_mfma_f32_16x16x32_bf16 v[126:129], v[150:153], v[166:169], v[126:129]
	v_mfma_f32_16x16x32_bf16 v[122:125], v[158:161], v[166:169], v[122:125]
	v_mfma_f32_16x16x32_bf16 v[118:121], v[150:153], v[174:177], v[118:121]
	v_mfma_f32_16x16x32_bf16 v[114:117], v[158:161], v[174:177], v[114:117]
	v_mfma_f32_16x16x32_bf16 v[94:97], v[150:153], v[182:185], v[94:97]
	v_mfma_f32_16x16x32_bf16 v[90:93], v[158:161], v[182:185], v[90:93]
	v_mfma_f32_16x16x32_bf16 v[86:89], v[150:153], v[190:193], v[86:89]
	v_mfma_f32_16x16x32_bf16 v[82:85], v[158:161], v[190:193], v[82:85]
	v_mfma_f32_16x16x32_bf16 v[126:129], v[154:157], v[170:173], v[126:129]
	v_mfma_f32_16x16x32_bf16 v[122:125], v[162:165], v[170:173], v[122:125]
	v_mfma_f32_16x16x32_bf16 v[118:121], v[154:157], v[178:181], v[118:121]
	v_mfma_f32_16x16x32_bf16 v[114:117], v[162:165], v[178:181], v[114:117]
	v_mfma_f32_16x16x32_bf16 v[94:97], v[154:157], v[186:189], v[94:97]
	v_mfma_f32_16x16x32_bf16 v[90:93], v[162:165], v[186:189], v[90:93]
	v_mfma_f32_16x16x32_bf16 v[86:89], v[154:157], v[194:197], v[86:89]
	v_mfma_f32_16x16x32_bf16 v[82:85], v[162:165], v[194:197], v[82:85]
	s_setprio 0
	s_barrier
	s_add_i32 s76, s64, s26
	v_lshl_add_u64 v[142:143], s[58:59], 0, v[130:131]
	s_mov_b32 m0, s76
	ds_read_b128 v[198:201], v149
	ds_read_b128 v[202:205], v149 offset:1024
	ds_read_b128 v[206:209], v149 offset:2048
	ds_read_b128 v[210:213], v149 offset:3072
	global_load_lds_dwordx4 v[142:143], off
	v_lshl_add_u64 v[214:215], s[58:59], 0, v[132:133]
	s_add_i32 m0, s76, 0x2000
	s_nop 0
	global_load_lds_dwordx4 v[214:215], off
	s_barrier
	s_waitcnt lgkmcnt(0)
	s_setprio 1
	s_waitcnt lgkmcnt(0)
	v_mfma_f32_16x16x32_bf16 v[110:113], v[198:201], v[166:169], v[110:113]
	v_mfma_f32_16x16x32_bf16 v[106:109], v[206:209], v[166:169], v[106:109]
	v_mfma_f32_16x16x32_bf16 v[102:105], v[198:201], v[174:177], v[102:105]
	v_mfma_f32_16x16x32_bf16 v[98:101], v[206:209], v[174:177], v[98:101]
	v_mfma_f32_16x16x32_bf16 v[78:81], v[198:201], v[182:185], v[78:81]
	v_mfma_f32_16x16x32_bf16 v[74:77], v[206:209], v[182:185], v[74:77]
	v_mfma_f32_16x16x32_bf16 v[70:73], v[198:201], v[190:193], v[70:73]
	v_mfma_f32_16x16x32_bf16 v[66:69], v[206:209], v[190:193], v[66:69]
	v_mfma_f32_16x16x32_bf16 v[110:113], v[202:205], v[170:173], v[110:113]
	v_mfma_f32_16x16x32_bf16 v[106:109], v[210:213], v[170:173], v[106:109]
	v_mfma_f32_16x16x32_bf16 v[102:105], v[202:205], v[178:181], v[102:105]
	v_mfma_f32_16x16x32_bf16 v[98:101], v[210:213], v[178:181], v[98:101]
	v_mfma_f32_16x16x32_bf16 v[78:81], v[202:205], v[186:189], v[78:81]
	v_mfma_f32_16x16x32_bf16 v[74:77], v[210:213], v[186:189], v[74:77]
	v_mfma_f32_16x16x32_bf16 v[70:73], v[202:205], v[194:197], v[70:73]
	v_mfma_f32_16x16x32_bf16 v[66:69], v[210:213], v[194:197], v[66:69]
	s_setprio 0
	s_mov_b32 m0, s33
	v_lshl_add_u64 v[216:217], s[60:61], 0, v[130:131]
	s_barrier
	ds_read_b128 v[166:169], v148 offset:16384
	ds_read_b128 v[170:173], v148 offset:17408
	ds_read_b128 v[174:177], v148 offset:18432
	ds_read_b128 v[178:181], v148 offset:19456
	ds_read_b128 v[182:185], v148 offset:20480
	ds_read_b128 v[186:189], v148 offset:21504
	ds_read_b128 v[190:193], v148 offset:22528
	ds_read_b128 v[194:197], v148 offset:23552
	global_load_lds_dwordx4 v[216:217], off
	v_lshl_add_u64 v[220:221], s[60:61], 0, v[132:133]
	s_mov_b32 m0, s34
	s_nop 0
	global_load_lds_dwordx4 v[220:221], off
	s_barrier
	s_waitcnt lgkmcnt(0)
	s_setprio 1
	s_waitcnt lgkmcnt(0)
	v_mfma_f32_16x16x32_bf16 v[62:65], v[150:153], v[166:169], v[62:65]
	v_mfma_f32_16x16x32_bf16 v[58:61], v[158:161], v[166:169], v[58:61]
	v_mfma_f32_16x16x32_bf16 v[54:57], v[150:153], v[174:177], v[54:57]
	v_mfma_f32_16x16x32_bf16 v[50:53], v[158:161], v[174:177], v[50:53]
	v_mfma_f32_16x16x32_bf16 v[30:33], v[150:153], v[182:185], v[30:33]
	v_mfma_f32_16x16x32_bf16 v[26:29], v[158:161], v[182:185], v[26:29]
	v_mfma_f32_16x16x32_bf16 v[22:25], v[150:153], v[190:193], v[22:25]
	v_mfma_f32_16x16x32_bf16 v[14:17], v[158:161], v[190:193], v[14:17]
	v_mfma_f32_16x16x32_bf16 v[62:65], v[154:157], v[170:173], v[62:65]
	v_mfma_f32_16x16x32_bf16 v[58:61], v[162:165], v[170:173], v[58:61]
	v_mfma_f32_16x16x32_bf16 v[54:57], v[154:157], v[178:181], v[54:57]
	v_mfma_f32_16x16x32_bf16 v[50:53], v[162:165], v[178:181], v[50:53]
	v_mfma_f32_16x16x32_bf16 v[30:33], v[154:157], v[186:189], v[30:33]
	v_mfma_f32_16x16x32_bf16 v[26:29], v[162:165], v[186:189], v[26:29]
	v_mfma_f32_16x16x32_bf16 v[22:25], v[154:157], v[194:197], v[22:25]
	v_mfma_f32_16x16x32_bf16 v[14:17], v[162:165], v[194:197], v[14:17]
	s_setprio 0
	s_barrier
	s_add_u32 s76, s58, 0x80000
	s_addc_u32 s77, s59, 0
	s_add_i32 s78, s65, s26
	s_mov_b32 m0, s78
	s_nop 0
	global_load_lds_dwordx4 v130, s[76:77]
	s_add_i32 m0, s78, 0x2000
	s_nop 0
	global_load_lds_dwordx4 v132, s[76:77]
	s_waitcnt vmcnt(6)
	s_barrier
	s_setprio 1
	v_mfma_f32_16x16x32_bf16 v[46:49], v[198:201], v[166:169], v[46:49]
	v_mfma_f32_16x16x32_bf16 v[42:45], v[206:209], v[166:169], v[42:45]
	v_mfma_f32_16x16x32_bf16 v[38:41], v[198:201], v[174:177], v[38:41]
	v_mfma_f32_16x16x32_bf16 v[34:37], v[206:209], v[174:177], v[34:37]
	v_mfma_f32_16x16x32_bf16 v[18:21], v[198:201], v[182:185], v[18:21]
	v_mfma_f32_16x16x32_bf16 v[10:13], v[206:209], v[182:185], v[10:13]
	v_mfma_f32_16x16x32_bf16 v[6:9], v[198:201], v[190:193], v[6:9]
	v_mfma_f32_16x16x32_bf16 v[2:5], v[206:209], v[190:193], v[2:5]
	v_mfma_f32_16x16x32_bf16 v[46:49], v[202:205], v[170:173], v[46:49]
	v_mfma_f32_16x16x32_bf16 v[42:45], v[210:213], v[170:173], v[42:45]
	v_mfma_f32_16x16x32_bf16 v[38:41], v[202:205], v[178:181], v[38:41]
	v_mfma_f32_16x16x32_bf16 v[34:37], v[210:213], v[178:181], v[34:37]
	v_mfma_f32_16x16x32_bf16 v[18:21], v[202:205], v[186:189], v[18:21]
	v_mfma_f32_16x16x32_bf16 v[10:13], v[210:213], v[186:189], v[10:13]
	v_mfma_f32_16x16x32_bf16 v[6:9], v[202:205], v[194:197], v[6:9]
	v_mfma_f32_16x16x32_bf16 v[2:5], v[210:213], v[194:197], v[2:5]
	s_setprio 0
	s_add_i32 s76, 0, 0x18000
	v_add_u32_e32 v1, s76, v145
	s_barrier
	ds_read_b128 v[150:153], v1
	ds_read_b128 v[154:157], v1 offset:1024
	ds_read_b128 v[158:161], v1 offset:2048
	ds_read_b128 v[162:165], v1 offset:3072
	s_add_u32 s60, s60, 0x80000
	s_addc_u32 s61, s61, 0
	s_mov_b32 m0, s35
	ds_read_b128 v[166:169], v148 offset:32768
	ds_read_b128 v[170:173], v148 offset:33792
	ds_read_b128 v[174:177], v148 offset:34816
	ds_read_b128 v[178:181], v148 offset:35840
	ds_read_b128 v[182:185], v148 offset:36864
	ds_read_b128 v[186:189], v148 offset:37888
	ds_read_b128 v[190:193], v148 offset:38912
	ds_read_b128 v[194:197], v148 offset:39936
	global_load_lds_dwordx4 v130, s[60:61]
	s_mov_b32 m0, s40
	s_nop 0
	global_load_lds_dwordx4 v132, s[60:61]
	s_waitcnt lgkmcnt(8)
	s_barrier
	s_waitcnt lgkmcnt(0)
	s_setprio 1
	s_waitcnt lgkmcnt(0)
	v_mfma_f32_16x16x32_bf16 v[126:129], v[150:153], v[166:169], v[126:129]
	v_mfma_f32_16x16x32_bf16 v[122:125], v[158:161], v[166:169], v[122:125]
	v_mfma_f32_16x16x32_bf16 v[118:121], v[150:153], v[174:177], v[118:121]
	v_mfma_f32_16x16x32_bf16 v[114:117], v[158:161], v[174:177], v[114:117]
	v_mfma_f32_16x16x32_bf16 v[94:97], v[150:153], v[182:185], v[94:97]
	v_mfma_f32_16x16x32_bf16 v[90:93], v[158:161], v[182:185], v[90:93]
	v_mfma_f32_16x16x32_bf16 v[86:89], v[150:153], v[190:193], v[86:89]
	v_mfma_f32_16x16x32_bf16 v[82:85], v[158:161], v[190:193], v[82:85]
	v_mfma_f32_16x16x32_bf16 v[126:129], v[154:157], v[170:173], v[126:129]
	v_mfma_f32_16x16x32_bf16 v[122:125], v[162:165], v[170:173], v[122:125]
	v_mfma_f32_16x16x32_bf16 v[118:121], v[154:157], v[178:181], v[118:121]
	v_mfma_f32_16x16x32_bf16 v[114:117], v[162:165], v[178:181], v[114:117]
	v_mfma_f32_16x16x32_bf16 v[94:97], v[154:157], v[186:189], v[94:97]
	v_mfma_f32_16x16x32_bf16 v[90:93], v[162:165], v[186:189], v[90:93]
	v_mfma_f32_16x16x32_bf16 v[86:89], v[154:157], v[194:197], v[86:89]
	v_mfma_f32_16x16x32_bf16 v[82:85], v[162:165], v[194:197], v[82:85]
	s_setprio 0
	s_barrier
	s_add_i32 s60, 0, 0x1c000
	s_add_i32 s61, s76, s26
	v_add_u32_e32 v1, s60, v145
	v_lshl_add_u64 v[142:143], v[142:143], 0, s[8:9]
	s_mov_b32 m0, s61
	ds_read_b128 v[198:201], v1
	ds_read_b128 v[202:205], v1 offset:1024
	ds_read_b128 v[206:209], v1 offset:2048
	ds_read_b128 v[210:213], v1 offset:3072
	global_load_lds_dwordx4 v[142:143], off
	v_lshl_add_u64 v[142:143], v[214:215], 0, s[8:9]
	s_add_i32 m0, s61, 0x2000
	s_nop 0
	global_load_lds_dwordx4 v[142:143], off
	s_barrier
	s_waitcnt lgkmcnt(0)
	s_setprio 1
	s_waitcnt lgkmcnt(0)
	v_mfma_f32_16x16x32_bf16 v[110:113], v[198:201], v[166:169], v[110:113]
	v_mfma_f32_16x16x32_bf16 v[106:109], v[206:209], v[166:169], v[106:109]
	v_mfma_f32_16x16x32_bf16 v[102:105], v[198:201], v[174:177], v[102:105]
	v_mfma_f32_16x16x32_bf16 v[98:101], v[206:209], v[174:177], v[98:101]
	v_mfma_f32_16x16x32_bf16 v[78:81], v[198:201], v[182:185], v[78:81]
	v_mfma_f32_16x16x32_bf16 v[74:77], v[206:209], v[182:185], v[74:77]
	v_mfma_f32_16x16x32_bf16 v[70:73], v[198:201], v[190:193], v[70:73]
	v_mfma_f32_16x16x32_bf16 v[66:69], v[206:209], v[190:193], v[66:69]
	v_mfma_f32_16x16x32_bf16 v[110:113], v[202:205], v[170:173], v[110:113]
	v_mfma_f32_16x16x32_bf16 v[106:109], v[210:213], v[170:173], v[106:109]
	v_mfma_f32_16x16x32_bf16 v[102:105], v[202:205], v[178:181], v[102:105]
	v_mfma_f32_16x16x32_bf16 v[98:101], v[210:213], v[178:181], v[98:101]
	v_mfma_f32_16x16x32_bf16 v[78:81], v[202:205], v[186:189], v[78:81]
	v_mfma_f32_16x16x32_bf16 v[74:77], v[210:213], v[186:189], v[74:77]
	v_mfma_f32_16x16x32_bf16 v[70:73], v[202:205], v[194:197], v[70:73]
	v_mfma_f32_16x16x32_bf16 v[66:69], v[210:213], v[194:197], v[66:69]
	s_setprio 0
	s_mov_b32 m0, s55
	v_lshl_add_u64 v[142:143], v[216:217], 0, s[8:9]
	s_barrier
	ds_read_b128 v[166:169], v148 offset:49152
	ds_read_b128 v[170:173], v148 offset:50176
	ds_read_b128 v[174:177], v148 offset:51200
	ds_read_b128 v[178:181], v148 offset:52224
	ds_read_b128 v[182:185], v148 offset:53248
	ds_read_b128 v[186:189], v148 offset:54272
	ds_read_b128 v[190:193], v148 offset:55296
	ds_read_b128 v[194:197], v148 offset:56320
	global_load_lds_dwordx4 v[142:143], off
	v_lshl_add_u64 v[142:143], v[220:221], 0, s[8:9]
	s_mov_b32 m0, s62
	s_nop 0
	global_load_lds_dwordx4 v[142:143], off
	s_barrier
	s_waitcnt lgkmcnt(0)
	s_setprio 1
	s_waitcnt lgkmcnt(0)
	v_mfma_f32_16x16x32_bf16 v[62:65], v[150:153], v[166:169], v[62:65]
	v_mfma_f32_16x16x32_bf16 v[58:61], v[158:161], v[166:169], v[58:61]
	v_mfma_f32_16x16x32_bf16 v[54:57], v[150:153], v[174:177], v[54:57]
	v_mfma_f32_16x16x32_bf16 v[50:53], v[158:161], v[174:177], v[50:53]
	v_mfma_f32_16x16x32_bf16 v[30:33], v[150:153], v[182:185], v[30:33]
	v_mfma_f32_16x16x32_bf16 v[26:29], v[158:161], v[182:185], v[26:29]
	v_mfma_f32_16x16x32_bf16 v[22:25], v[150:153], v[190:193], v[22:25]
	v_mfma_f32_16x16x32_bf16 v[14:17], v[158:161], v[190:193], v[14:17]
	v_mfma_f32_16x16x32_bf16 v[62:65], v[154:157], v[170:173], v[62:65]
	v_mfma_f32_16x16x32_bf16 v[58:61], v[162:165], v[170:173], v[58:61]
	v_mfma_f32_16x16x32_bf16 v[54:57], v[154:157], v[178:181], v[54:57]
	v_mfma_f32_16x16x32_bf16 v[50:53], v[162:165], v[178:181], v[50:53]
	v_mfma_f32_16x16x32_bf16 v[30:33], v[154:157], v[186:189], v[30:33]
	v_mfma_f32_16x16x32_bf16 v[26:29], v[162:165], v[186:189], v[26:29]
	v_mfma_f32_16x16x32_bf16 v[22:25], v[154:157], v[194:197], v[22:25]
	v_mfma_f32_16x16x32_bf16 v[14:17], v[162:165], v[194:197], v[14:17]
	s_setprio 0
	s_barrier
	s_add_u32 s58, s58, 0x80080
	s_addc_u32 s59, s59, 0
	s_add_i32 s60, s60, s26
	s_mov_b32 m0, s60
	s_nop 0
	global_load_lds_dwordx4 v130, s[58:59]
	s_add_i32 m0, s60, 0x2000
	s_nop 0
	global_load_lds_dwordx4 v132, s[58:59]
	s_waitcnt vmcnt(6)
	s_barrier
	s_setprio 1
	v_mfma_f32_16x16x32_bf16 v[46:49], v[198:201], v[166:169], v[46:49]
	v_mfma_f32_16x16x32_bf16 v[42:45], v[206:209], v[166:169], v[42:45]
	v_mfma_f32_16x16x32_bf16 v[38:41], v[198:201], v[174:177], v[38:41]
	v_mfma_f32_16x16x32_bf16 v[34:37], v[206:209], v[174:177], v[34:37]
	v_mfma_f32_16x16x32_bf16 v[18:21], v[198:201], v[182:185], v[18:21]
	v_mfma_f32_16x16x32_bf16 v[10:13], v[206:209], v[182:185], v[10:13]
	v_mfma_f32_16x16x32_bf16 v[6:9], v[198:201], v[190:193], v[6:9]
	v_mfma_f32_16x16x32_bf16 v[2:5], v[206:209], v[190:193], v[2:5]
	v_mfma_f32_16x16x32_bf16 v[46:49], v[202:205], v[170:173], v[46:49]
	v_mfma_f32_16x16x32_bf16 v[42:45], v[210:213], v[170:173], v[42:45]
	v_mfma_f32_16x16x32_bf16 v[38:41], v[202:205], v[178:181], v[38:41]
	v_mfma_f32_16x16x32_bf16 v[34:37], v[210:213], v[178:181], v[34:37]
	v_mfma_f32_16x16x32_bf16 v[18:21], v[202:205], v[186:189], v[18:21]
	v_mfma_f32_16x16x32_bf16 v[10:13], v[210:213], v[186:189], v[10:13]
	v_mfma_f32_16x16x32_bf16 v[6:9], v[202:205], v[194:197], v[6:9]
	v_mfma_f32_16x16x32_bf16 v[2:5], v[210:213], v[194:197], v[2:5]
	s_setprio 0
	s_add_i32 s75, s75, 2
	s_add_u32 s56, s56, 0x100
	s_addc_u32 s57, s57, 0
	s_add_u32 s73, s73, 0x100
	s_addc_u32 s74, s74, 0
	s_cmp_gt_u32 s75, 29
	s_barrier
	s_cbranch_scc0 .LBB0_1239

.LBB0_1521:
	s_ashr_i32 s9, s8, 31
	s_lshl_b64 s[10:11], s[8:9], 20
	s_add_u32 s10, s25, s10
	s_addc_u32 s11, s26, s11
	s_and_b64 s[14:15], s[14:15], exec
	s_cselect_b32 s9, s11, s13
	s_cselect_b32 s58, s10, s12
	v_mov_b32_e32 v139, v135
	v_mov_b32_e32 v141, v135
	s_add_u32 s59, s12, 0x100
	v_mov_b32_e32 v2, 0
	v_lshl_add_u64 v[142:143], s[6:7], 0, v[140:141]
	v_lshl_add_u64 v[144:145], s[6:7], 0, v[138:139]
	s_addc_u32 s60, s13, 0
	s_mov_b32 s61, -2
	s_mov_b64 s[12:13], 0
	s_add_u32 s14, s28, s12
	s_addc_u32 s15, s29, s13
	s_add_u32 s16, s14, 0x2a300100
	ds_read_b128 v[158:161], v151
	ds_read_b128 v[162:165], v151 offset:1024
	ds_read_b128 v[166:169], v151 offset:2048
	ds_read_b128 v[170:173], v151 offset:3072
	s_addc_u32 s17, s15, 0
	s_add_u32 s62, s59, s12
	s_addc_u32 s63, s60, s13
	s_cmpk_eq_i32 s12, 0xf00
	s_cselect_b64 vcc, -1, 0
	s_and_b64 s[14:15], vcc, exec
	v_cndmask_b32_e32 v134, v137, v154, vcc
	v_cndmask_b32_e32 v222, v136, v155, vcc
	v_cndmask_b32_e32 v139, v138, v156, vcc
	v_cndmask_b32_e32 v141, v140, v157, vcc
	s_cselect_b32 s17, s37, s17
	s_cselect_b32 s16, s36, s16
	s_cselect_b32 s15, s9, s63
	s_cselect_b32 s14, s58, s62
	v_lshl_add_u64 v[206:207], v[144:145], 0, s[12:13]
	s_add_i32 m0, s34, 0xc000
	ds_read_b128 v[174:177], v152
	ds_read_b128 v[178:181], v152 offset:1024
	ds_read_b128 v[182:185], v152 offset:2048
	ds_read_b128 v[186:189], v152 offset:3072
	ds_read_b128 v[190:193], v152 offset:4096
	ds_read_b128 v[194:197], v152 offset:5120
	ds_read_b128 v[198:201], v152 offset:6144
	ds_read_b128 v[202:205], v152 offset:7168
	global_load_lds_dwordx4 v[206:207], off
	v_lshl_add_u64 v[206:207], v[142:143], 0, s[12:13]
	s_add_i32 m0, s34, 0xe000
	s_nop 0
	global_load_lds_dwordx4 v[206:207], off
	s_waitcnt lgkmcnt(8)
	s_barrier
	s_waitcnt lgkmcnt(0)
	s_setprio 1
	s_waitcnt lgkmcnt(0)
	v_mfma_f32_16x16x32_bf16 v[126:129], v[158:161], v[174:177], 0
	v_mfma_f32_16x16x32_bf16 v[122:125], v[166:169], v[174:177], 0
	v_mfma_f32_16x16x32_bf16 v[110:113], v[158:161], v[182:185], 0
	v_mfma_f32_16x16x32_bf16 v[106:109], v[166:169], v[182:185], 0
	v_mfma_f32_16x16x32_bf16 v[94:97], v[158:161], v[190:193], 0
	v_mfma_f32_16x16x32_bf16 v[90:93], v[166:169], v[190:193], 0
	v_mfma_f32_16x16x32_bf16 v[78:81], v[158:161], v[198:201], 0
	v_mfma_f32_16x16x32_bf16 v[74:77], v[166:169], v[198:201], 0
	v_mfma_f32_16x16x32_bf16 v[126:129], v[162:165], v[178:181], v[126:129]
	v_mfma_f32_16x16x32_bf16 v[122:125], v[170:173], v[178:181], v[122:125]
	v_mfma_f32_16x16x32_bf16 v[110:113], v[162:165], v[186:189], v[110:113]
	v_mfma_f32_16x16x32_bf16 v[106:109], v[170:173], v[186:189], v[106:109]
	v_mfma_f32_16x16x32_bf16 v[94:97], v[162:165], v[194:197], v[94:97]
	v_mfma_f32_16x16x32_bf16 v[90:93], v[170:173], v[194:197], v[90:93]
	v_mfma_f32_16x16x32_bf16 v[78:81], v[162:165], v[202:205], v[78:81]
	v_mfma_f32_16x16x32_bf16 v[74:77], v[170:173], v[202:205], v[74:77]
	s_setprio 0
	s_barrier
	s_add_i32 s62, s42, s33
	v_lshl_add_u64 v[224:225], s[14:15], 0, v[132:133]
	s_mov_b32 m0, s62
	ds_read_b128 v[206:209], v153
	ds_read_b128 v[210:213], v153 offset:1024
	ds_read_b128 v[214:217], v153 offset:2048
	ds_read_b128 v[218:221], v153 offset:3072
	global_load_lds_dwordx4 v[224:225], off
	v_lshl_add_u64 v[226:227], s[14:15], 0, v[130:131]
	s_add_i32 m0, s62, 0x2000
	s_nop 0
	global_load_lds_dwordx4 v[226:227], off
	s_barrier
	s_waitcnt lgkmcnt(0)
	s_setprio 1
	s_waitcnt lgkmcnt(0)
	v_mfma_f32_16x16x32_bf16 v[118:121], v[206:209], v[174:177], 0
	v_mfma_f32_16x16x32_bf16 v[114:117], v[214:217], v[174:177], 0
	v_mfma_f32_16x16x32_bf16 v[102:105], v[206:209], v[182:185], 0
	v_mfma_f32_16x16x32_bf16 v[98:101], v[214:217], v[182:185], 0
	v_mfma_f32_16x16x32_bf16 v[86:89], v[206:209], v[190:193], 0
	v_mfma_f32_16x16x32_bf16 v[82:85], v[214:217], v[190:193], 0
	v_mfma_f32_16x16x32_bf16 v[70:73], v[206:209], v[198:201], 0
	v_mfma_f32_16x16x32_bf16 v[66:69], v[214:217], v[198:201], 0
	v_mfma_f32_16x16x32_bf16 v[118:121], v[210:213], v[178:181], v[118:121]
	v_mfma_f32_16x16x32_bf16 v[114:117], v[218:221], v[178:181], v[114:117]
	v_mfma_f32_16x16x32_bf16 v[102:105], v[210:213], v[186:189], v[102:105]
	v_mfma_f32_16x16x32_bf16 v[98:101], v[218:221], v[186:189], v[98:101]
	v_mfma_f32_16x16x32_bf16 v[86:89], v[210:213], v[194:197], v[86:89]
	v_mfma_f32_16x16x32_bf16 v[82:85], v[218:221], v[194:197], v[82:85]
	v_mfma_f32_16x16x32_bf16 v[70:73], v[210:213], v[202:205], v[70:73]
	v_mfma_f32_16x16x32_bf16 v[66:69], v[218:221], v[202:205], v[66:69]
	s_setprio 0
	s_mov_b32 m0, s34
	s_barrier
	ds_read_b128 v[174:177], v152 offset:16384
	ds_read_b128 v[178:181], v152 offset:17408
	ds_read_b128 v[182:185], v152 offset:18432
	ds_read_b128 v[186:189], v152 offset:19456
	ds_read_b128 v[190:193], v152 offset:20480
	ds_read_b128 v[194:197], v152 offset:21504
	ds_read_b128 v[198:201], v152 offset:22528
	ds_read_b128 v[202:205], v152 offset:23552
	global_load_lds_dwordx4 v134, s[16:17]
	s_mov_b32 m0, s35
	v_mov_b32_e32 v223, v135
	global_load_lds_dwordx4 v222, s[16:17]
	s_barrier
	s_waitcnt lgkmcnt(0)
	v_lshl_add_u64 v[228:229], s[16:17], 0, v[134:135]
	v_lshl_add_u64 v[222:223], s[16:17], 0, v[222:223]
	s_setprio 1
	s_waitcnt lgkmcnt(0)
	v_mfma_f32_16x16x32_bf16 v[62:65], v[158:161], v[174:177], 0
	v_mfma_f32_16x16x32_bf16 v[58:61], v[166:169], v[174:177], 0
	v_mfma_f32_16x16x32_bf16 v[46:49], v[158:161], v[182:185], 0
	v_mfma_f32_16x16x32_bf16 v[42:45], v[166:169], v[182:185], 0
	v_mfma_f32_16x16x32_bf16 v[30:33], v[158:161], v[190:193], 0
	v_mfma_f32_16x16x32_bf16 v[26:29], v[166:169], v[190:193], 0
	v_mfma_f32_16x16x32_bf16 v[14:17], v[158:161], v[198:201], 0
	v_mfma_f32_16x16x32_bf16 v[10:13], v[166:169], v[198:201], 0
	v_mfma_f32_16x16x32_bf16 v[62:65], v[162:165], v[178:181], v[62:65]
	v_mfma_f32_16x16x32_bf16 v[58:61], v[170:173], v[178:181], v[58:61]
	v_mfma_f32_16x16x32_bf16 v[46:49], v[162:165], v[186:189], v[46:49]
	v_mfma_f32_16x16x32_bf16 v[42:45], v[170:173], v[186:189], v[42:45]
	v_mfma_f32_16x16x32_bf16 v[30:33], v[162:165], v[194:197], v[30:33]
	v_mfma_f32_16x16x32_bf16 v[26:29], v[170:173], v[194:197], v[26:29]
	v_mfma_f32_16x16x32_bf16 v[14:17], v[162:165], v[202:205], v[14:17]
	v_mfma_f32_16x16x32_bf16 v[10:13], v[170:173], v[202:205], v[10:13]
	s_setprio 0
	s_barrier
	s_add_u32 s62, s14, 0x80000
	s_addc_u32 s63, s15, 0
	s_add_i32 s64, s43, s33
	s_mov_b32 m0, s64
	s_nop 0
	global_load_lds_dwordx4 v132, s[62:63]
	s_add_i32 m0, s64, 0x2000
	s_nop 0
	global_load_lds_dwordx4 v130, s[62:63]
	s_waitcnt vmcnt(6)
	s_barrier
	s_setprio 1
	v_mfma_f32_16x16x32_bf16 v[54:57], v[206:209], v[174:177], 0
	v_mfma_f32_16x16x32_bf16 v[50:53], v[214:217], v[174:177], 0
	v_mfma_f32_16x16x32_bf16 v[38:41], v[206:209], v[182:185], 0
	v_mfma_f32_16x16x32_bf16 v[34:37], v[214:217], v[182:185], 0
	v_mfma_f32_16x16x32_bf16 v[22:25], v[206:209], v[190:193], 0
	v_mfma_f32_16x16x32_bf16 v[18:21], v[214:217], v[190:193], 0
	v_mfma_f32_16x16x32_bf16 v[6:9], v[206:209], v[198:201], 0
	v_mfma_f32_16x16x32_bf16 v[2:5], v[214:217], v[198:201], 0
	v_mfma_f32_16x16x32_bf16 v[54:57], v[210:213], v[178:181], v[54:57]
	v_mfma_f32_16x16x32_bf16 v[50:53], v[218:221], v[178:181], v[50:53]
	v_mfma_f32_16x16x32_bf16 v[38:41], v[210:213], v[186:189], v[38:41]
	v_mfma_f32_16x16x32_bf16 v[34:37], v[218:221], v[186:189], v[34:37]
	v_mfma_f32_16x16x32_bf16 v[22:25], v[210:213], v[194:197], v[22:25]
	v_mfma_f32_16x16x32_bf16 v[18:21], v[218:221], v[194:197], v[18:21]
	v_mfma_f32_16x16x32_bf16 v[6:9], v[210:213], v[202:205], v[6:9]
	v_mfma_f32_16x16x32_bf16 v[2:5], v[218:221], v[202:205], v[2:5]
	s_setprio 0
	s_add_i32 s62, 0, 0x18000
	v_add_u32_e32 v134, s62, v149
	s_barrier
	ds_read_b128 v[158:161], v134
	ds_read_b128 v[162:165], v134 offset:1024
	ds_read_b128 v[166:169], v134 offset:2048
	ds_read_b128 v[170:173], v134 offset:3072
	s_mov_b32 m0, s38
	ds_read_b128 v[174:177], v152 offset:32768
	ds_read_b128 v[178:181], v152 offset:33792
	ds_read_b128 v[182:185], v152 offset:34816
	ds_read_b128 v[186:189], v152 offset:35840
	ds_read_b128 v[190:193], v152 offset:36864
	ds_read_b128 v[194:197], v152 offset:37888
	ds_read_b128 v[198:201], v152 offset:38912
	ds_read_b128 v[202:205], v152 offset:39936
	global_load_lds_dwordx4 v139, s[16:17]
	s_mov_b32 m0, s39
	s_nop 0
	global_load_lds_dwordx4 v141, s[16:17]
	s_waitcnt lgkmcnt(8)
	s_barrier
	s_waitcnt lgkmcnt(0)
	s_setprio 1
	s_waitcnt lgkmcnt(0)
	v_mfma_f32_16x16x32_bf16 v[126:129], v[158:161], v[174:177], v[126:129]
	v_mfma_f32_16x16x32_bf16 v[122:125], v[166:169], v[174:177], v[122:125]
	v_mfma_f32_16x16x32_bf16 v[110:113], v[158:161], v[182:185], v[110:113]
	v_mfma_f32_16x16x32_bf16 v[106:109], v[166:169], v[182:185], v[106:109]
	v_mfma_f32_16x16x32_bf16 v[94:97], v[158:161], v[190:193], v[94:97]
	v_mfma_f32_16x16x32_bf16 v[90:93], v[166:169], v[190:193], v[90:93]
	v_mfma_f32_16x16x32_bf16 v[78:81], v[158:161], v[198:201], v[78:81]
	v_mfma_f32_16x16x32_bf16 v[74:77], v[166:169], v[198:201], v[74:77]
	v_mfma_f32_16x16x32_bf16 v[126:129], v[162:165], v[178:181], v[126:129]
	v_mfma_f32_16x16x32_bf16 v[122:125], v[170:173], v[178:181], v[122:125]
	v_mfma_f32_16x16x32_bf16 v[110:113], v[162:165], v[186:189], v[110:113]
	v_mfma_f32_16x16x32_bf16 v[106:109], v[170:173], v[186:189], v[106:109]
	v_mfma_f32_16x16x32_bf16 v[94:97], v[162:165], v[194:197], v[94:97]
	v_mfma_f32_16x16x32_bf16 v[90:93], v[170:173], v[194:197], v[90:93]
	v_mfma_f32_16x16x32_bf16 v[78:81], v[162:165], v[202:205], v[78:81]
	v_mfma_f32_16x16x32_bf16 v[74:77], v[170:173], v[202:205], v[74:77]
	s_setprio 0
	s_barrier
	s_add_i32 s16, 0, 0x1c000
	s_add_i32 s17, s62, s33
	v_add_u32_e32 v134, s16, v149
	v_lshl_add_u64 v[224:225], v[224:225], 0, s[0:1]
	s_mov_b32 m0, s17
	ds_read_b128 v[206:209], v134
	ds_read_b128 v[210:213], v134 offset:1024
	ds_read_b128 v[214:217], v134 offset:2048
	ds_read_b128 v[218:221], v134 offset:3072
	global_load_lds_dwordx4 v[224:225], off
	v_lshl_add_u64 v[224:225], v[226:227], 0, s[0:1]
	s_add_i32 m0, s17, 0x2000
	s_nop 0
	global_load_lds_dwordx4 v[224:225], off
	s_barrier
	s_waitcnt lgkmcnt(0)
	s_setprio 1
	s_waitcnt lgkmcnt(0)
	v_mfma_f32_16x16x32_bf16 v[118:121], v[206:209], v[174:177], v[118:121]
	v_mfma_f32_16x16x32_bf16 v[114:117], v[214:217], v[174:177], v[114:117]
	v_mfma_f32_16x16x32_bf16 v[102:105], v[206:209], v[182:185], v[102:105]
	v_mfma_f32_16x16x32_bf16 v[98:101], v[214:217], v[182:185], v[98:101]
	v_mfma_f32_16x16x32_bf16 v[86:89], v[206:209], v[190:193], v[86:89]
	v_mfma_f32_16x16x32_bf16 v[82:85], v[214:217], v[190:193], v[82:85]
	v_mfma_f32_16x16x32_bf16 v[70:73], v[206:209], v[198:201], v[70:73]
	v_mfma_f32_16x16x32_bf16 v[66:69], v[214:217], v[198:201], v[66:69]
	v_mfma_f32_16x16x32_bf16 v[118:121], v[210:213], v[178:181], v[118:121]
	v_mfma_f32_16x16x32_bf16 v[114:117], v[218:221], v[178:181], v[114:117]
	v_mfma_f32_16x16x32_bf16 v[102:105], v[210:213], v[186:189], v[102:105]
	v_mfma_f32_16x16x32_bf16 v[98:101], v[218:221], v[186:189], v[98:101]
	v_mfma_f32_16x16x32_bf16 v[86:89], v[210:213], v[194:197], v[86:89]
	v_mfma_f32_16x16x32_bf16 v[82:85], v[218:221], v[194:197], v[82:85]
	v_mfma_f32_16x16x32_bf16 v[70:73], v[210:213], v[202:205], v[70:73]
	v_mfma_f32_16x16x32_bf16 v[66:69], v[218:221], v[202:205], v[66:69]
	s_setprio 0
	s_mov_b32 m0, s40
	v_lshl_add_u64 v[224:225], v[228:229], 0, s[0:1]
	s_barrier
	ds_read_b128 v[174:177], v152 offset:49152
	ds_read_b128 v[178:181], v152 offset:50176
	ds_read_b128 v[182:185], v152 offset:51200
	ds_read_b128 v[186:189], v152 offset:52224
	ds_read_b128 v[190:193], v152 offset:53248
	ds_read_b128 v[194:197], v152 offset:54272
	ds_read_b128 v[198:201], v152 offset:55296
	ds_read_b128 v[202:205], v152 offset:56320
	global_load_lds_dwordx4 v[224:225], off
	v_lshl_add_u64 v[222:223], v[222:223], 0, s[0:1]
	s_mov_b32 m0, s41
	s_nop 0
	global_load_lds_dwordx4 v[222:223], off
	s_barrier
	s_waitcnt lgkmcnt(0)
	s_setprio 1
	s_waitcnt lgkmcnt(0)
	v_mfma_f32_16x16x32_bf16 v[62:65], v[158:161], v[174:177], v[62:65]
	v_mfma_f32_16x16x32_bf16 v[58:61], v[166:169], v[174:177], v[58:61]
	v_mfma_f32_16x16x32_bf16 v[46:49], v[158:161], v[182:185], v[46:49]
	v_mfma_f32_16x16x32_bf16 v[42:45], v[166:169], v[182:185], v[42:45]
	v_mfma_f32_16x16x32_bf16 v[30:33], v[158:161], v[190:193], v[30:33]
	v_mfma_f32_16x16x32_bf16 v[26:29], v[166:169], v[190:193], v[26:29]
	v_mfma_f32_16x16x32_bf16 v[14:17], v[158:161], v[198:201], v[14:17]
	v_mfma_f32_16x16x32_bf16 v[10:13], v[166:169], v[198:201], v[10:13]
	v_mfma_f32_16x16x32_bf16 v[62:65], v[162:165], v[178:181], v[62:65]
	v_mfma_f32_16x16x32_bf16 v[58:61], v[170:173], v[178:181], v[58:61]
	v_mfma_f32_16x16x32_bf16 v[46:49], v[162:165], v[186:189], v[46:49]
	v_mfma_f32_16x16x32_bf16 v[42:45], v[170:173], v[186:189], v[42:45]
	v_mfma_f32_16x16x32_bf16 v[30:33], v[162:165], v[194:197], v[30:33]
	v_mfma_f32_16x16x32_bf16 v[26:29], v[170:173], v[194:197], v[26:29]
	v_mfma_f32_16x16x32_bf16 v[14:17], v[162:165], v[202:205], v[14:17]
	v_mfma_f32_16x16x32_bf16 v[10:13], v[170:173], v[202:205], v[10:13]
	s_setprio 0
	s_barrier
	s_add_u32 s14, s14, 0x80080
	s_addc_u32 s15, s15, 0
	s_add_i32 s16, s16, s33
	s_mov_b32 m0, s16
	s_nop 0
	global_load_lds_dwordx4 v132, s[14:15]
	s_add_i32 m0, s16, 0x2000
	s_nop 0
	global_load_lds_dwordx4 v130, s[14:15]
	s_waitcnt vmcnt(6)
	s_barrier
	s_setprio 1
	v_mfma_f32_16x16x32_bf16 v[54:57], v[206:209], v[174:177], v[54:57]
	v_mfma_f32_16x16x32_bf16 v[50:53], v[214:217], v[174:177], v[50:53]
	v_mfma_f32_16x16x32_bf16 v[38:41], v[206:209], v[182:185], v[38:41]
	v_mfma_f32_16x16x32_bf16 v[34:37], v[214:217], v[182:185], v[34:37]
	v_mfma_f32_16x16x32_bf16 v[22:25], v[206:209], v[190:193], v[22:25]
	v_mfma_f32_16x16x32_bf16 v[18:21], v[214:217], v[190:193], v[18:21]
	v_mfma_f32_16x16x32_bf16 v[6:9], v[206:209], v[198:201], v[6:9]
	v_mfma_f32_16x16x32_bf16 v[2:5], v[214:217], v[198:201], v[2:5]
	v_mfma_f32_16x16x32_bf16 v[54:57], v[210:213], v[178:181], v[54:57]
	v_mfma_f32_16x16x32_bf16 v[50:53], v[218:221], v[178:181], v[50:53]
	v_mfma_f32_16x16x32_bf16 v[38:41], v[210:213], v[186:189], v[38:41]
	v_mfma_f32_16x16x32_bf16 v[34:37], v[218:221], v[186:189], v[34:37]
	v_mfma_f32_16x16x32_bf16 v[22:25], v[210:213], v[194:197], v[22:25]
	v_mfma_f32_16x16x32_bf16 v[18:21], v[218:221], v[194:197], v[18:21]
	v_mfma_f32_16x16x32_bf16 v[6:9], v[210:213], v[202:205], v[6:9]
	v_mfma_f32_16x16x32_bf16 v[2:5], v[218:221], v[202:205], v[2:5]
	s_setprio 0
	s_add_i32 s61, s61, 2
	s_add_u32 s12, s12, 0x100
	s_addc_u32 s13, s13, 0
	s_cmp_gt_u32 s61, 29
	s_barrier
	s_cbranch_scc1 .Lpeel_1522_after
.LBB0_1522:
	s_add_u32 s14, s28, s12
	s_addc_u32 s15, s29, s13
	s_add_u32 s16, s14, 0x2a300100
	ds_read_b128 v[158:161], v151
	ds_read_b128 v[162:165], v151 offset:1024
	ds_read_b128 v[166:169], v151 offset:2048
	ds_read_b128 v[170:173], v151 offset:3072
	s_addc_u32 s17, s15, 0
	s_add_u32 s62, s59, s12
	s_addc_u32 s63, s60, s13
	s_cmpk_eq_i32 s12, 0xf00
	s_cselect_b64 vcc, -1, 0
	s_and_b64 s[14:15], vcc, exec
	v_cndmask_b32_e32 v134, v137, v154, vcc
	v_cndmask_b32_e32 v222, v136, v155, vcc
	v_cndmask_b32_e32 v139, v138, v156, vcc
	v_cndmask_b32_e32 v141, v140, v157, vcc
	s_cselect_b32 s17, s37, s17
	s_cselect_b32 s16, s36, s16
	s_cselect_b32 s15, s9, s63
	s_cselect_b32 s14, s58, s62
	v_lshl_add_u64 v[206:207], v[144:145], 0, s[12:13]
	s_add_i32 m0, s34, 0xc000
	ds_read_b128 v[174:177], v152
	ds_read_b128 v[178:181], v152 offset:1024
	ds_read_b128 v[182:185], v152 offset:2048
	ds_read_b128 v[186:189], v152 offset:3072
	ds_read_b128 v[190:193], v152 offset:4096
	ds_read_b128 v[194:197], v152 offset:5120
	ds_read_b128 v[198:201], v152 offset:6144
	ds_read_b128 v[202:205], v152 offset:7168
	global_load_lds_dwordx4 v[206:207], off
	v_lshl_add_u64 v[206:207], v[142:143], 0, s[12:13]
	s_add_i32 m0, s34, 0xe000
	s_nop 0
	global_load_lds_dwordx4 v[206:207], off
	s_waitcnt lgkmcnt(8)
	s_barrier
	s_waitcnt lgkmcnt(0)
	s_setprio 1
	s_waitcnt lgkmcnt(0)
	v_mfma_f32_16x16x32_bf16 v[126:129], v[158:161], v[174:177], v[126:129]
	v_mfma_f32_16x16x32_bf16 v[122:125], v[166:169], v[174:177], v[122:125]
	v_mfma_f32_16x16x32_bf16 v[110:113], v[158:161], v[182:185], v[110:113]
	v_mfma_f32_16x16x32_bf16 v[106:109], v[166:169], v[182:185], v[106:109]
	v_mfma_f32_16x16x32_bf16 v[94:97], v[158:161], v[190:193], v[94:97]
	v_mfma_f32_16x16x32_bf16 v[90:93], v[166:169], v[190:193], v[90:93]
	v_mfma_f32_16x16x32_bf16 v[78:81], v[158:161], v[198:201], v[78:81]
	v_mfma_f32_16x16x32_bf16 v[74:77], v[166:169], v[198:201], v[74:77]
	v_mfma_f32_16x16x32_bf16 v[126:129], v[162:165], v[178:181], v[126:129]
	v_mfma_f32_16x16x32_bf16 v[122:125], v[170:173], v[178:181], v[122:125]
	v_mfma_f32_16x16x32_bf16 v[110:113], v[162:165], v[186:189], v[110:113]
	v_mfma_f32_16x16x32_bf16 v[106:109], v[170:173], v[186:189], v[106:109]
	v_mfma_f32_16x16x32_bf16 v[94:97], v[162:165], v[194:197], v[94:97]
	v_mfma_f32_16x16x32_bf16 v[90:93], v[170:173], v[194:197], v[90:93]
	v_mfma_f32_16x16x32_bf16 v[78:81], v[162:165], v[202:205], v[78:81]
	v_mfma_f32_16x16x32_bf16 v[74:77], v[170:173], v[202:205], v[74:77]
	s_setprio 0
	s_barrier
	s_add_i32 s62, s42, s33
	v_lshl_add_u64 v[224:225], s[14:15], 0, v[132:133]
	s_mov_b32 m0, s62
	ds_read_b128 v[206:209], v153
	ds_read_b128 v[210:213], v153 offset:1024
	ds_read_b128 v[214:217], v153 offset:2048
	ds_read_b128 v[218:221], v153 offset:3072
	global_load_lds_dwordx4 v[224:225], off
	v_lshl_add_u64 v[226:227], s[14:15], 0, v[130:131]
	s_add_i32 m0, s62, 0x2000
	s_nop 0
	global_load_lds_dwordx4 v[226:227], off
	s_barrier
	s_waitcnt lgkmcnt(0)
	s_setprio 1
	s_waitcnt lgkmcnt(0)
	v_mfma_f32_16x16x32_bf16 v[118:121], v[206:209], v[174:177], v[118:121]
	v_mfma_f32_16x16x32_bf16 v[114:117], v[214:217], v[174:177], v[114:117]
	v_mfma_f32_16x16x32_bf16 v[102:105], v[206:209], v[182:185], v[102:105]
	v_mfma_f32_16x16x32_bf16 v[98:101], v[214:217], v[182:185], v[98:101]
	v_mfma_f32_16x16x32_bf16 v[86:89], v[206:209], v[190:193], v[86:89]
	v_mfma_f32_16x16x32_bf16 v[82:85], v[214:217], v[190:193], v[82:85]
	v_mfma_f32_16x16x32_bf16 v[70:73], v[206:209], v[198:201], v[70:73]
	v_mfma_f32_16x16x32_bf16 v[66:69], v[214:217], v[198:201], v[66:69]
	v_mfma_f32_16x16x32_bf16 v[118:121], v[210:213], v[178:181], v[118:121]
	v_mfma_f32_16x16x32_bf16 v[114:117], v[218:221], v[178:181], v[114:117]
	v_mfma_f32_16x16x32_bf16 v[102:105], v[210:213], v[186:189], v[102:105]
	v_mfma_f32_16x16x32_bf16 v[98:101], v[218:221], v[186:189], v[98:101]
	v_mfma_f32_16x16x32_bf16 v[86:89], v[210:213], v[194:197], v[86:89]
	v_mfma_f32_16x16x32_bf16 v[82:85], v[218:221], v[194:197], v[82:85]
	v_mfma_f32_16x16x32_bf16 v[70:73], v[210:213], v[202:205], v[70:73]
	v_mfma_f32_16x16x32_bf16 v[66:69], v[218:221], v[202:205], v[66:69]
	s_setprio 0
	s_mov_b32 m0, s34
	s_barrier
	ds_read_b128 v[174:177], v152 offset:16384
	ds_read_b128 v[178:181], v152 offset:17408
	ds_read_b128 v[182:185], v152 offset:18432
	ds_read_b128 v[186:189], v152 offset:19456
	ds_read_b128 v[190:193], v152 offset:20480
	ds_read_b128 v[194:197], v152 offset:21504
	ds_read_b128 v[198:201], v152 offset:22528
	ds_read_b128 v[202:205], v152 offset:23552
	global_load_lds_dwordx4 v134, s[16:17]
	s_mov_b32 m0, s35
	v_mov_b32_e32 v223, v135
	global_load_lds_dwordx4 v222, s[16:17]
	s_barrier
	s_waitcnt lgkmcnt(0)
	v_lshl_add_u64 v[228:229], s[16:17], 0, v[134:135]
	v_lshl_add_u64 v[222:223], s[16:17], 0, v[222:223]
	s_setprio 1
	s_waitcnt lgkmcnt(0)
	v_mfma_f32_16x16x32_bf16 v[62:65], v[158:161], v[174:177], v[62:65]
	v_mfma_f32_16x16x32_bf16 v[58:61], v[166:169], v[174:177], v[58:61]
	v_mfma_f32_16x16x32_bf16 v[46:49], v[158:161], v[182:185], v[46:49]
	v_mfma_f32_16x16x32_bf16 v[42:45], v[166:169], v[182:185], v[42:45]
	v_mfma_f32_16x16x32_bf16 v[30:33], v[158:161], v[190:193], v[30:33]
	v_mfma_f32_16x16x32_bf16 v[26:29], v[166:169], v[190:193], v[26:29]
	v_mfma_f32_16x16x32_bf16 v[14:17], v[158:161], v[198:201], v[14:17]
	v_mfma_f32_16x16x32_bf16 v[10:13], v[166:169], v[198:201], v[10:13]
	v_mfma_f32_16x16x32_bf16 v[62:65], v[162:165], v[178:181], v[62:65]
	v_mfma_f32_16x16x32_bf16 v[58:61], v[170:173], v[178:181], v[58:61]
	v_mfma_f32_16x16x32_bf16 v[46:49], v[162:165], v[186:189], v[46:49]
	v_mfma_f32_16x16x32_bf16 v[42:45], v[170:173], v[186:189], v[42:45]
	v_mfma_f32_16x16x32_bf16 v[30:33], v[162:165], v[194:197], v[30:33]
	v_mfma_f32_16x16x32_bf16 v[26:29], v[170:173], v[194:197], v[26:29]
	v_mfma_f32_16x16x32_bf16 v[14:17], v[162:165], v[202:205], v[14:17]
	v_mfma_f32_16x16x32_bf16 v[10:13], v[170:173], v[202:205], v[10:13]
	s_setprio 0
	s_barrier
	s_add_u32 s62, s14, 0x80000
	s_addc_u32 s63, s15, 0
	s_add_i32 s64, s43, s33
	s_mov_b32 m0, s64
	s_nop 0
	global_load_lds_dwordx4 v132, s[62:63]
	s_add_i32 m0, s64, 0x2000
	s_nop 0
	global_load_lds_dwordx4 v130, s[62:63]
	s_waitcnt vmcnt(6)
	s_barrier
	s_setprio 1
	v_mfma_f32_16x16x32_bf16 v[54:57], v[206:209], v[174:177], v[54:57]
	v_mfma_f32_16x16x32_bf16 v[50:53], v[214:217], v[174:177], v[50:53]
	v_mfma_f32_16x16x32_bf16 v[38:41], v[206:209], v[182:185], v[38:41]
	v_mfma_f32_16x16x32_bf16 v[34:37], v[214:217], v[182:185], v[34:37]
	v_mfma_f32_16x16x32_bf16 v[22:25], v[206:209], v[190:193], v[22:25]
	v_mfma_f32_16x16x32_bf16 v[18:21], v[214:217], v[190:193], v[18:21]
	v_mfma_f32_16x16x32_bf16 v[6:9], v[206:209], v[198:201], v[6:9]
	v_mfma_f32_16x16x32_bf16 v[2:5], v[214:217], v[198:201], v[2:5]
	v_mfma_f32_16x16x32_bf16 v[54:57], v[210:213], v[178:181], v[54:57]
	v_mfma_f32_16x16x32_bf16 v[50:53], v[218:221], v[178:181], v[50:53]
	v_mfma_f32_16x16x32_bf16 v[38:41], v[210:213], v[186:189], v[38:41]
	v_mfma_f32_16x16x32_bf16 v[34:37], v[218:221], v[186:189], v[34:37]
	v_mfma_f32_16x16x32_bf16 v[22:25], v[210:213], v[194:197], v[22:25]
	v_mfma_f32_16x16x32_bf16 v[18:21], v[218:221], v[194:197], v[18:21]
	v_mfma_f32_16x16x32_bf16 v[6:9], v[210:213], v[202:205], v[6:9]
	v_mfma_f32_16x16x32_bf16 v[2:5], v[218:221], v[202:205], v[2:5]
	s_setprio 0
	s_add_i32 s62, 0, 0x18000
	v_add_u32_e32 v134, s62, v149
	s_barrier
	ds_read_b128 v[158:161], v134
	ds_read_b128 v[162:165], v134 offset:1024
	ds_read_b128 v[166:169], v134 offset:2048
	ds_read_b128 v[170:173], v134 offset:3072
	s_mov_b32 m0, s38
	ds_read_b128 v[174:177], v152 offset:32768
	ds_read_b128 v[178:181], v152 offset:33792
	ds_read_b128 v[182:185], v152 offset:34816
	ds_read_b128 v[186:189], v152 offset:35840
	ds_read_b128 v[190:193], v152 offset:36864
	ds_read_b128 v[194:197], v152 offset:37888
	ds_read_b128 v[198:201], v152 offset:38912
	ds_read_b128 v[202:205], v152 offset:39936
	global_load_lds_dwordx4 v139, s[16:17]
	s_mov_b32 m0, s39
	s_nop 0
	global_load_lds_dwordx4 v141, s[16:17]
	s_waitcnt lgkmcnt(8)
	s_barrier
	s_waitcnt lgkmcnt(0)
	s_setprio 1
	s_waitcnt lgkmcnt(0)
	v_mfma_f32_16x16x32_bf16 v[126:129], v[158:161], v[174:177], v[126:129]
	v_mfma_f32_16x16x32_bf16 v[122:125], v[166:169], v[174:177], v[122:125]
	v_mfma_f32_16x16x32_bf16 v[110:113], v[158:161], v[182:185], v[110:113]
	v_mfma_f32_16x16x32_bf16 v[106:109], v[166:169], v[182:185], v[106:109]
	v_mfma_f32_16x16x32_bf16 v[94:97], v[158:161], v[190:193], v[94:97]
	v_mfma_f32_16x16x32_bf16 v[90:93], v[166:169], v[190:193], v[90:93]
	v_mfma_f32_16x16x32_bf16 v[78:81], v[158:161], v[198:201], v[78:81]
	v_mfma_f32_16x16x32_bf16 v[74:77], v[166:169], v[198:201], v[74:77]
	v_mfma_f32_16x16x32_bf16 v[126:129], v[162:165], v[178:181], v[126:129]
	v_mfma_f32_16x16x32_bf16 v[122:125], v[170:173], v[178:181], v[122:125]
	v_mfma_f32_16x16x32_bf16 v[110:113], v[162:165], v[186:189], v[110:113]
	v_mfma_f32_16x16x32_bf16 v[106:109], v[170:173], v[186:189], v[106:109]
	v_mfma_f32_16x16x32_bf16 v[94:97], v[162:165], v[194:197], v[94:97]
	v_mfma_f32_16x16x32_bf16 v[90:93], v[170:173], v[194:197], v[90:93]
	v_mfma_f32_16x16x32_bf16 v[78:81], v[162:165], v[202:205], v[78:81]
	v_mfma_f32_16x16x32_bf16 v[74:77], v[170:173], v[202:205], v[74:77]
	s_setprio 0
	s_barrier
	s_add_i32 s16, 0, 0x1c000
	s_add_i32 s17, s62, s33
	v_add_u32_e32 v134, s16, v149
	v_lshl_add_u64 v[224:225], v[224:225], 0, s[0:1]
	s_mov_b32 m0, s17
	ds_read_b128 v[206:209], v134
	ds_read_b128 v[210:213], v134 offset:1024
	ds_read_b128 v[214:217], v134 offset:2048
	ds_read_b128 v[218:221], v134 offset:3072
	global_load_lds_dwordx4 v[224:225], off
	v_lshl_add_u64 v[224:225], v[226:227], 0, s[0:1]
	s_add_i32 m0, s17, 0x2000
	s_nop 0
	global_load_lds_dwordx4 v[224:225], off
	s_barrier
	s_waitcnt lgkmcnt(0)
	s_setprio 1
	s_waitcnt lgkmcnt(0)
	v_mfma_f32_16x16x32_bf16 v[118:121], v[206:209], v[174:177], v[118:121]
	v_mfma_f32_16x16x32_bf16 v[114:117], v[214:217], v[174:177], v[114:117]
	v_mfma_f32_16x16x32_bf16 v[102:105], v[206:209], v[182:185], v[102:105]
	v_mfma_f32_16x16x32_bf16 v[98:101], v[214:217], v[182:185], v[98:101]
	v_mfma_f32_16x16x32_bf16 v[86:89], v[206:209], v[190:193], v[86:89]
	v_mfma_f32_16x16x32_bf16 v[82:85], v[214:217], v[190:193], v[82:85]
	v_mfma_f32_16x16x32_bf16 v[70:73], v[206:209], v[198:201], v[70:73]
	v_mfma_f32_16x16x32_bf16 v[66:69], v[214:217], v[198:201], v[66:69]
	v_mfma_f32_16x16x32_bf16 v[118:121], v[210:213], v[178:181], v[118:121]
	v_mfma_f32_16x16x32_bf16 v[114:117], v[218:221], v[178:181], v[114:117]
	v_mfma_f32_16x16x32_bf16 v[102:105], v[210:213], v[186:189], v[102:105]
	v_mfma_f32_16x16x32_bf16 v[98:101], v[218:221], v[186:189], v[98:101]
	v_mfma_f32_16x16x32_bf16 v[86:89], v[210:213], v[194:197], v[86:89]
	v_mfma_f32_16x16x32_bf16 v[82:85], v[218:221], v[194:197], v[82:85]
	v_mfma_f32_16x16x32_bf16 v[70:73], v[210:213], v[202:205], v[70:73]
	v_mfma_f32_16x16x32_bf16 v[66:69], v[218:221], v[202:205], v[66:69]
	s_setprio 0
	s_mov_b32 m0, s40
	v_lshl_add_u64 v[224:225], v[228:229], 0, s[0:1]
	s_barrier
	ds_read_b128 v[174:177], v152 offset:49152
	ds_read_b128 v[178:181], v152 offset:50176
	ds_read_b128 v[182:185], v152 offset:51200
	ds_read_b128 v[186:189], v152 offset:52224
	ds_read_b128 v[190:193], v152 offset:53248
	ds_read_b128 v[194:197], v152 offset:54272
	ds_read_b128 v[198:201], v152 offset:55296
	ds_read_b128 v[202:205], v152 offset:56320
	global_load_lds_dwordx4 v[224:225], off
	v_lshl_add_u64 v[222:223], v[222:223], 0, s[0:1]
	s_mov_b32 m0, s41
	s_nop 0
	global_load_lds_dwordx4 v[222:223], off
	s_barrier
	s_waitcnt lgkmcnt(0)
	s_setprio 1
	s_waitcnt lgkmcnt(0)
	v_mfma_f32_16x16x32_bf16 v[62:65], v[158:161], v[174:177], v[62:65]
	v_mfma_f32_16x16x32_bf16 v[58:61], v[166:169], v[174:177], v[58:61]
	v_mfma_f32_16x16x32_bf16 v[46:49], v[158:161], v[182:185], v[46:49]
	v_mfma_f32_16x16x32_bf16 v[42:45], v[166:169], v[182:185], v[42:45]
	v_mfma_f32_16x16x32_bf16 v[30:33], v[158:161], v[190:193], v[30:33]
	v_mfma_f32_16x16x32_bf16 v[26:29], v[166:169], v[190:193], v[26:29]
	v_mfma_f32_16x16x32_bf16 v[14:17], v[158:161], v[198:201], v[14:17]
	v_mfma_f32_16x16x32_bf16 v[10:13], v[166:169], v[198:201], v[10:13]
	v_mfma_f32_16x16x32_bf16 v[62:65], v[162:165], v[178:181], v[62:65]
	v_mfma_f32_16x16x32_bf16 v[58:61], v[170:173], v[178:181], v[58:61]
	v_mfma_f32_16x16x32_bf16 v[46:49], v[162:165], v[186:189], v[46:49]
	v_mfma_f32_16x16x32_bf16 v[42:45], v[170:173], v[186:189], v[42:45]
	v_mfma_f32_16x16x32_bf16 v[30:33], v[162:165], v[194:197], v[30:33]
	v_mfma_f32_16x16x32_bf16 v[26:29], v[170:173], v[194:197], v[26:29]
	v_mfma_f32_16x16x32_bf16 v[14:17], v[162:165], v[202:205], v[14:17]
	v_mfma_f32_16x16x32_bf16 v[10:13], v[170:173], v[202:205], v[10:13]
	s_setprio 0
	s_barrier
	s_add_u32 s14, s14, 0x80080
	s_addc_u32 s15, s15, 0
	s_add_i32 s16, s16, s33
	s_mov_b32 m0, s16
	s_nop 0
	global_load_lds_dwordx4 v132, s[14:15]
	s_add_i32 m0, s16, 0x2000
	s_nop 0
	global_load_lds_dwordx4 v130, s[14:15]
	s_waitcnt vmcnt(6)
	s_barrier
	s_setprio 1
	v_mfma_f32_16x16x32_bf16 v[54:57], v[206:209], v[174:177], v[54:57]
	v_mfma_f32_16x16x32_bf16 v[50:53], v[214:217], v[174:177], v[50:53]
	v_mfma_f32_16x16x32_bf16 v[38:41], v[206:209], v[182:185], v[38:41]
	v_mfma_f32_16x16x32_bf16 v[34:37], v[214:217], v[182:185], v[34:37]
	v_mfma_f32_16x16x32_bf16 v[22:25], v[206:209], v[190:193], v[22:25]
	v_mfma_f32_16x16x32_bf16 v[18:21], v[214:217], v[190:193], v[18:21]
	v_mfma_f32_16x16x32_bf16 v[6:9], v[206:209], v[198:201], v[6:9]
	v_mfma_f32_16x16x32_bf16 v[2:5], v[214:217], v[198:201], v[2:5]
	v_mfma_f32_16x16x32_bf16 v[54:57], v[210:213], v[178:181], v[54:57]
	v_mfma_f32_16x16x32_bf16 v[50:53], v[218:221], v[178:181], v[50:53]
	v_mfma_f32_16x16x32_bf16 v[38:41], v[210:213], v[186:189], v[38:41]
	v_mfma_f32_16x16x32_bf16 v[34:37], v[218:221], v[186:189], v[34:37]
	v_mfma_f32_16x16x32_bf16 v[22:25], v[210:213], v[194:197], v[22:25]
	v_mfma_f32_16x16x32_bf16 v[18:21], v[218:221], v[194:197], v[18:21]
	v_mfma_f32_16x16x32_bf16 v[6:9], v[210:213], v[202:205], v[6:9]
	v_mfma_f32_16x16x32_bf16 v[2:5], v[218:221], v[202:205], v[2:5]
	s_setprio 0
	s_add_i32 s61, s61, 2
	s_add_u32 s12, s12, 0x100
	s_addc_u32 s13, s13, 0
	s_cmp_gt_u32 s61, 29
	s_barrier
	s_cbranch_scc0 .LBB0_1522

.LBB0_1626:
	s_add_u32 s18, s18, 0x30080
	s_addc_u32 s19, s19, 0
	s_add_u32 s64, s20, 0x100
	v_mov_b32_e32 v2, 0
	s_addc_u32 s65, s21, 0
	s_mov_b32 s66, -2
	ds_read_b128 v[148:151], v144
	ds_read_b128 v[152:155], v144 offset:1024
	ds_read_b128 v[156:159], v144 offset:2048
	ds_read_b128 v[160:163], v144 offset:3072
	s_add_u32 s20, s18, 0xfffd0080
	s_addc_u32 s21, s19, -1
	s_cmp_eq_u32 s66, 8
	s_cselect_b32 s23, s17, s21
	s_cselect_b32 s22, s16, s20
	s_cselect_b32 s21, s1, s65
	s_cselect_b32 s20, s0, s64
	s_add_i32 m0, s40, 0xc000
	ds_read_b128 v[164:167], v145
	ds_read_b128 v[168:171], v145 offset:1024
	ds_read_b128 v[172:175], v145 offset:2048
	ds_read_b128 v[176:179], v145 offset:3072
	ds_read_b128 v[180:183], v145 offset:4096
	ds_read_b128 v[184:187], v145 offset:5120
	ds_read_b128 v[188:191], v145 offset:6144
	ds_read_b128 v[192:195], v145 offset:7168
	global_load_lds_dwordx4 v138, s[18:19]
	s_add_i32 m0, s40, 0xe000
	s_nop 0
	global_load_lds_dwordx4 v140, s[18:19]
	s_waitcnt lgkmcnt(8)
	s_barrier
	s_waitcnt lgkmcnt(0)
	s_setprio 1
	s_waitcnt lgkmcnt(0)
	v_mfma_f32_16x16x32_bf16 v[126:129], v[148:151], v[164:167], 0
	v_mfma_f32_16x16x32_bf16 v[122:125], v[156:159], v[164:167], 0
	v_mfma_f32_16x16x32_bf16 v[118:121], v[148:151], v[172:175], 0
	v_mfma_f32_16x16x32_bf16 v[114:117], v[156:159], v[172:175], 0
	v_mfma_f32_16x16x32_bf16 v[102:105], v[148:151], v[180:183], 0
	v_mfma_f32_16x16x32_bf16 v[98:101], v[156:159], v[180:183], 0
	v_mfma_f32_16x16x32_bf16 v[86:89], v[148:151], v[188:191], 0
	v_mfma_f32_16x16x32_bf16 v[82:85], v[156:159], v[188:191], 0
	v_mfma_f32_16x16x32_bf16 v[126:129], v[152:155], v[168:171], v[126:129]
	v_mfma_f32_16x16x32_bf16 v[122:125], v[160:163], v[168:171], v[122:125]
	v_mfma_f32_16x16x32_bf16 v[118:121], v[152:155], v[176:179], v[118:121]
	v_mfma_f32_16x16x32_bf16 v[114:117], v[160:163], v[176:179], v[114:117]
	v_mfma_f32_16x16x32_bf16 v[102:105], v[152:155], v[184:187], v[102:105]
	v_mfma_f32_16x16x32_bf16 v[98:101], v[160:163], v[184:187], v[98:101]
	v_mfma_f32_16x16x32_bf16 v[86:89], v[152:155], v[192:195], v[86:89]
	v_mfma_f32_16x16x32_bf16 v[82:85], v[160:163], v[192:195], v[82:85]
	s_setprio 0
	s_barrier
	s_add_i32 s67, s52, s39
	v_lshl_add_u64 v[212:213], s[20:21], 0, v[134:135]
	s_mov_b32 m0, s67
	ds_read_b128 v[196:199], v146
	ds_read_b128 v[200:203], v146 offset:1024
	ds_read_b128 v[204:207], v146 offset:2048
	ds_read_b128 v[208:211], v146 offset:3072
	global_load_lds_dwordx4 v[212:213], off
	v_lshl_add_u64 v[214:215], s[20:21], 0, v[130:131]
	s_add_i32 m0, s67, 0x2000
	s_nop 0
	global_load_lds_dwordx4 v[214:215], off
	s_barrier
	s_waitcnt lgkmcnt(0)
	s_setprio 1
	s_waitcnt lgkmcnt(0)
	v_mfma_f32_16x16x32_bf16 v[110:113], v[196:199], v[164:167], 0
	v_mfma_f32_16x16x32_bf16 v[106:109], v[204:207], v[164:167], 0
	v_mfma_f32_16x16x32_bf16 v[94:97], v[196:199], v[172:175], 0
	v_mfma_f32_16x16x32_bf16 v[90:93], v[204:207], v[172:175], 0
	v_mfma_f32_16x16x32_bf16 v[78:81], v[196:199], v[180:183], 0
	v_mfma_f32_16x16x32_bf16 v[74:77], v[204:207], v[180:183], 0
	v_mfma_f32_16x16x32_bf16 v[70:73], v[196:199], v[188:191], 0
	v_mfma_f32_16x16x32_bf16 v[66:69], v[204:207], v[188:191], 0
	v_mfma_f32_16x16x32_bf16 v[110:113], v[200:203], v[168:171], v[110:113]
	v_mfma_f32_16x16x32_bf16 v[106:109], v[208:211], v[168:171], v[106:109]
	v_mfma_f32_16x16x32_bf16 v[94:97], v[200:203], v[176:179], v[94:97]
	v_mfma_f32_16x16x32_bf16 v[90:93], v[208:211], v[176:179], v[90:93]
	v_mfma_f32_16x16x32_bf16 v[78:81], v[200:203], v[184:187], v[78:81]
	v_mfma_f32_16x16x32_bf16 v[74:77], v[208:211], v[184:187], v[74:77]
	v_mfma_f32_16x16x32_bf16 v[70:73], v[200:203], v[192:195], v[70:73]
	v_mfma_f32_16x16x32_bf16 v[66:69], v[208:211], v[192:195], v[66:69]
	s_setprio 0
	s_mov_b32 m0, s40
	v_lshl_add_u64 v[216:217], s[22:23], 0, v[136:137]
	s_barrier
	ds_read_b128 v[164:167], v145 offset:16384
	ds_read_b128 v[168:171], v145 offset:17408
	ds_read_b128 v[172:175], v145 offset:18432
	ds_read_b128 v[176:179], v145 offset:19456
	ds_read_b128 v[180:183], v145 offset:20480
	ds_read_b128 v[184:187], v145 offset:21504
	ds_read_b128 v[188:191], v145 offset:22528
	ds_read_b128 v[192:195], v145 offset:23552
	global_load_lds_dwordx4 v[216:217], off
	v_lshl_add_u64 v[218:219], s[22:23], 0, v[132:133]
	s_mov_b32 m0, s41
	s_nop 0
	global_load_lds_dwordx4 v[218:219], off
	s_barrier
	s_waitcnt lgkmcnt(0)
	s_setprio 1
	s_waitcnt lgkmcnt(0)
	v_mfma_f32_16x16x32_bf16 v[62:65], v[148:151], v[164:167], 0
	v_mfma_f32_16x16x32_bf16 v[58:61], v[156:159], v[164:167], 0
	v_mfma_f32_16x16x32_bf16 v[54:57], v[148:151], v[172:175], 0
	v_mfma_f32_16x16x32_bf16 v[50:53], v[156:159], v[172:175], 0
	v_mfma_f32_16x16x32_bf16 v[38:41], v[148:151], v[180:183], 0
	v_mfma_f32_16x16x32_bf16 v[34:37], v[156:159], v[180:183], 0
	v_mfma_f32_16x16x32_bf16 v[22:25], v[148:151], v[188:191], 0
	v_mfma_f32_16x16x32_bf16 v[18:21], v[156:159], v[188:191], 0
	v_mfma_f32_16x16x32_bf16 v[62:65], v[152:155], v[168:171], v[62:65]
	v_mfma_f32_16x16x32_bf16 v[58:61], v[160:163], v[168:171], v[58:61]
	v_mfma_f32_16x16x32_bf16 v[54:57], v[152:155], v[176:179], v[54:57]
	v_mfma_f32_16x16x32_bf16 v[50:53], v[160:163], v[176:179], v[50:53]
	v_mfma_f32_16x16x32_bf16 v[38:41], v[152:155], v[184:187], v[38:41]
	v_mfma_f32_16x16x32_bf16 v[34:37], v[160:163], v[184:187], v[34:37]
	v_mfma_f32_16x16x32_bf16 v[22:25], v[152:155], v[192:195], v[22:25]
	v_mfma_f32_16x16x32_bf16 v[18:21], v[160:163], v[192:195], v[18:21]
	s_setprio 0
	s_barrier
	s_add_u32 s68, s20, 0x30000
	s_addc_u32 s69, s21, 0
	s_add_i32 s67, s53, s39
	s_mov_b32 m0, s67
	s_nop 0
	global_load_lds_dwordx4 v134, s[68:69]
	s_add_i32 m0, s67, 0x2000
	s_nop 0
	global_load_lds_dwordx4 v130, s[68:69]
	s_waitcnt vmcnt(6)
	s_barrier
	s_setprio 1
	v_mfma_f32_16x16x32_bf16 v[46:49], v[196:199], v[164:167], 0
	v_mfma_f32_16x16x32_bf16 v[42:45], v[204:207], v[164:167], 0
	v_mfma_f32_16x16x32_bf16 v[30:33], v[196:199], v[172:175], 0
	v_mfma_f32_16x16x32_bf16 v[26:29], v[204:207], v[172:175], 0
	v_mfma_f32_16x16x32_bf16 v[14:17], v[196:199], v[180:183], 0
	v_mfma_f32_16x16x32_bf16 v[10:13], v[204:207], v[180:183], 0
	v_mfma_f32_16x16x32_bf16 v[6:9], v[196:199], v[188:191], 0
	v_mfma_f32_16x16x32_bf16 v[2:5], v[204:207], v[188:191], 0
	v_mfma_f32_16x16x32_bf16 v[46:49], v[200:203], v[168:171], v[46:49]
	v_mfma_f32_16x16x32_bf16 v[42:45], v[208:211], v[168:171], v[42:45]
	v_mfma_f32_16x16x32_bf16 v[30:33], v[200:203], v[176:179], v[30:33]
	v_mfma_f32_16x16x32_bf16 v[26:29], v[208:211], v[176:179], v[26:29]
	v_mfma_f32_16x16x32_bf16 v[14:17], v[200:203], v[184:187], v[14:17]
	v_mfma_f32_16x16x32_bf16 v[10:13], v[208:211], v[184:187], v[10:13]
	v_mfma_f32_16x16x32_bf16 v[6:9], v[200:203], v[192:195], v[6:9]
	v_mfma_f32_16x16x32_bf16 v[2:5], v[208:211], v[192:195], v[2:5]
	s_setprio 0
	s_add_i32 s67, 0, 0x18000
	v_add_u32_e32 v147, s67, v1
	s_barrier
	ds_read_b128 v[148:151], v147
	ds_read_b128 v[152:155], v147 offset:1024
	ds_read_b128 v[156:159], v147 offset:2048
	ds_read_b128 v[160:163], v147 offset:3072
	s_add_u32 s22, s22, 0x30000
	s_addc_u32 s23, s23, 0
	s_mov_b32 m0, s42
	ds_read_b128 v[164:167], v145 offset:32768
	ds_read_b128 v[168:171], v145 offset:33792
	ds_read_b128 v[172:175], v145 offset:34816
	ds_read_b128 v[176:179], v145 offset:35840
	ds_read_b128 v[180:183], v145 offset:36864
	ds_read_b128 v[184:187], v145 offset:37888
	ds_read_b128 v[188:191], v145 offset:38912
	ds_read_b128 v[192:195], v145 offset:39936
	global_load_lds_dwordx4 v136, s[22:23]
	s_mov_b32 m0, s43
	s_nop 0
	global_load_lds_dwordx4 v132, s[22:23]
	s_waitcnt lgkmcnt(8)
	s_barrier
	s_waitcnt lgkmcnt(0)
	s_setprio 1
	s_waitcnt lgkmcnt(0)
	v_mfma_f32_16x16x32_bf16 v[126:129], v[148:151], v[164:167], v[126:129]
	v_mfma_f32_16x16x32_bf16 v[122:125], v[156:159], v[164:167], v[122:125]
	v_mfma_f32_16x16x32_bf16 v[118:121], v[148:151], v[172:175], v[118:121]
	v_mfma_f32_16x16x32_bf16 v[114:117], v[156:159], v[172:175], v[114:117]
	v_mfma_f32_16x16x32_bf16 v[102:105], v[148:151], v[180:183], v[102:105]
	v_mfma_f32_16x16x32_bf16 v[98:101], v[156:159], v[180:183], v[98:101]
	v_mfma_f32_16x16x32_bf16 v[86:89], v[148:151], v[188:191], v[86:89]
	v_mfma_f32_16x16x32_bf16 v[82:85], v[156:159], v[188:191], v[82:85]
	v_mfma_f32_16x16x32_bf16 v[126:129], v[152:155], v[168:171], v[126:129]
	v_mfma_f32_16x16x32_bf16 v[122:125], v[160:163], v[168:171], v[122:125]
	v_mfma_f32_16x16x32_bf16 v[118:121], v[152:155], v[176:179], v[118:121]
	v_mfma_f32_16x16x32_bf16 v[114:117], v[160:163], v[176:179], v[114:117]
	v_mfma_f32_16x16x32_bf16 v[102:105], v[152:155], v[184:187], v[102:105]
	v_mfma_f32_16x16x32_bf16 v[98:101], v[160:163], v[184:187], v[98:101]
	v_mfma_f32_16x16x32_bf16 v[86:89], v[152:155], v[192:195], v[86:89]
	v_mfma_f32_16x16x32_bf16 v[82:85], v[160:163], v[192:195], v[82:85]
	s_setprio 0
	s_barrier
	s_add_i32 s22, 0, 0x1c000
	s_add_i32 s23, s67, s39
	v_add_u32_e32 v147, s22, v1
	v_lshl_add_u64 v[212:213], v[212:213], 0, s[6:7]
	s_mov_b32 m0, s23
	ds_read_b128 v[196:199], v147
	ds_read_b128 v[200:203], v147 offset:1024
	ds_read_b128 v[204:207], v147 offset:2048
	ds_read_b128 v[208:211], v147 offset:3072
	global_load_lds_dwordx4 v[212:213], off
	v_lshl_add_u64 v[212:213], v[214:215], 0, s[6:7]
	s_add_i32 m0, s23, 0x2000
	s_nop 0
	global_load_lds_dwordx4 v[212:213], off
	s_barrier
	s_waitcnt lgkmcnt(0)
	s_setprio 1
	s_waitcnt lgkmcnt(0)
	v_mfma_f32_16x16x32_bf16 v[110:113], v[196:199], v[164:167], v[110:113]
	v_mfma_f32_16x16x32_bf16 v[106:109], v[204:207], v[164:167], v[106:109]
	v_mfma_f32_16x16x32_bf16 v[94:97], v[196:199], v[172:175], v[94:97]
	v_mfma_f32_16x16x32_bf16 v[90:93], v[204:207], v[172:175], v[90:93]
	v_mfma_f32_16x16x32_bf16 v[78:81], v[196:199], v[180:183], v[78:81]
	v_mfma_f32_16x16x32_bf16 v[74:77], v[204:207], v[180:183], v[74:77]
	v_mfma_f32_16x16x32_bf16 v[70:73], v[196:199], v[188:191], v[70:73]
	v_mfma_f32_16x16x32_bf16 v[66:69], v[204:207], v[188:191], v[66:69]
	v_mfma_f32_16x16x32_bf16 v[110:113], v[200:203], v[168:171], v[110:113]
	v_mfma_f32_16x16x32_bf16 v[106:109], v[208:211], v[168:171], v[106:109]
	v_mfma_f32_16x16x32_bf16 v[94:97], v[200:203], v[176:179], v[94:97]
	v_mfma_f32_16x16x32_bf16 v[90:93], v[208:211], v[176:179], v[90:93]
	v_mfma_f32_16x16x32_bf16 v[78:81], v[200:203], v[184:187], v[78:81]
	v_mfma_f32_16x16x32_bf16 v[74:77], v[208:211], v[184:187], v[74:77]
	v_mfma_f32_16x16x32_bf16 v[70:73], v[200:203], v[192:195], v[70:73]
	v_mfma_f32_16x16x32_bf16 v[66:69], v[208:211], v[192:195], v[66:69]
	s_setprio 0
	s_mov_b32 m0, s46
	v_lshl_add_u64 v[212:213], v[216:217], 0, s[6:7]
	s_barrier
	ds_read_b128 v[164:167], v145 offset:49152
	ds_read_b128 v[168:171], v145 offset:50176
	ds_read_b128 v[172:175], v145 offset:51200
	ds_read_b128 v[176:179], v145 offset:52224
	ds_read_b128 v[180:183], v145 offset:53248
	ds_read_b128 v[184:187], v145 offset:54272
	ds_read_b128 v[188:191], v145 offset:55296
	ds_read_b128 v[192:195], v145 offset:56320
	global_load_lds_dwordx4 v[212:213], off
	v_lshl_add_u64 v[212:213], v[218:219], 0, s[6:7]
	s_mov_b32 m0, s47
	s_nop 0
	global_load_lds_dwordx4 v[212:213], off
	s_barrier
	s_waitcnt lgkmcnt(0)
	s_setprio 1
	s_waitcnt lgkmcnt(0)
	v_mfma_f32_16x16x32_bf16 v[62:65], v[148:151], v[164:167], v[62:65]
	v_mfma_f32_16x16x32_bf16 v[58:61], v[156:159], v[164:167], v[58:61]
	v_mfma_f32_16x16x32_bf16 v[54:57], v[148:151], v[172:175], v[54:57]
	v_mfma_f32_16x16x32_bf16 v[50:53], v[156:159], v[172:175], v[50:53]
	v_mfma_f32_16x16x32_bf16 v[38:41], v[148:151], v[180:183], v[38:41]
	v_mfma_f32_16x16x32_bf16 v[34:37], v[156:159], v[180:183], v[34:37]
	v_mfma_f32_16x16x32_bf16 v[22:25], v[148:151], v[188:191], v[22:25]
	v_mfma_f32_16x16x32_bf16 v[18:21], v[156:159], v[188:191], v[18:21]
	v_mfma_f32_16x16x32_bf16 v[62:65], v[152:155], v[168:171], v[62:65]
	v_mfma_f32_16x16x32_bf16 v[58:61], v[160:163], v[168:171], v[58:61]
	v_mfma_f32_16x16x32_bf16 v[54:57], v[152:155], v[176:179], v[54:57]
	v_mfma_f32_16x16x32_bf16 v[50:53], v[160:163], v[176:179], v[50:53]
	v_mfma_f32_16x16x32_bf16 v[38:41], v[152:155], v[184:187], v[38:41]
	v_mfma_f32_16x16x32_bf16 v[34:37], v[160:163], v[184:187], v[34:37]
	v_mfma_f32_16x16x32_bf16 v[22:25], v[152:155], v[192:195], v[22:25]
	v_mfma_f32_16x16x32_bf16 v[18:21], v[160:163], v[192:195], v[18:21]
	s_setprio 0
	s_barrier
	s_add_u32 s20, s20, 0x30080
	s_addc_u32 s21, s21, 0
	s_add_i32 s22, s22, s39
	s_mov_b32 m0, s22
	s_nop 0
	global_load_lds_dwordx4 v134, s[20:21]
	s_add_i32 m0, s22, 0x2000
	s_nop 0
	global_load_lds_dwordx4 v130, s[20:21]
	s_waitcnt vmcnt(6)
	s_barrier
	s_setprio 1
	v_mfma_f32_16x16x32_bf16 v[46:49], v[196:199], v[164:167], v[46:49]
	v_mfma_f32_16x16x32_bf16 v[42:45], v[204:207], v[164:167], v[42:45]
	v_mfma_f32_16x16x32_bf16 v[30:33], v[196:199], v[172:175], v[30:33]
	v_mfma_f32_16x16x32_bf16 v[26:29], v[204:207], v[172:175], v[26:29]
	v_mfma_f32_16x16x32_bf16 v[14:17], v[196:199], v[180:183], v[14:17]
	v_mfma_f32_16x16x32_bf16 v[10:13], v[204:207], v[180:183], v[10:13]
	v_mfma_f32_16x16x32_bf16 v[6:9], v[196:199], v[188:191], v[6:9]
	v_mfma_f32_16x16x32_bf16 v[2:5], v[204:207], v[188:191], v[2:5]
	v_mfma_f32_16x16x32_bf16 v[46:49], v[200:203], v[168:171], v[46:49]
	v_mfma_f32_16x16x32_bf16 v[42:45], v[208:211], v[168:171], v[42:45]
	v_mfma_f32_16x16x32_bf16 v[30:33], v[200:203], v[176:179], v[30:33]
	v_mfma_f32_16x16x32_bf16 v[26:29], v[208:211], v[176:179], v[26:29]
	v_mfma_f32_16x16x32_bf16 v[14:17], v[200:203], v[184:187], v[14:17]
	v_mfma_f32_16x16x32_bf16 v[10:13], v[208:211], v[184:187], v[10:13]
	v_mfma_f32_16x16x32_bf16 v[6:9], v[200:203], v[192:195], v[6:9]
	v_mfma_f32_16x16x32_bf16 v[2:5], v[208:211], v[192:195], v[2:5]
	s_setprio 0
	s_add_i32 s66, s66, 2
	s_add_u32 s18, s18, 0x100
	s_addc_u32 s19, s19, 0
	s_add_u32 s64, s64, 0x100
	s_addc_u32 s65, s65, 0
	s_cmp_gt_u32 s66, 9
	s_barrier
	s_cbranch_scc1 .Lpeel_1627_after
.LBB0_1627:
	ds_read_b128 v[148:151], v144
	ds_read_b128 v[152:155], v144 offset:1024
	ds_read_b128 v[156:159], v144 offset:2048
	ds_read_b128 v[160:163], v144 offset:3072
	s_add_u32 s20, s18, 0xfffd0080
	s_addc_u32 s21, s19, -1
	s_cmp_eq_u32 s66, 8
	s_cselect_b32 s23, s17, s21
	s_cselect_b32 s22, s16, s20
	s_cselect_b32 s21, s1, s65
	s_cselect_b32 s20, s0, s64
	s_add_i32 m0, s40, 0xc000
	ds_read_b128 v[164:167], v145
	ds_read_b128 v[168:171], v145 offset:1024
	ds_read_b128 v[172:175], v145 offset:2048
	ds_read_b128 v[176:179], v145 offset:3072
	ds_read_b128 v[180:183], v145 offset:4096
	ds_read_b128 v[184:187], v145 offset:5120
	ds_read_b128 v[188:191], v145 offset:6144
	ds_read_b128 v[192:195], v145 offset:7168
	global_load_lds_dwordx4 v138, s[18:19]
	s_add_i32 m0, s40, 0xe000
	s_nop 0
	global_load_lds_dwordx4 v140, s[18:19]
	s_waitcnt lgkmcnt(8)
	s_barrier
	s_waitcnt lgkmcnt(0)
	s_setprio 1
	s_waitcnt lgkmcnt(0)
	v_mfma_f32_16x16x32_bf16 v[126:129], v[148:151], v[164:167], v[126:129]
	v_mfma_f32_16x16x32_bf16 v[122:125], v[156:159], v[164:167], v[122:125]
	v_mfma_f32_16x16x32_bf16 v[118:121], v[148:151], v[172:175], v[118:121]
	v_mfma_f32_16x16x32_bf16 v[114:117], v[156:159], v[172:175], v[114:117]
	v_mfma_f32_16x16x32_bf16 v[102:105], v[148:151], v[180:183], v[102:105]
	v_mfma_f32_16x16x32_bf16 v[98:101], v[156:159], v[180:183], v[98:101]
	v_mfma_f32_16x16x32_bf16 v[86:89], v[148:151], v[188:191], v[86:89]
	v_mfma_f32_16x16x32_bf16 v[82:85], v[156:159], v[188:191], v[82:85]
	v_mfma_f32_16x16x32_bf16 v[126:129], v[152:155], v[168:171], v[126:129]
	v_mfma_f32_16x16x32_bf16 v[122:125], v[160:163], v[168:171], v[122:125]
	v_mfma_f32_16x16x32_bf16 v[118:121], v[152:155], v[176:179], v[118:121]
	v_mfma_f32_16x16x32_bf16 v[114:117], v[160:163], v[176:179], v[114:117]
	v_mfma_f32_16x16x32_bf16 v[102:105], v[152:155], v[184:187], v[102:105]
	v_mfma_f32_16x16x32_bf16 v[98:101], v[160:163], v[184:187], v[98:101]
	v_mfma_f32_16x16x32_bf16 v[86:89], v[152:155], v[192:195], v[86:89]
	v_mfma_f32_16x16x32_bf16 v[82:85], v[160:163], v[192:195], v[82:85]
	s_setprio 0
	s_barrier
	s_add_i32 s67, s52, s39
	v_lshl_add_u64 v[212:213], s[20:21], 0, v[134:135]
	s_mov_b32 m0, s67
	ds_read_b128 v[196:199], v146
	ds_read_b128 v[200:203], v146 offset:1024
	ds_read_b128 v[204:207], v146 offset:2048
	ds_read_b128 v[208:211], v146 offset:3072
	global_load_lds_dwordx4 v[212:213], off
	v_lshl_add_u64 v[214:215], s[20:21], 0, v[130:131]
	s_add_i32 m0, s67, 0x2000
	s_nop 0
	global_load_lds_dwordx4 v[214:215], off
	s_barrier
	s_waitcnt lgkmcnt(0)
	s_setprio 1
	s_waitcnt lgkmcnt(0)
	v_mfma_f32_16x16x32_bf16 v[110:113], v[196:199], v[164:167], v[110:113]
	v_mfma_f32_16x16x32_bf16 v[106:109], v[204:207], v[164:167], v[106:109]
	v_mfma_f32_16x16x32_bf16 v[94:97], v[196:199], v[172:175], v[94:97]
	v_mfma_f32_16x16x32_bf16 v[90:93], v[204:207], v[172:175], v[90:93]
	v_mfma_f32_16x16x32_bf16 v[78:81], v[196:199], v[180:183], v[78:81]
	v_mfma_f32_16x16x32_bf16 v[74:77], v[204:207], v[180:183], v[74:77]
	v_mfma_f32_16x16x32_bf16 v[70:73], v[196:199], v[188:191], v[70:73]
	v_mfma_f32_16x16x32_bf16 v[66:69], v[204:207], v[188:191], v[66:69]
	v_mfma_f32_16x16x32_bf16 v[110:113], v[200:203], v[168:171], v[110:113]
	v_mfma_f32_16x16x32_bf16 v[106:109], v[208:211], v[168:171], v[106:109]
	v_mfma_f32_16x16x32_bf16 v[94:97], v[200:203], v[176:179], v[94:97]
	v_mfma_f32_16x16x32_bf16 v[90:93], v[208:211], v[176:179], v[90:93]
	v_mfma_f32_16x16x32_bf16 v[78:81], v[200:203], v[184:187], v[78:81]
	v_mfma_f32_16x16x32_bf16 v[74:77], v[208:211], v[184:187], v[74:77]
	v_mfma_f32_16x16x32_bf16 v[70:73], v[200:203], v[192:195], v[70:73]
	v_mfma_f32_16x16x32_bf16 v[66:69], v[208:211], v[192:195], v[66:69]
	s_setprio 0
	s_mov_b32 m0, s40
	v_lshl_add_u64 v[216:217], s[22:23], 0, v[136:137]
	s_barrier
	ds_read_b128 v[164:167], v145 offset:16384
	ds_read_b128 v[168:171], v145 offset:17408
	ds_read_b128 v[172:175], v145 offset:18432
	ds_read_b128 v[176:179], v145 offset:19456
	ds_read_b128 v[180:183], v145 offset:20480
	ds_read_b128 v[184:187], v145 offset:21504
	ds_read_b128 v[188:191], v145 offset:22528
	ds_read_b128 v[192:195], v145 offset:23552
	global_load_lds_dwordx4 v[216:217], off
	v_lshl_add_u64 v[218:219], s[22:23], 0, v[132:133]
	s_mov_b32 m0, s41
	s_nop 0
	global_load_lds_dwordx4 v[218:219], off
	s_barrier
	s_waitcnt lgkmcnt(0)
	s_setprio 1
	s_waitcnt lgkmcnt(0)
	v_mfma_f32_16x16x32_bf16 v[62:65], v[148:151], v[164:167], v[62:65]
	v_mfma_f32_16x16x32_bf16 v[58:61], v[156:159], v[164:167], v[58:61]
	v_mfma_f32_16x16x32_bf16 v[54:57], v[148:151], v[172:175], v[54:57]
	v_mfma_f32_16x16x32_bf16 v[50:53], v[156:159], v[172:175], v[50:53]
	v_mfma_f32_16x16x32_bf16 v[38:41], v[148:151], v[180:183], v[38:41]
	v_mfma_f32_16x16x32_bf16 v[34:37], v[156:159], v[180:183], v[34:37]
	v_mfma_f32_16x16x32_bf16 v[22:25], v[148:151], v[188:191], v[22:25]
	v_mfma_f32_16x16x32_bf16 v[18:21], v[156:159], v[188:191], v[18:21]
	v_mfma_f32_16x16x32_bf16 v[62:65], v[152:155], v[168:171], v[62:65]
	v_mfma_f32_16x16x32_bf16 v[58:61], v[160:163], v[168:171], v[58:61]
	v_mfma_f32_16x16x32_bf16 v[54:57], v[152:155], v[176:179], v[54:57]
	v_mfma_f32_16x16x32_bf16 v[50:53], v[160:163], v[176:179], v[50:53]
	v_mfma_f32_16x16x32_bf16 v[38:41], v[152:155], v[184:187], v[38:41]
	v_mfma_f32_16x16x32_bf16 v[34:37], v[160:163], v[184:187], v[34:37]
	v_mfma_f32_16x16x32_bf16 v[22:25], v[152:155], v[192:195], v[22:25]
	v_mfma_f32_16x16x32_bf16 v[18:21], v[160:163], v[192:195], v[18:21]
	s_setprio 0
	s_barrier
	s_add_u32 s68, s20, 0x30000
	s_addc_u32 s69, s21, 0
	s_add_i32 s67, s53, s39
	s_mov_b32 m0, s67
	s_nop 0
	global_load_lds_dwordx4 v134, s[68:69]
	s_add_i32 m0, s67, 0x2000
	s_nop 0
	global_load_lds_dwordx4 v130, s[68:69]
	s_waitcnt vmcnt(6)
	s_barrier
	s_setprio 1
	v_mfma_f32_16x16x32_bf16 v[46:49], v[196:199], v[164:167], v[46:49]
	v_mfma_f32_16x16x32_bf16 v[42:45], v[204:207], v[164:167], v[42:45]
	v_mfma_f32_16x16x32_bf16 v[30:33], v[196:199], v[172:175], v[30:33]
	v_mfma_f32_16x16x32_bf16 v[26:29], v[204:207], v[172:175], v[26:29]
	v_mfma_f32_16x16x32_bf16 v[14:17], v[196:199], v[180:183], v[14:17]
	v_mfma_f32_16x16x32_bf16 v[10:13], v[204:207], v[180:183], v[10:13]
	v_mfma_f32_16x16x32_bf16 v[6:9], v[196:199], v[188:191], v[6:9]
	v_mfma_f32_16x16x32_bf16 v[2:5], v[204:207], v[188:191], v[2:5]
	v_mfma_f32_16x16x32_bf16 v[46:49], v[200:203], v[168:171], v[46:49]
	v_mfma_f32_16x16x32_bf16 v[42:45], v[208:211], v[168:171], v[42:45]
	v_mfma_f32_16x16x32_bf16 v[30:33], v[200:203], v[176:179], v[30:33]
	v_mfma_f32_16x16x32_bf16 v[26:29], v[208:211], v[176:179], v[26:29]
	v_mfma_f32_16x16x32_bf16 v[14:17], v[200:203], v[184:187], v[14:17]
	v_mfma_f32_16x16x32_bf16 v[10:13], v[208:211], v[184:187], v[10:13]
	v_mfma_f32_16x16x32_bf16 v[6:9], v[200:203], v[192:195], v[6:9]
	v_mfma_f32_16x16x32_bf16 v[2:5], v[208:211], v[192:195], v[2:5]
	s_setprio 0
	s_add_i32 s67, 0, 0x18000
	v_add_u32_e32 v147, s67, v1
	s_barrier
	ds_read_b128 v[148:151], v147
	ds_read_b128 v[152:155], v147 offset:1024
	ds_read_b128 v[156:159], v147 offset:2048
	ds_read_b128 v[160:163], v147 offset:3072
	s_add_u32 s22, s22, 0x30000
	s_addc_u32 s23, s23, 0
	s_mov_b32 m0, s42
	ds_read_b128 v[164:167], v145 offset:32768
	ds_read_b128 v[168:171], v145 offset:33792
	ds_read_b128 v[172:175], v145 offset:34816
	ds_read_b128 v[176:179], v145 offset:35840
	ds_read_b128 v[180:183], v145 offset:36864
	ds_read_b128 v[184:187], v145 offset:37888
	ds_read_b128 v[188:191], v145 offset:38912
	ds_read_b128 v[192:195], v145 offset:39936
	global_load_lds_dwordx4 v136, s[22:23]
	s_mov_b32 m0, s43
	s_nop 0
	global_load_lds_dwordx4 v132, s[22:23]
	s_waitcnt lgkmcnt(8)
	s_barrier
	s_waitcnt lgkmcnt(0)
	s_setprio 1
	s_waitcnt lgkmcnt(0)
	v_mfma_f32_16x16x32_bf16 v[126:129], v[148:151], v[164:167], v[126:129]
	v_mfma_f32_16x16x32_bf16 v[122:125], v[156:159], v[164:167], v[122:125]
	v_mfma_f32_16x16x32_bf16 v[118:121], v[148:151], v[172:175], v[118:121]
	v_mfma_f32_16x16x32_bf16 v[114:117], v[156:159], v[172:175], v[114:117]
	v_mfma_f32_16x16x32_bf16 v[102:105], v[148:151], v[180:183], v[102:105]
	v_mfma_f32_16x16x32_bf16 v[98:101], v[156:159], v[180:183], v[98:101]
	v_mfma_f32_16x16x32_bf16 v[86:89], v[148:151], v[188:191], v[86:89]
	v_mfma_f32_16x16x32_bf16 v[82:85], v[156:159], v[188:191], v[82:85]
	v_mfma_f32_16x16x32_bf16 v[126:129], v[152:155], v[168:171], v[126:129]
	v_mfma_f32_16x16x32_bf16 v[122:125], v[160:163], v[168:171], v[122:125]
	v_mfma_f32_16x16x32_bf16 v[118:121], v[152:155], v[176:179], v[118:121]
	v_mfma_f32_16x16x32_bf16 v[114:117], v[160:163], v[176:179], v[114:117]
	v_mfma_f32_16x16x32_bf16 v[102:105], v[152:155], v[184:187], v[102:105]
	v_mfma_f32_16x16x32_bf16 v[98:101], v[160:163], v[184:187], v[98:101]
	v_mfma_f32_16x16x32_bf16 v[86:89], v[152:155], v[192:195], v[86:89]
	v_mfma_f32_16x16x32_bf16 v[82:85], v[160:163], v[192:195], v[82:85]
	s_setprio 0
	s_barrier
	s_add_i32 s22, 0, 0x1c000
	s_add_i32 s23, s67, s39
	v_add_u32_e32 v147, s22, v1
	v_lshl_add_u64 v[212:213], v[212:213], 0, s[6:7]
	s_mov_b32 m0, s23
	ds_read_b128 v[196:199], v147
	ds_read_b128 v[200:203], v147 offset:1024
	ds_read_b128 v[204:207], v147 offset:2048
	ds_read_b128 v[208:211], v147 offset:3072
	global_load_lds_dwordx4 v[212:213], off
	v_lshl_add_u64 v[212:213], v[214:215], 0, s[6:7]
	s_add_i32 m0, s23, 0x2000
	s_nop 0
	global_load_lds_dwordx4 v[212:213], off
	s_barrier
	s_waitcnt lgkmcnt(0)
	s_setprio 1
	s_waitcnt lgkmcnt(0)
	v_mfma_f32_16x16x32_bf16 v[110:113], v[196:199], v[164:167], v[110:113]
	v_mfma_f32_16x16x32_bf16 v[106:109], v[204:207], v[164:167], v[106:109]
	v_mfma_f32_16x16x32_bf16 v[94:97], v[196:199], v[172:175], v[94:97]
	v_mfma_f32_16x16x32_bf16 v[90:93], v[204:207], v[172:175], v[90:93]
	v_mfma_f32_16x16x32_bf16 v[78:81], v[196:199], v[180:183], v[78:81]
	v_mfma_f32_16x16x32_bf16 v[74:77], v[204:207], v[180:183], v[74:77]
	v_mfma_f32_16x16x32_bf16 v[70:73], v[196:199], v[188:191], v[70:73]
	v_mfma_f32_16x16x32_bf16 v[66:69], v[204:207], v[188:191], v[66:69]
	v_mfma_f32_16x16x32_bf16 v[110:113], v[200:203], v[168:171], v[110:113]
	v_mfma_f32_16x16x32_bf16 v[106:109], v[208:211], v[168:171], v[106:109]
	v_mfma_f32_16x16x32_bf16 v[94:97], v[200:203], v[176:179], v[94:97]
	v_mfma_f32_16x16x32_bf16 v[90:93], v[208:211], v[176:179], v[90:93]
	v_mfma_f32_16x16x32_bf16 v[78:81], v[200:203], v[184:187], v[78:81]
	v_mfma_f32_16x16x32_bf16 v[74:77], v[208:211], v[184:187], v[74:77]
	v_mfma_f32_16x16x32_bf16 v[70:73], v[200:203], v[192:195], v[70:73]
	v_mfma_f32_16x16x32_bf16 v[66:69], v[208:211], v[192:195], v[66:69]
	s_setprio 0
	s_mov_b32 m0, s46
	v_lshl_add_u64 v[212:213], v[216:217], 0, s[6:7]
	s_barrier
	ds_read_b128 v[164:167], v145 offset:49152
	ds_read_b128 v[168:171], v145 offset:50176
	ds_read_b128 v[172:175], v145 offset:51200
	ds_read_b128 v[176:179], v145 offset:52224
	ds_read_b128 v[180:183], v145 offset:53248
	ds_read_b128 v[184:187], v145 offset:54272
	ds_read_b128 v[188:191], v145 offset:55296
	ds_read_b128 v[192:195], v145 offset:56320
	global_load_lds_dwordx4 v[212:213], off
	v_lshl_add_u64 v[212:213], v[218:219], 0, s[6:7]
	s_mov_b32 m0, s47
	s_nop 0
	global_load_lds_dwordx4 v[212:213], off
	s_barrier
	s_waitcnt lgkmcnt(0)
	s_setprio 1
	s_waitcnt lgkmcnt(0)
	v_mfma_f32_16x16x32_bf16 v[62:65], v[148:151], v[164:167], v[62:65]
	v_mfma_f32_16x16x32_bf16 v[58:61], v[156:159], v[164:167], v[58:61]
	v_mfma_f32_16x16x32_bf16 v[54:57], v[148:151], v[172:175], v[54:57]
	v_mfma_f32_16x16x32_bf16 v[50:53], v[156:159], v[172:175], v[50:53]
	v_mfma_f32_16x16x32_bf16 v[38:41], v[148:151], v[180:183], v[38:41]
	v_mfma_f32_16x16x32_bf16 v[34:37], v[156:159], v[180:183], v[34:37]
	v_mfma_f32_16x16x32_bf16 v[22:25], v[148:151], v[188:191], v[22:25]
	v_mfma_f32_16x16x32_bf16 v[18:21], v[156:159], v[188:191], v[18:21]
	v_mfma_f32_16x16x32_bf16 v[62:65], v[152:155], v[168:171], v[62:65]
	v_mfma_f32_16x16x32_bf16 v[58:61], v[160:163], v[168:171], v[58:61]
	v_mfma_f32_16x16x32_bf16 v[54:57], v[152:155], v[176:179], v[54:57]
	v_mfma_f32_16x16x32_bf16 v[50:53], v[160:163], v[176:179], v[50:53]
	v_mfma_f32_16x16x32_bf16 v[38:41], v[152:155], v[184:187], v[38:41]
	v_mfma_f32_16x16x32_bf16 v[34:37], v[160:163], v[184:187], v[34:37]
	v_mfma_f32_16x16x32_bf16 v[22:25], v[152:155], v[192:195], v[22:25]
	v_mfma_f32_16x16x32_bf16 v[18:21], v[160:163], v[192:195], v[18:21]
	s_setprio 0
	s_barrier
	s_add_u32 s20, s20, 0x30080
	s_addc_u32 s21, s21, 0
	s_add_i32 s22, s22, s39
	s_mov_b32 m0, s22
	s_nop 0
	global_load_lds_dwordx4 v134, s[20:21]
	s_add_i32 m0, s22, 0x2000
	s_nop 0
	global_load_lds_dwordx4 v130, s[20:21]
	s_waitcnt vmcnt(6)
	s_barrier
	s_setprio 1
	v_mfma_f32_16x16x32_bf16 v[46:49], v[196:199], v[164:167], v[46:49]
	v_mfma_f32_16x16x32_bf16 v[42:45], v[204:207], v[164:167], v[42:45]
	v_mfma_f32_16x16x32_bf16 v[30:33], v[196:199], v[172:175], v[30:33]
	v_mfma_f32_16x16x32_bf16 v[26:29], v[204:207], v[172:175], v[26:29]
	v_mfma_f32_16x16x32_bf16 v[14:17], v[196:199], v[180:183], v[14:17]
	v_mfma_f32_16x16x32_bf16 v[10:13], v[204:207], v[180:183], v[10:13]
	v_mfma_f32_16x16x32_bf16 v[6:9], v[196:199], v[188:191], v[6:9]
	v_mfma_f32_16x16x32_bf16 v[2:5], v[204:207], v[188:191], v[2:5]
	v_mfma_f32_16x16x32_bf16 v[46:49], v[200:203], v[168:171], v[46:49]
	v_mfma_f32_16x16x32_bf16 v[42:45], v[208:211], v[168:171], v[42:45]
	v_mfma_f32_16x16x32_bf16 v[30:33], v[200:203], v[176:179], v[30:33]
	v_mfma_f32_16x16x32_bf16 v[26:29], v[208:211], v[176:179], v[26:29]
	v_mfma_f32_16x16x32_bf16 v[14:17], v[200:203], v[184:187], v[14:17]
	v_mfma_f32_16x16x32_bf16 v[10:13], v[208:211], v[184:187], v[10:13]
	v_mfma_f32_16x16x32_bf16 v[6:9], v[200:203], v[192:195], v[6:9]
	v_mfma_f32_16x16x32_bf16 v[2:5], v[208:211], v[192:195], v[2:5]
	s_setprio 0
	s_add_i32 s66, s66, 2
	s_add_u32 s18, s18, 0x100
	s_addc_u32 s19, s19, 0
	s_add_u32 s64, s64, 0x100
	s_addc_u32 s65, s65, 0
	s_cmp_gt_u32 s66, 9
	s_barrier
	s_cbranch_scc0 .LBB0_1627
